# c9 + removed the back-to-back s_setprio 0 / s_setprio 3 pairs inside MFMA segments
# speedup vs baseline: 1.0139x; 1.0023x over previous
; #define PG8_STAGE(bufoff, gbase, voff) do { _Pragma("unroll") for (int _i = 0; _i < 2; ++_i) \
;         __builtin_amdgcn_global_load_lds((const unsigned*)((const char*)(gbase) + (voff)[_i]), (PG8_LAS unsigned*)(lds + (bufoff) + ldsw + _i * 8192), 16, 0, 0); } while (0)
; #define PG8_LDA(dst, b, h) do { _Pragma("unroll") for (int m = 0; m < 4; ++m) Frag<F8>::load(dst[m], lds + PG8_SA(b, h) + aoff + m * 2048); } while (0)
; #define PG8_LDB(dst, b, h) do { _Pragma("unroll") for (int n = 0; n < 2; ++n) Frag<F8>::load(dst[n], lds + PG8_SB(b, h) + boff + n * 2048); } while (0)
; #define PG8_WAIT_V(n) asm volatile("s_waitcnt vmcnt(" #n ")" ::: "memory")
; #define PG8_WAIT_L(n) asm volatile("s_waitcnt lgkmcnt(" #n ")" ::: "memory")
; template <class Epi, class Sched, bool ALIGN_EPI = false, bool SP2 = false, bool F8 = false>
; __device__ __forceinline__ void gemm_phase(PG8_LAS unsigned char* lds, const Gemm g, const Sched& S, const Epi& E) {
;     ...
;         const bool has_next = S.next(ui + 1, nxt);
;         const char* nA = has_next ? (const char*)g.A + (size_t)nxt.pm * tstep + nxt.ko : cA; const char* nB = has_next ? (const char*)g.Bt + (size_t)nxt.pn * tstep + nxt.ko : cB;
;         for (int t = 0; t < nt; t += 2) {
;             const bool last = (t == nt - 2);
;             const char* a1 = cA + (size_t)(t + 1) * kstep;
;             const char* a2 = last ? nA : cA + (size_t)(t + 2) * kstep; const char* b2 = last ? nB : cB + (size_t)(t + 2) * kstep;
;             const char* a3 = a2 + kstep; const char* b3 = b2 + kstep;
;             if (last && has_next) S.a_ready(nxt);
;             if constexpr (SP2) {
;             PG8_LDB(B0, 0, 0); PG8_LDB(B1, 0, 1); PG8_SCHED; PG8_LDA(At, 0, 0); PG8_STAGE(PG8_SA(1, 1), a1 + hstep, voffA);
;             PG8_WAIT_V(8); PG8_WAIT_L(0); PG8_BAR; PG8_MMA(0, 0, At, B0); PG8_MMA(0, 1, At, B1); PG8_BAR; PG8_SCHED;
;             PG8_LDA(At, 0, 1); PG8_STAGE(PG8_SB(0, 0), b2, voffB); PG8_STAGE(PG8_SB(0, 1), b2 + hstep, voffB); PG8_STAGE(PG8_SA(0, 0), a2, voffA);
;             PG8_WAIT_V(8); PG8_WAIT_L(0); PG8_BAR; PG8_MMA(1, 0, At, B0); PG8_MMA(1, 1, At, B1); PG8_BAR; PG8_SCHED;
;             PG8_LDB(B0, 1, 0); PG8_LDB(B1, 1, 1); PG8_SCHED; PG8_LDA(At, 1, 0); PG8_STAGE(PG8_SA(0, 1), a2 + hstep, voffA);
;             PG8_WAIT_V(8); PG8_WAIT_L(0); PG8_BAR; PG8_MMA(0, 0, At, B0); PG8_MMA(0, 1, At, B1); PG8_BAR; PG8_SCHED;
.LBB0_150:
	s_ashr_i32 s25, s24, 31
	s_lshl_b64 s[4:5], s[24:25], 18
	s_add_u32 s38, s77, s4
	s_addc_u32 s39, s78, s5
	s_and_b64 s[4:5], s[8:9], exec
	s_cselect_b32 s25, s39, s71
	s_cselect_b32 s91, s38, s70
	s_ashr_i32 s31, s30, 31
	s_lshl_b64 s[4:5], s[30:31], 18
	s_add_u32 s42, s79, s4
	s_addc_u32 s43, s80, s5
	s_and_b64 s[4:5], s[8:9], exec
	s_cselect_b32 s31, s43, s73
	s_cselect_b32 s92, s42, s72
	s_add_u32 s70, s70, 0x20080
	s_addc_u32 s71, s71, 0
	s_add_u32 s93, s72, 0x100
	s_addc_u32 s95, s73, 0
	s_mov_b32 s96, -2
	ds_read_b128 v[18:21], v194
	ds_read_b128 v[22:25], v194 offset:1024
	ds_read_b128 v[26:29], v194 offset:2048
	ds_read_b128 v[30:33], v194 offset:3072
	ds_read_b128 v[2:5], v195
	ds_read_b128 v[6:9], v195 offset:1024
	ds_read_b128 v[10:13], v195 offset:2048
	ds_read_b128 v[14:17], v195 offset:3072
	s_add_u32 s0, s70, 0xfffe0080
	s_addc_u32 s1, s71, -1
	s_cmp_eq_u32 s96, 4
	s_cselect_b32 s75, s25, s1
	s_cselect_b32 s74, s91, s0
	s_cselect_b32 s73, s31, s95
	s_cselect_b32 s72, s92, s93
	v_lshl_add_u64 v[224:225], s[70:71], 0, v[174:175]
	s_add_i32 m0, s45, 0xc000
	ds_read_b128 v[182:185], v196
	ds_read_b128 v[186:189], v196 offset:1024
	ds_read_b128 v[200:203], v196 offset:2048
	ds_read_b128 v[204:207], v196 offset:3072
	ds_read_b128 v[208:211], v196 offset:4096
	ds_read_b128 v[212:215], v196 offset:5120
	ds_read_b128 v[216:219], v196 offset:6144
	ds_read_b128 v[220:223], v196 offset:7168
	global_load_lds_dwordx4 v[224:225], off
	v_lshl_add_u64 v[224:225], s[70:71], 0, v[176:177]
	s_add_i32 m0, s45, 0xe000
	s_nop 0
	global_load_lds_dwordx4 v[224:225], off
	s_waitcnt vmcnt(8)
	s_waitcnt lgkmcnt(0)
	s_barrier
	s_setprio 3
	s_waitcnt lgkmcnt(0)
	v_mfma_f32_16x16x128_f8f6f4 v[158:161], v[18:25], v[182:189], 0
	v_mfma_f32_16x16x128_f8f6f4 v[154:157], v[26:33], v[182:189], 0
	v_mfma_f32_16x16x128_f8f6f4 v[150:153], v[18:25], v[200:207], 0
	v_mfma_f32_16x16x128_f8f6f4 v[142:145], v[26:33], v[200:207], 0
	v_mfma_f32_16x16x128_f8f6f4 v[130:133], v[18:25], v[208:215], 0
	v_mfma_f32_16x16x128_f8f6f4 v[122:125], v[26:33], v[208:215], 0
	v_mfma_f32_16x16x128_f8f6f4 v[118:121], v[18:25], v[216:223], 0
	v_mfma_f32_16x16x128_f8f6f4 v[110:113], v[26:33], v[216:223], 0
	v_mfma_f32_16x16x128_f8f6f4 v[146:149], v[2:9], v[182:189], 0
	v_mfma_f32_16x16x128_f8f6f4 v[138:141], v[10:17], v[182:189], 0
	v_mfma_f32_16x16x128_f8f6f4 v[134:137], v[2:9], v[200:207], 0
	v_mfma_f32_16x16x128_f8f6f4 v[126:129], v[10:17], v[200:207], 0
	v_mfma_f32_16x16x128_f8f6f4 v[114:117], v[2:9], v[208:215], 0
	v_mfma_f32_16x16x128_f8f6f4 v[106:109], v[10:17], v[208:215], 0
	v_mfma_f32_16x16x128_f8f6f4 v[102:105], v[2:9], v[216:223], 0
	v_mfma_f32_16x16x128_f8f6f4 v[98:101], v[10:17], v[216:223], 0
	s_setprio 0
	s_barrier
	s_add_i32 s0, s87, s76
	v_lshl_add_u64 v[182:183], s[72:73], 0, v[170:171]
	s_mov_b32 m0, s0
	ds_read_b128 v[200:203], v196 offset:16384
	ds_read_b128 v[204:207], v196 offset:17408
	ds_read_b128 v[208:211], v196 offset:18432
	ds_read_b128 v[212:215], v196 offset:19456
	ds_read_b128 v[216:219], v196 offset:20480
	ds_read_b128 v[220:223], v196 offset:21504
	ds_read_b128 v[224:227], v196 offset:22528
	ds_read_b128 v[228:231], v196 offset:23552
	global_load_lds_dwordx4 v[182:183], off
	s_add_i32 m0, s0, 0x2000
	s_add_u32 s4, s72, 0x20000
	v_lshl_add_u64 v[184:185], s[72:73], 0, v[166:167]
	s_addc_u32 s5, s73, 0
	s_add_i32 s0, s88, s76
	global_load_lds_dwordx4 v[184:185], off
	v_lshl_add_u64 v[186:187], s[4:5], 0, v[170:171]
	s_mov_b32 m0, s0
	v_lshl_add_u64 v[188:189], s[74:75], 0, v[168:169]
	global_load_lds_dwordx4 v[186:187], off
	v_lshl_add_u64 v[186:187], s[4:5], 0, v[166:167]
	s_add_i32 m0, s0, 0x2000
	s_nop 0
	global_load_lds_dwordx4 v[186:187], off
	v_lshl_add_u64 v[186:187], s[74:75], 0, v[172:173]
	s_mov_b32 m0, s45
	s_nop 0
	global_load_lds_dwordx4 v[186:187], off
	s_mov_b32 m0, s82
	s_nop 0
	global_load_lds_dwordx4 v[188:189], off
	s_waitcnt vmcnt(8)
	s_waitcnt lgkmcnt(0)
	s_barrier
	s_setprio 3
	s_waitcnt lgkmcnt(0)
	v_mfma_f32_16x16x128_f8f6f4 v[94:97], v[18:25], v[200:207], 0
	v_mfma_f32_16x16x128_f8f6f4 v[90:93], v[26:33], v[200:207], 0
	v_mfma_f32_16x16x128_f8f6f4 v[86:89], v[18:25], v[208:215], 0
	v_mfma_f32_16x16x128_f8f6f4 v[82:85], v[26:33], v[208:215], 0
	v_mfma_f32_16x16x128_f8f6f4 v[70:73], v[18:25], v[216:223], 0
	v_mfma_f32_16x16x128_f8f6f4 v[66:69], v[26:33], v[216:223], 0
	v_mfma_f32_16x16x128_f8f6f4 v[54:57], v[18:25], v[224:231], 0
	v_mfma_f32_16x16x128_f8f6f4 v[50:53], v[26:33], v[224:231], 0
	v_mfma_f32_16x16x128_f8f6f4 v[78:81], v[2:9], v[200:207], 0
	v_mfma_f32_16x16x128_f8f6f4 v[74:77], v[10:17], v[200:207], 0
	v_mfma_f32_16x16x128_f8f6f4 v[62:65], v[2:9], v[208:215], 0
	v_mfma_f32_16x16x128_f8f6f4 v[58:61], v[10:17], v[208:215], 0
	v_mfma_f32_16x16x128_f8f6f4 v[46:49], v[2:9], v[216:223], 0
	v_mfma_f32_16x16x128_f8f6f4 v[42:45], v[10:17], v[216:223], 0
	v_mfma_f32_16x16x128_f8f6f4 v[38:41], v[2:9], v[224:231], 0
	v_mfma_f32_16x16x128_f8f6f4 v[34:37], v[10:17], v[224:231], 0
	s_setprio 0
	s_barrier
	s_add_i32 s0, 0, 0x18000
	s_add_i32 s1, 0, 0x1c000
	v_add_u32_e32 v14, s0, v190
	v_add_u32_e32 v30, s1, v190
	ds_read_b128 v[2:5], v14
	ds_read_b128 v[6:9], v14 offset:1024
	ds_read_b128 v[10:13], v14 offset:2048
	ds_read_b128 v[14:17], v14 offset:3072
	ds_read_b128 v[18:21], v30
	ds_read_b128 v[22:25], v30 offset:1024
	ds_read_b128 v[26:29], v30 offset:2048
	ds_read_b128 v[30:33], v30 offset:3072
	s_add_u32 s4, s74, 0x20000
	s_addc_u32 s5, s75, 0
	s_mov_b32 m0, s83
	v_lshl_add_u64 v[232:233], s[4:5], 0, v[172:173]
	ds_read_b128 v[200:203], v196 offset:32768
	ds_read_b128 v[204:207], v196 offset:33792
	ds_read_b128 v[208:211], v196 offset:34816
	ds_read_b128 v[212:215], v196 offset:35840
	ds_read_b128 v[216:219], v196 offset:36864
	ds_read_b128 v[220:223], v196 offset:37888
	ds_read_b128 v[224:227], v196 offset:38912
	ds_read_b128 v[228:231], v196 offset:39936
	global_load_lds_dwordx4 v[232:233], off
	v_lshl_add_u64 v[232:233], s[4:5], 0, v[168:169]
	s_mov_b32 m0, s84
	s_nop 0
	global_load_lds_dwordx4 v[232:233], off
	s_waitcnt vmcnt(8)
	s_waitcnt lgkmcnt(0)
	s_barrier
; #define PG8_STAGE(bufoff, gbase, voff) do { _Pragma("unroll") for (int _i = 0; _i < 2; ++_i) \
;         __builtin_amdgcn_global_load_lds((const unsigned*)((const char*)(gbase) + (voff)[_i]), (PG8_LAS unsigned*)(lds + (bufoff) + ldsw + _i * 8192), 16, 0, 0); } while (0)
; #define PG8_LDA(dst, b, h) do { _Pragma("unroll") for (int m = 0; m < 4; ++m) Frag<F8>::load(dst[m], lds + PG8_SA(b, h) + aoff + m * 2048); } while (0)
; #define PG8_LDB(dst, b, h) do { _Pragma("unroll") for (int n = 0; n < 2; ++n) Frag<F8>::load(dst[n], lds + PG8_SB(b, h) + boff + n * 2048); } while (0)
; #define PG8_MMA(ai, bj, At, Bt) do { __builtin_amdgcn_s_setprio(3); _Pragma("unroll") for (int m = 0; m < 4; ++m) _Pragma("unroll") for (int n = 0; n < 2; ++n) Frag<F8>::mma(acc[ai][bj][m][n], Bt[n], At[m]); \
;         __builtin_amdgcn_s_setprio(0); } while (0)
; #define PG8_WAIT_V(n) asm volatile("s_waitcnt vmcnt(" #n ")" ::: "memory")
; #define PG8_WAIT_L(n) asm volatile("s_waitcnt lgkmcnt(" #n ")" ::: "memory")
; #define PG8_BAR __builtin_amdgcn_s_barrier()
; #define PG8_SCHED __builtin_amdgcn_sched_barrier(0)
; template <class Epi, class Sched, bool ALIGN_EPI = false, bool SP2 = false, bool F8 = false>
; __device__ __forceinline__ void gemm_phase(PG8_LAS unsigned char* lds, const Gemm g, const Sched& S, const Epi& E) {
;     ...
;             PG8_LDB(B0, 0, 0); PG8_LDB(B1, 0, 1); PG8_SCHED; PG8_LDA(At, 0, 0); PG8_STAGE(PG8_SA(1, 1), a1 + hstep, voffA);
;             PG8_WAIT_V(8); PG8_WAIT_L(0); PG8_BAR; PG8_MMA(0, 0, At, B0); PG8_MMA(0, 1, At, B1); PG8_BAR; PG8_SCHED;
;             PG8_LDA(At, 0, 1); PG8_STAGE(PG8_SB(0, 0), b2, voffB); PG8_STAGE(PG8_SB(0, 1), b2 + hstep, voffB); PG8_STAGE(PG8_SA(0, 0), a2, voffA);
;             PG8_WAIT_V(8); PG8_WAIT_L(0); PG8_BAR; PG8_MMA(1, 0, At, B0); PG8_MMA(1, 1, At, B1); PG8_BAR; PG8_SCHED;
;             PG8_LDB(B0, 1, 0); PG8_LDB(B1, 1, 1); PG8_SCHED; PG8_LDA(At, 1, 0); PG8_STAGE(PG8_SA(0, 1), a2 + hstep, voffA);
;             PG8_WAIT_V(8); PG8_WAIT_L(0); PG8_BAR; PG8_MMA(0, 0, At, B0); PG8_MMA(0, 1, At, B1); PG8_BAR; PG8_SCHED;
;             PG8_LDA(At, 1, 1); PG8_STAGE(PG8_SB(1, 0), b3, voffB); PG8_STAGE(PG8_SB(1, 1), b3 + hstep, voffB); PG8_STAGE(PG8_SA(1, 0), a3, voffA);
;             PG8_WAIT_V(8); PG8_WAIT_L(0); PG8_BAR; PG8_MMA(1, 0, At, B0); PG8_MMA(1, 1, At, B1); PG8_BAR; PG8_SCHED;
	s_setprio 3
	s_waitcnt lgkmcnt(0)
	v_mfma_f32_16x16x128_f8f6f4 v[158:161], v[2:9], v[200:207], v[158:161]
	v_mfma_f32_16x16x128_f8f6f4 v[154:157], v[10:17], v[200:207], v[154:157]
	v_mfma_f32_16x16x128_f8f6f4 v[150:153], v[2:9], v[208:215], v[150:153]
	v_mfma_f32_16x16x128_f8f6f4 v[142:145], v[10:17], v[208:215], v[142:145]
	v_mfma_f32_16x16x128_f8f6f4 v[130:133], v[2:9], v[216:223], v[130:133]
	v_mfma_f32_16x16x128_f8f6f4 v[122:125], v[10:17], v[216:223], v[122:125]
	v_mfma_f32_16x16x128_f8f6f4 v[118:121], v[2:9], v[224:231], v[118:121]
	v_mfma_f32_16x16x128_f8f6f4 v[110:113], v[10:17], v[224:231], v[110:113]
	v_mfma_f32_16x16x128_f8f6f4 v[146:149], v[18:25], v[200:207], v[146:149]
	v_mfma_f32_16x16x128_f8f6f4 v[138:141], v[26:33], v[200:207], v[138:141]
	v_mfma_f32_16x16x128_f8f6f4 v[134:137], v[18:25], v[208:215], v[134:137]
	v_mfma_f32_16x16x128_f8f6f4 v[126:129], v[26:33], v[208:215], v[126:129]
	v_mfma_f32_16x16x128_f8f6f4 v[114:117], v[18:25], v[216:223], v[114:117]
	v_mfma_f32_16x16x128_f8f6f4 v[106:109], v[26:33], v[216:223], v[106:109]
	v_mfma_f32_16x16x128_f8f6f4 v[102:105], v[18:25], v[224:231], v[102:105]
	v_mfma_f32_16x16x128_f8f6f4 v[98:101], v[26:33], v[224:231], v[98:101]
	s_setprio 0
	s_barrier
	s_add_i32 s0, s0, s76
	v_lshl_add_u64 v[182:183], v[182:183], 0, s[18:19]
	s_mov_b32 m0, s0
	ds_read_b128 v[200:203], v196 offset:49152
	ds_read_b128 v[204:207], v196 offset:50176
	ds_read_b128 v[208:211], v196 offset:51200
	ds_read_b128 v[212:215], v196 offset:52224
	ds_read_b128 v[216:219], v196 offset:53248
	ds_read_b128 v[220:223], v196 offset:54272
	ds_read_b128 v[224:227], v196 offset:55296
	ds_read_b128 v[228:231], v196 offset:56320
	global_load_lds_dwordx4 v[182:183], off
	s_add_i32 m0, s0, 0x2000
	s_add_u32 s4, s72, 0x20080
	v_lshl_add_u64 v[182:183], v[184:185], 0, s[18:19]
	s_addc_u32 s5, s73, 0
	s_add_i32 s0, s1, s76
	global_load_lds_dwordx4 v[182:183], off
	v_lshl_add_u64 v[182:183], s[4:5], 0, v[170:171]
	s_mov_b32 m0, s0
	s_nop 0
	global_load_lds_dwordx4 v[182:183], off
	v_lshl_add_u64 v[182:183], s[4:5], 0, v[166:167]
	s_add_i32 m0, s0, 0x2000
	s_nop 0
	global_load_lds_dwordx4 v[182:183], off
	v_lshl_add_u64 v[182:183], v[186:187], 0, s[18:19]
	s_mov_b32 m0, s85
	s_nop 0
	global_load_lds_dwordx4 v[182:183], off
	v_lshl_add_u64 v[182:183], v[188:189], 0, s[18:19]
	s_mov_b32 m0, s86
	s_nop 0
	global_load_lds_dwordx4 v[182:183], off
	s_waitcnt vmcnt(8)
	s_waitcnt lgkmcnt(0)
	s_barrier
	s_setprio 3
	s_waitcnt lgkmcnt(0)
	v_mfma_f32_16x16x128_f8f6f4 v[94:97], v[2:9], v[200:207], v[94:97]
	v_mfma_f32_16x16x128_f8f6f4 v[90:93], v[10:17], v[200:207], v[90:93]
	v_mfma_f32_16x16x128_f8f6f4 v[86:89], v[2:9], v[208:215], v[86:89]
	v_mfma_f32_16x16x128_f8f6f4 v[82:85], v[10:17], v[208:215], v[82:85]
	v_mfma_f32_16x16x128_f8f6f4 v[70:73], v[2:9], v[216:223], v[70:73]
	v_mfma_f32_16x16x128_f8f6f4 v[66:69], v[10:17], v[216:223], v[66:69]
	v_mfma_f32_16x16x128_f8f6f4 v[54:57], v[2:9], v[224:231], v[54:57]
	v_mfma_f32_16x16x128_f8f6f4 v[50:53], v[10:17], v[224:231], v[50:53]
	v_mfma_f32_16x16x128_f8f6f4 v[78:81], v[18:25], v[200:207], v[78:81]
	v_mfma_f32_16x16x128_f8f6f4 v[74:77], v[26:33], v[200:207], v[74:77]
	v_mfma_f32_16x16x128_f8f6f4 v[62:65], v[18:25], v[208:215], v[62:65]
	v_mfma_f32_16x16x128_f8f6f4 v[58:61], v[26:33], v[208:215], v[58:61]
	v_mfma_f32_16x16x128_f8f6f4 v[46:49], v[18:25], v[216:223], v[46:49]
	v_mfma_f32_16x16x128_f8f6f4 v[42:45], v[26:33], v[216:223], v[42:45]
	v_mfma_f32_16x16x128_f8f6f4 v[38:41], v[18:25], v[224:231], v[38:41]
	v_mfma_f32_16x16x128_f8f6f4 v[34:37], v[26:33], v[224:231], v[34:37]
	s_setprio 0
	s_barrier
	s_add_i32 s96, s96, 2
	s_add_u32 s70, s70, 0x100
	s_addc_u32 s71, s71, 0
	s_add_u32 s93, s93, 0x100
	s_addc_u32 s95, s95, 0
	s_cmp_gt_u32 s96, 5
	s_cbranch_scc1 .Lpeel_exit_0
.LBB0_151:
	ds_read_b128 v[18:21], v194
	ds_read_b128 v[22:25], v194 offset:1024
	ds_read_b128 v[26:29], v194 offset:2048
	ds_read_b128 v[30:33], v194 offset:3072
	ds_read_b128 v[2:5], v195
	ds_read_b128 v[6:9], v195 offset:1024
	ds_read_b128 v[10:13], v195 offset:2048
	ds_read_b128 v[14:17], v195 offset:3072
	s_add_u32 s0, s70, 0xfffe0080
	s_addc_u32 s1, s71, -1
	s_cmp_eq_u32 s96, 4
	s_cselect_b32 s75, s25, s1
	s_cselect_b32 s74, s91, s0
	s_cselect_b32 s73, s31, s95
	s_cselect_b32 s72, s92, s93
	v_lshl_add_u64 v[224:225], s[70:71], 0, v[174:175]
	s_add_i32 m0, s45, 0xc000
	ds_read_b128 v[182:185], v196
	ds_read_b128 v[186:189], v196 offset:1024
	ds_read_b128 v[200:203], v196 offset:2048
	ds_read_b128 v[204:207], v196 offset:3072
	ds_read_b128 v[208:211], v196 offset:4096
	ds_read_b128 v[212:215], v196 offset:5120
	ds_read_b128 v[216:219], v196 offset:6144
	ds_read_b128 v[220:223], v196 offset:7168
	global_load_lds_dwordx4 v[224:225], off
	v_lshl_add_u64 v[224:225], s[70:71], 0, v[176:177]
	s_add_i32 m0, s45, 0xe000
	s_nop 0
	global_load_lds_dwordx4 v[224:225], off
	s_waitcnt vmcnt(8)
	s_waitcnt lgkmcnt(0)
	s_barrier
	s_setprio 3
	s_waitcnt lgkmcnt(0)
	v_mfma_f32_16x16x128_f8f6f4 v[158:161], v[18:25], v[182:189], v[158:161]
	v_mfma_f32_16x16x128_f8f6f4 v[154:157], v[26:33], v[182:189], v[154:157]
	v_mfma_f32_16x16x128_f8f6f4 v[150:153], v[18:25], v[200:207], v[150:153]
	v_mfma_f32_16x16x128_f8f6f4 v[142:145], v[26:33], v[200:207], v[142:145]
	v_mfma_f32_16x16x128_f8f6f4 v[130:133], v[18:25], v[208:215], v[130:133]
	v_mfma_f32_16x16x128_f8f6f4 v[122:125], v[26:33], v[208:215], v[122:125]
	v_mfma_f32_16x16x128_f8f6f4 v[118:121], v[18:25], v[216:223], v[118:121]
	v_mfma_f32_16x16x128_f8f6f4 v[110:113], v[26:33], v[216:223], v[110:113]
	v_mfma_f32_16x16x128_f8f6f4 v[146:149], v[2:9], v[182:189], v[146:149]
	v_mfma_f32_16x16x128_f8f6f4 v[138:141], v[10:17], v[182:189], v[138:141]
	v_mfma_f32_16x16x128_f8f6f4 v[134:137], v[2:9], v[200:207], v[134:137]
	v_mfma_f32_16x16x128_f8f6f4 v[126:129], v[10:17], v[200:207], v[126:129]
	v_mfma_f32_16x16x128_f8f6f4 v[114:117], v[2:9], v[208:215], v[114:117]
	v_mfma_f32_16x16x128_f8f6f4 v[106:109], v[10:17], v[208:215], v[106:109]
	v_mfma_f32_16x16x128_f8f6f4 v[102:105], v[2:9], v[216:223], v[102:105]
	v_mfma_f32_16x16x128_f8f6f4 v[98:101], v[10:17], v[216:223], v[98:101]
	s_setprio 0
	s_barrier
; #define PG8_STAGE(bufoff, gbase, voff) do { _Pragma("unroll") for (int _i = 0; _i < 2; ++_i) \
;         __builtin_amdgcn_global_load_lds((const unsigned*)((const char*)(gbase) + (voff)[_i]), (PG8_LAS unsigned*)(lds + (bufoff) + ldsw + _i * 8192), 16, 0, 0); } while (0)
; #define PG8_LDA(dst, b, h) do { _Pragma("unroll") for (int m = 0; m < 4; ++m) Frag<F8>::load(dst[m], lds + PG8_SA(b, h) + aoff + m * 2048); } while (0)
; #define PG8_LDB(dst, b, h) do { _Pragma("unroll") for (int n = 0; n < 2; ++n) Frag<F8>::load(dst[n], lds + PG8_SB(b, h) + boff + n * 2048); } while (0)
; #define PG8_MMA(ai, bj, At, Bt) do { __builtin_amdgcn_s_setprio(3); _Pragma("unroll") for (int m = 0; m < 4; ++m) _Pragma("unroll") for (int n = 0; n < 2; ++n) Frag<F8>::mma(acc[ai][bj][m][n], Bt[n], At[m]); \
;         __builtin_amdgcn_s_setprio(0); } while (0)
; #define PG8_WAIT_V(n) asm volatile("s_waitcnt vmcnt(" #n ")" ::: "memory")
; #define PG8_WAIT_L(n) asm volatile("s_waitcnt lgkmcnt(" #n ")" ::: "memory")
; #define PG8_BAR __builtin_amdgcn_s_barrier()
; #define PG8_SCHED __builtin_amdgcn_sched_barrier(0)
; template <class Epi, class Sched, bool ALIGN_EPI = false, bool SP2 = false, bool F8 = false>
; __device__ __forceinline__ void gemm_phase(PG8_LAS unsigned char* lds, const Gemm g, const Sched& S, const Epi& E) {
;     ...
;             PG8_LDA(At, 0, 1); PG8_STAGE(PG8_SB(0, 0), b2, voffB); PG8_STAGE(PG8_SB(0, 1), b2 + hstep, voffB); PG8_STAGE(PG8_SA(0, 0), a2, voffA);
;             PG8_WAIT_V(8); PG8_WAIT_L(0); PG8_BAR; PG8_MMA(1, 0, At, B0); PG8_MMA(1, 1, At, B1); PG8_BAR; PG8_SCHED;
;             PG8_LDB(B0, 1, 0); PG8_LDB(B1, 1, 1); PG8_SCHED; PG8_LDA(At, 1, 0); PG8_STAGE(PG8_SA(0, 1), a2 + hstep, voffA);
;             PG8_WAIT_V(8); PG8_WAIT_L(0); PG8_BAR; PG8_MMA(0, 0, At, B0); PG8_MMA(0, 1, At, B1); PG8_BAR; PG8_SCHED;
	s_add_i32 s0, s87, s76
	v_lshl_add_u64 v[182:183], s[72:73], 0, v[170:171]
	s_mov_b32 m0, s0
	ds_read_b128 v[200:203], v196 offset:16384
	ds_read_b128 v[204:207], v196 offset:17408
	ds_read_b128 v[208:211], v196 offset:18432
	ds_read_b128 v[212:215], v196 offset:19456
	ds_read_b128 v[216:219], v196 offset:20480
	ds_read_b128 v[220:223], v196 offset:21504
	ds_read_b128 v[224:227], v196 offset:22528
	ds_read_b128 v[228:231], v196 offset:23552
	global_load_lds_dwordx4 v[182:183], off
	s_add_i32 m0, s0, 0x2000
	s_add_u32 s4, s72, 0x20000
	v_lshl_add_u64 v[184:185], s[72:73], 0, v[166:167]
	s_addc_u32 s5, s73, 0
	s_add_i32 s0, s88, s76
	global_load_lds_dwordx4 v[184:185], off
	v_lshl_add_u64 v[186:187], s[4:5], 0, v[170:171]
	s_mov_b32 m0, s0
	v_lshl_add_u64 v[188:189], s[74:75], 0, v[168:169]
	global_load_lds_dwordx4 v[186:187], off
	v_lshl_add_u64 v[186:187], s[4:5], 0, v[166:167]
	s_add_i32 m0, s0, 0x2000
	s_nop 0
	global_load_lds_dwordx4 v[186:187], off
	v_lshl_add_u64 v[186:187], s[74:75], 0, v[172:173]
	s_mov_b32 m0, s45
	s_nop 0
	global_load_lds_dwordx4 v[186:187], off
	s_mov_b32 m0, s82
	s_nop 0
	global_load_lds_dwordx4 v[188:189], off
	s_waitcnt vmcnt(8)
	s_waitcnt lgkmcnt(0)
	s_barrier
	s_setprio 3
	s_waitcnt lgkmcnt(0)
	v_mfma_f32_16x16x128_f8f6f4 v[94:97], v[18:25], v[200:207], v[94:97]
	v_mfma_f32_16x16x128_f8f6f4 v[90:93], v[26:33], v[200:207], v[90:93]
	v_mfma_f32_16x16x128_f8f6f4 v[86:89], v[18:25], v[208:215], v[86:89]
	v_mfma_f32_16x16x128_f8f6f4 v[82:85], v[26:33], v[208:215], v[82:85]
	v_mfma_f32_16x16x128_f8f6f4 v[70:73], v[18:25], v[216:223], v[70:73]
	v_mfma_f32_16x16x128_f8f6f4 v[66:69], v[26:33], v[216:223], v[66:69]
	v_mfma_f32_16x16x128_f8f6f4 v[54:57], v[18:25], v[224:231], v[54:57]
	v_mfma_f32_16x16x128_f8f6f4 v[50:53], v[26:33], v[224:231], v[50:53]
	v_mfma_f32_16x16x128_f8f6f4 v[78:81], v[2:9], v[200:207], v[78:81]
	v_mfma_f32_16x16x128_f8f6f4 v[74:77], v[10:17], v[200:207], v[74:77]
	v_mfma_f32_16x16x128_f8f6f4 v[62:65], v[2:9], v[208:215], v[62:65]
	v_mfma_f32_16x16x128_f8f6f4 v[58:61], v[10:17], v[208:215], v[58:61]
	v_mfma_f32_16x16x128_f8f6f4 v[46:49], v[2:9], v[216:223], v[46:49]
	v_mfma_f32_16x16x128_f8f6f4 v[42:45], v[10:17], v[216:223], v[42:45]
	v_mfma_f32_16x16x128_f8f6f4 v[38:41], v[2:9], v[224:231], v[38:41]
	v_mfma_f32_16x16x128_f8f6f4 v[34:37], v[10:17], v[224:231], v[34:37]
	s_setprio 0
	s_barrier
	s_add_i32 s0, 0, 0x18000
	s_add_i32 s1, 0, 0x1c000
	v_add_u32_e32 v14, s0, v190
	v_add_u32_e32 v30, s1, v190
	ds_read_b128 v[2:5], v14
	ds_read_b128 v[6:9], v14 offset:1024
	ds_read_b128 v[10:13], v14 offset:2048
	ds_read_b128 v[14:17], v14 offset:3072
	ds_read_b128 v[18:21], v30
	ds_read_b128 v[22:25], v30 offset:1024
	ds_read_b128 v[26:29], v30 offset:2048
	ds_read_b128 v[30:33], v30 offset:3072
	s_add_u32 s4, s74, 0x20000
	s_addc_u32 s5, s75, 0
	s_mov_b32 m0, s83
	v_lshl_add_u64 v[232:233], s[4:5], 0, v[172:173]
	ds_read_b128 v[200:203], v196 offset:32768
	ds_read_b128 v[204:207], v196 offset:33792
	ds_read_b128 v[208:211], v196 offset:34816
	ds_read_b128 v[212:215], v196 offset:35840
	ds_read_b128 v[216:219], v196 offset:36864
	ds_read_b128 v[220:223], v196 offset:37888
	ds_read_b128 v[224:227], v196 offset:38912
	ds_read_b128 v[228:231], v196 offset:39936
	global_load_lds_dwordx4 v[232:233], off
	v_lshl_add_u64 v[232:233], s[4:5], 0, v[168:169]
	s_mov_b32 m0, s84
	s_nop 0
	global_load_lds_dwordx4 v[232:233], off
	s_waitcnt vmcnt(8)
	s_waitcnt lgkmcnt(0)
	s_barrier
; #define PG8_STAGE(bufoff, gbase, voff) do { _Pragma("unroll") for (int _i = 0; _i < 2; ++_i) \
;         __builtin_amdgcn_global_load_lds((const unsigned*)((const char*)(gbase) + (voff)[_i]), (PG8_LAS unsigned*)(lds + (bufoff) + ldsw + _i * 8192), 16, 0, 0); } while (0)
; #define PG8_LDA(dst, b, h) do { _Pragma("unroll") for (int m = 0; m < 4; ++m) Frag<F8>::load(dst[m], lds + PG8_SA(b, h) + aoff + m * 2048); } while (0)
; #define PG8_LDB(dst, b, h) do { _Pragma("unroll") for (int n = 0; n < 2; ++n) Frag<F8>::load(dst[n], lds + PG8_SB(b, h) + boff + n * 2048); } while (0)
; #define PG8_MMA(ai, bj, At, Bt) do { __builtin_amdgcn_s_setprio(3); _Pragma("unroll") for (int m = 0; m < 4; ++m) _Pragma("unroll") for (int n = 0; n < 2; ++n) Frag<F8>::mma(acc[ai][bj][m][n], Bt[n], At[m]); \
;         __builtin_amdgcn_s_setprio(0); } while (0)
; #define PG8_WAIT_V(n) asm volatile("s_waitcnt vmcnt(" #n ")" ::: "memory")
; #define PG8_WAIT_L(n) asm volatile("s_waitcnt lgkmcnt(" #n ")" ::: "memory")
; #define PG8_BAR __builtin_amdgcn_s_barrier()
; #define PG8_SCHED __builtin_amdgcn_sched_barrier(0)
; template <class Epi, class Sched, bool ALIGN_EPI = false, bool SP2 = false, bool F8 = false>
; __device__ __forceinline__ void gemm_phase(PG8_LAS unsigned char* lds, const Gemm g, const Sched& S, const Epi& E) {
;     ...
;             PG8_LDB(B0, 1, 0); PG8_LDB(B1, 1, 1); PG8_SCHED; PG8_LDA(At, 1, 0); PG8_STAGE(PG8_SA(0, 1), a2 + hstep, voffA);
;             PG8_WAIT_V(8); PG8_WAIT_L(0); PG8_BAR; PG8_MMA(0, 0, At, B0); PG8_MMA(0, 1, At, B1); PG8_BAR; PG8_SCHED;
;             PG8_LDA(At, 1, 1); PG8_STAGE(PG8_SB(1, 0), b3, voffB); PG8_STAGE(PG8_SB(1, 1), b3 + hstep, voffB); PG8_STAGE(PG8_SA(1, 0), a3, voffA);
;             PG8_WAIT_V(8); PG8_WAIT_L(0); PG8_BAR; PG8_MMA(1, 0, At, B0); PG8_MMA(1, 1, At, B1); PG8_BAR; PG8_SCHED;
	s_setprio 3
	s_waitcnt lgkmcnt(0)
	v_mfma_f32_16x16x128_f8f6f4 v[158:161], v[2:9], v[200:207], v[158:161]
	v_mfma_f32_16x16x128_f8f6f4 v[154:157], v[10:17], v[200:207], v[154:157]
	v_mfma_f32_16x16x128_f8f6f4 v[150:153], v[2:9], v[208:215], v[150:153]
	v_mfma_f32_16x16x128_f8f6f4 v[142:145], v[10:17], v[208:215], v[142:145]
	v_mfma_f32_16x16x128_f8f6f4 v[130:133], v[2:9], v[216:223], v[130:133]
	v_mfma_f32_16x16x128_f8f6f4 v[122:125], v[10:17], v[216:223], v[122:125]
	v_mfma_f32_16x16x128_f8f6f4 v[118:121], v[2:9], v[224:231], v[118:121]
	v_mfma_f32_16x16x128_f8f6f4 v[110:113], v[10:17], v[224:231], v[110:113]
	v_mfma_f32_16x16x128_f8f6f4 v[146:149], v[18:25], v[200:207], v[146:149]
	v_mfma_f32_16x16x128_f8f6f4 v[138:141], v[26:33], v[200:207], v[138:141]
	v_mfma_f32_16x16x128_f8f6f4 v[134:137], v[18:25], v[208:215], v[134:137]
	v_mfma_f32_16x16x128_f8f6f4 v[126:129], v[26:33], v[208:215], v[126:129]
	v_mfma_f32_16x16x128_f8f6f4 v[114:117], v[18:25], v[216:223], v[114:117]
	v_mfma_f32_16x16x128_f8f6f4 v[106:109], v[26:33], v[216:223], v[106:109]
	v_mfma_f32_16x16x128_f8f6f4 v[102:105], v[18:25], v[224:231], v[102:105]
	v_mfma_f32_16x16x128_f8f6f4 v[98:101], v[26:33], v[224:231], v[98:101]
	s_setprio 0
	s_barrier
	s_add_i32 s0, s0, s76
	v_lshl_add_u64 v[182:183], v[182:183], 0, s[18:19]
	s_mov_b32 m0, s0
	ds_read_b128 v[200:203], v196 offset:49152
	ds_read_b128 v[204:207], v196 offset:50176
	ds_read_b128 v[208:211], v196 offset:51200
	ds_read_b128 v[212:215], v196 offset:52224
	ds_read_b128 v[216:219], v196 offset:53248
	ds_read_b128 v[220:223], v196 offset:54272
	ds_read_b128 v[224:227], v196 offset:55296
	ds_read_b128 v[228:231], v196 offset:56320
	global_load_lds_dwordx4 v[182:183], off
	s_add_i32 m0, s0, 0x2000
	s_add_u32 s4, s72, 0x20080
	v_lshl_add_u64 v[182:183], v[184:185], 0, s[18:19]
	s_addc_u32 s5, s73, 0
	s_add_i32 s0, s1, s76
	global_load_lds_dwordx4 v[182:183], off
	v_lshl_add_u64 v[182:183], s[4:5], 0, v[170:171]
	s_mov_b32 m0, s0
	s_nop 0
	global_load_lds_dwordx4 v[182:183], off
	v_lshl_add_u64 v[182:183], s[4:5], 0, v[166:167]
	s_add_i32 m0, s0, 0x2000
	s_nop 0
	global_load_lds_dwordx4 v[182:183], off
	v_lshl_add_u64 v[182:183], v[186:187], 0, s[18:19]
	s_mov_b32 m0, s85
	s_nop 0
	global_load_lds_dwordx4 v[182:183], off
	v_lshl_add_u64 v[182:183], v[188:189], 0, s[18:19]
	s_mov_b32 m0, s86
	s_nop 0
	global_load_lds_dwordx4 v[182:183], off
	s_waitcnt vmcnt(8)
	s_waitcnt lgkmcnt(0)
	s_barrier
	s_setprio 3
	s_waitcnt lgkmcnt(0)
	v_mfma_f32_16x16x128_f8f6f4 v[94:97], v[2:9], v[200:207], v[94:97]
	v_mfma_f32_16x16x128_f8f6f4 v[90:93], v[10:17], v[200:207], v[90:93]
	v_mfma_f32_16x16x128_f8f6f4 v[86:89], v[2:9], v[208:215], v[86:89]
	v_mfma_f32_16x16x128_f8f6f4 v[82:85], v[10:17], v[208:215], v[82:85]
	v_mfma_f32_16x16x128_f8f6f4 v[70:73], v[2:9], v[216:223], v[70:73]
	v_mfma_f32_16x16x128_f8f6f4 v[66:69], v[10:17], v[216:223], v[66:69]
	v_mfma_f32_16x16x128_f8f6f4 v[54:57], v[2:9], v[224:231], v[54:57]
	v_mfma_f32_16x16x128_f8f6f4 v[50:53], v[10:17], v[224:231], v[50:53]
	v_mfma_f32_16x16x128_f8f6f4 v[78:81], v[18:25], v[200:207], v[78:81]
	v_mfma_f32_16x16x128_f8f6f4 v[74:77], v[26:33], v[200:207], v[74:77]
	v_mfma_f32_16x16x128_f8f6f4 v[62:65], v[18:25], v[208:215], v[62:65]
	v_mfma_f32_16x16x128_f8f6f4 v[58:61], v[26:33], v[208:215], v[58:61]
	v_mfma_f32_16x16x128_f8f6f4 v[46:49], v[18:25], v[216:223], v[46:49]
	v_mfma_f32_16x16x128_f8f6f4 v[42:45], v[26:33], v[216:223], v[42:45]
	v_mfma_f32_16x16x128_f8f6f4 v[38:41], v[18:25], v[224:231], v[38:41]
	v_mfma_f32_16x16x128_f8f6f4 v[34:37], v[26:33], v[224:231], v[34:37]
	s_setprio 0
	s_barrier
	s_add_i32 s96, s96, 2
	s_add_u32 s70, s70, 0x100
	s_addc_u32 s71, s71, 0
	s_add_u32 s93, s93, 0x100
	s_addc_u32 s95, s95, 0
	s_cmp_gt_u32 s96, 5
	s_cbranch_scc0 .LBB0_151

; #define PG8_STAGE(bufoff, gbase, voff) do { _Pragma("unroll") for (int _i = 0; _i < 2; ++_i) \
;         __builtin_amdgcn_global_load_lds((const unsigned*)((const char*)(gbase) + (voff)[_i]), (PG8_LAS unsigned*)(lds + (bufoff) + ldsw + _i * 8192), 16, 0, 0); } while (0)
; #define PG8_LDA(dst, b, h) do { _Pragma("unroll") for (int m = 0; m < 4; ++m) Frag<F8>::load(dst[m], lds + PG8_SA(b, h) + aoff + m * 2048); } while (0)
; #define PG8_LDB(dst, b, h) do { _Pragma("unroll") for (int n = 0; n < 2; ++n) Frag<F8>::load(dst[n], lds + PG8_SB(b, h) + boff + n * 2048); } while (0)
; #define PG8_MMA(ai, bj, At, Bt) do { __builtin_amdgcn_s_setprio(3); _Pragma("unroll") for (int m = 0; m < 4; ++m) _Pragma("unroll") for (int n = 0; n < 2; ++n) Frag<F8>::mma(acc[ai][bj][m][n], Bt[n], At[m]); \
;         __builtin_amdgcn_s_setprio(0); } while (0)
; #define PG8_WAIT_V(n) asm volatile("s_waitcnt vmcnt(" #n ")" ::: "memory")
; #define PG8_WAIT_L(n) asm volatile("s_waitcnt lgkmcnt(" #n ")" ::: "memory")
; #define PG8_BAR __builtin_amdgcn_s_barrier()
; #define PG8_SCHED __builtin_amdgcn_sched_barrier(0)
; template <class Epi, class Sched, bool ALIGN_EPI = false, bool SP2 = false, bool F8 = false>
; __device__ __forceinline__ void gemm_phase(PG8_LAS unsigned char* lds, const Gemm g, const Sched& S, const Epi& E) {
;     ...
;             PG8_LDB(B0, 0, 0); PG8_LDB(B1, 0, 1); PG8_SCHED; PG8_LDA(At, 0, 0); PG8_STAGE(PG8_SA(1, 1), a1 + hstep, voffA);
;             PG8_WAIT_V(8); PG8_WAIT_L(0); PG8_BAR; PG8_MMA(0, 0, At, B0); PG8_MMA(0, 1, At, B1); PG8_BAR; PG8_SCHED;
;             PG8_LDA(At, 0, 1); PG8_STAGE(PG8_SB(0, 0), b2, voffB); PG8_STAGE(PG8_SB(0, 1), b2 + hstep, voffB); PG8_STAGE(PG8_SA(0, 0), a2, voffA);
;             PG8_WAIT_V(8); PG8_WAIT_L(0); PG8_BAR; PG8_MMA(1, 0, At, B0); PG8_MMA(1, 1, At, B1); PG8_BAR; PG8_SCHED;
.LBB0_162:
	ds_read_b128 v[18:21], v167
	ds_read_b128 v[22:25], v167 offset:1024
	ds_read_b128 v[26:29], v167 offset:2048
	ds_read_b128 v[30:33], v167 offset:3072
	ds_read_b128 v[2:5], v188
	ds_read_b128 v[6:9], v188 offset:1024
	ds_read_b128 v[10:13], v188 offset:2048
	ds_read_b128 v[14:17], v188 offset:3072
	s_add_u32 s0, s16, 0x100100
	s_addc_u32 s1, s17, 0
	s_add_u32 s3, s16, s45
	s_addc_u32 s4, s17, s70
	s_cmp_eq_u32 s71, 4
	s_cselect_b32 s23, s9, s1
	s_cselect_b32 s22, s8, s0
	s_cselect_b32 s19, s13, s4
	s_cselect_b32 s18, s12, s3
	s_mov_b32 m0, s72
	v_lshl_add_u64 v[218:219], s[16:17], 0, v[176:177]
	ds_read_b128 v[180:183], v189
	ds_read_b128 v[184:187], v189 offset:1024
	ds_read_b128 v[194:197], v189 offset:2048
	ds_read_b128 v[198:201], v189 offset:3072
	ds_read_b128 v[202:205], v189 offset:4096
	ds_read_b128 v[206:209], v189 offset:5120
	ds_read_b128 v[210:213], v189 offset:6144
	ds_read_b128 v[214:217], v189 offset:7168
	global_load_lds_dwordx4 v[218:219], off
	v_lshl_add_u64 v[218:219], s[16:17], 0, v[178:179]
	s_mov_b32 m0, s73
	s_nop 0
	global_load_lds_dwordx4 v[218:219], off
	s_waitcnt vmcnt(8)
	s_waitcnt lgkmcnt(0)
	s_barrier
	s_setprio 3
	s_waitcnt lgkmcnt(0)
	v_mfma_f32_16x16x128_f8f6f4 v[158:161], v[18:25], v[180:187], v[158:161]
	v_mfma_f32_16x16x128_f8f6f4 v[154:157], v[26:33], v[180:187], v[154:157]
	v_mfma_f32_16x16x128_f8f6f4 v[150:153], v[18:25], v[194:201], v[150:153]
	v_mfma_f32_16x16x128_f8f6f4 v[142:145], v[26:33], v[194:201], v[142:145]
	v_mfma_f32_16x16x128_f8f6f4 v[134:137], v[18:25], v[202:209], v[134:137]
	v_mfma_f32_16x16x128_f8f6f4 v[126:129], v[26:33], v[202:209], v[126:129]
	v_mfma_f32_16x16x128_f8f6f4 v[118:121], v[18:25], v[210:217], v[118:121]
	v_mfma_f32_16x16x128_f8f6f4 v[110:113], v[26:33], v[210:217], v[110:113]
	v_mfma_f32_16x16x128_f8f6f4 v[146:149], v[2:9], v[180:187], v[146:149]
	v_mfma_f32_16x16x128_f8f6f4 v[138:141], v[10:17], v[180:187], v[138:141]
	v_mfma_f32_16x16x128_f8f6f4 v[130:133], v[2:9], v[194:201], v[130:133]
	v_mfma_f32_16x16x128_f8f6f4 v[122:125], v[10:17], v[194:201], v[122:125]
	v_mfma_f32_16x16x128_f8f6f4 v[114:117], v[2:9], v[202:209], v[114:117]
	v_mfma_f32_16x16x128_f8f6f4 v[106:109], v[10:17], v[202:209], v[106:109]
	v_mfma_f32_16x16x128_f8f6f4 v[102:105], v[2:9], v[210:217], v[102:105]
	v_mfma_f32_16x16x128_f8f6f4 v[98:101], v[10:17], v[210:217], v[98:101]
	s_setprio 0
	s_barrier
	s_mov_b32 m0, s74
	v_lshl_add_u64 v[180:181], s[18:19], 0, v[172:173]
	s_add_u32 s4, s18, 0x20000
	ds_read_b128 v[194:197], v189 offset:16384
	ds_read_b128 v[198:201], v189 offset:17408
	ds_read_b128 v[202:205], v189 offset:18432
	ds_read_b128 v[206:209], v189 offset:19456
	ds_read_b128 v[210:213], v189 offset:20480
	ds_read_b128 v[214:217], v189 offset:21504
	ds_read_b128 v[218:221], v189 offset:22528
	ds_read_b128 v[222:225], v189 offset:23552
	global_load_lds_dwordx4 v[180:181], off
	v_lshl_add_u64 v[182:183], s[18:19], 0, v[168:169]
	s_mov_b32 m0, s75
	s_addc_u32 s5, s19, 0
	global_load_lds_dwordx4 v[182:183], off
	v_lshl_add_u64 v[184:185], s[4:5], 0, v[172:173]
	s_mov_b32 m0, s76
	v_lshl_add_u64 v[186:187], s[22:23], 0, v[170:171]
	global_load_lds_dwordx4 v[184:185], off
	v_lshl_add_u64 v[184:185], s[4:5], 0, v[168:169]
	s_mov_b32 m0, s77
	s_nop 0
	global_load_lds_dwordx4 v[184:185], off
	v_lshl_add_u64 v[184:185], s[22:23], 0, v[174:175]
	s_mov_b32 m0, s30
	s_nop 0
	global_load_lds_dwordx4 v[184:185], off
	s_mov_b32 m0, s31
	s_nop 0
	global_load_lds_dwordx4 v[186:187], off
	s_waitcnt vmcnt(8)
	s_waitcnt lgkmcnt(0)
	s_barrier
	s_setprio 3
	s_waitcnt lgkmcnt(0)
	v_mfma_f32_16x16x128_f8f6f4 v[94:97], v[18:25], v[194:201], v[94:97]
	v_mfma_f32_16x16x128_f8f6f4 v[90:93], v[26:33], v[194:201], v[90:93]
	v_mfma_f32_16x16x128_f8f6f4 v[86:89], v[18:25], v[202:209], v[86:89]
	v_mfma_f32_16x16x128_f8f6f4 v[78:81], v[26:33], v[202:209], v[78:81]
	v_mfma_f32_16x16x128_f8f6f4 v[70:73], v[18:25], v[210:217], v[70:73]
	v_mfma_f32_16x16x128_f8f6f4 v[62:65], v[26:33], v[210:217], v[62:65]
	v_mfma_f32_16x16x128_f8f6f4 v[54:57], v[18:25], v[218:225], v[54:57]
	v_mfma_f32_16x16x128_f8f6f4 v[46:49], v[26:33], v[218:225], v[46:49]
	v_mfma_f32_16x16x128_f8f6f4 v[82:85], v[2:9], v[194:201], v[82:85]
	v_mfma_f32_16x16x128_f8f6f4 v[74:77], v[10:17], v[194:201], v[74:77]
	v_mfma_f32_16x16x128_f8f6f4 v[66:69], v[2:9], v[202:209], v[66:69]
	v_mfma_f32_16x16x128_f8f6f4 v[58:61], v[10:17], v[202:209], v[58:61]
	v_mfma_f32_16x16x128_f8f6f4 v[50:53], v[2:9], v[210:217], v[50:53]
	v_mfma_f32_16x16x128_f8f6f4 v[42:45], v[10:17], v[210:217], v[42:45]
	v_mfma_f32_16x16x128_f8f6f4 v[38:41], v[2:9], v[218:225], v[38:41]
	v_mfma_f32_16x16x128_f8f6f4 v[34:37], v[10:17], v[218:225], v[34:37]
	s_setprio 0
	s_barrier
; #define PG8_STAGE(bufoff, gbase, voff) do { _Pragma("unroll") for (int _i = 0; _i < 2; ++_i) \
;         __builtin_amdgcn_global_load_lds((const unsigned*)((const char*)(gbase) + (voff)[_i]), (PG8_LAS unsigned*)(lds + (bufoff) + ldsw + _i * 8192), 16, 0, 0); } while (0)
; #define PG8_LDA(dst, b, h) do { _Pragma("unroll") for (int m = 0; m < 4; ++m) Frag<F8>::load(dst[m], lds + PG8_SA(b, h) + aoff + m * 2048); } while (0)
; #define PG8_LDB(dst, b, h) do { _Pragma("unroll") for (int n = 0; n < 2; ++n) Frag<F8>::load(dst[n], lds + PG8_SB(b, h) + boff + n * 2048); } while (0)
; #define PG8_MMA(ai, bj, At, Bt) do { __builtin_amdgcn_s_setprio(3); _Pragma("unroll") for (int m = 0; m < 4; ++m) _Pragma("unroll") for (int n = 0; n < 2; ++n) Frag<F8>::mma(acc[ai][bj][m][n], Bt[n], At[m]); \
;         __builtin_amdgcn_s_setprio(0); } while (0)
; #define PG8_WAIT_V(n) asm volatile("s_waitcnt vmcnt(" #n ")" ::: "memory")
; #define PG8_WAIT_L(n) asm volatile("s_waitcnt lgkmcnt(" #n ")" ::: "memory")
; #define PG8_BAR __builtin_amdgcn_s_barrier()
; #define PG8_SCHED __builtin_amdgcn_sched_barrier(0)
; template <class Epi, class Sched, bool ALIGN_EPI = false, bool SP2 = false, bool F8 = false>
; __device__ __forceinline__ void gemm_phase(PG8_LAS unsigned char* lds, const Gemm g, const Sched& S, const Epi& E) {
;     ...
;             PG8_LDB(B0, 1, 0); PG8_LDB(B1, 1, 1); PG8_SCHED; PG8_LDA(At, 1, 0); PG8_STAGE(PG8_SA(0, 1), a2 + hstep, voffA);
;             PG8_WAIT_V(8); PG8_WAIT_L(0); PG8_BAR; PG8_MMA(0, 0, At, B0); PG8_MMA(0, 1, At, B1); PG8_BAR; PG8_SCHED;
;             PG8_LDA(At, 1, 1); PG8_STAGE(PG8_SB(1, 0), b3, voffB); PG8_STAGE(PG8_SB(1, 1), b3 + hstep, voffB); PG8_STAGE(PG8_SA(1, 0), a3, voffA);
;             PG8_WAIT_V(8); PG8_WAIT_L(0); PG8_BAR; PG8_MMA(1, 0, At, B0); PG8_MMA(1, 1, At, B1); PG8_BAR; PG8_SCHED;
;     ...
;         if constexpr (ALIGN_EPI) { if (wr == 0) PG8_BAR; }
	ds_read_b128 v[2:5], v191
	ds_read_b128 v[6:9], v191 offset:1024
	ds_read_b128 v[10:13], v191 offset:2048
	ds_read_b128 v[14:17], v191 offset:3072
	ds_read_b128 v[18:21], v192
	ds_read_b128 v[22:25], v192 offset:1024
	ds_read_b128 v[26:29], v192 offset:2048
	ds_read_b128 v[30:33], v192 offset:3072
	s_add_u32 s4, s22, 0x20000
	s_addc_u32 s5, s23, 0
	s_mov_b32 m0, s38
	v_lshl_add_u64 v[226:227], s[4:5], 0, v[174:175]
	ds_read_b128 v[194:197], v189 offset:32768
	ds_read_b128 v[198:201], v189 offset:33792
	ds_read_b128 v[202:205], v189 offset:34816
	ds_read_b128 v[206:209], v189 offset:35840
	ds_read_b128 v[210:213], v189 offset:36864
	ds_read_b128 v[214:217], v189 offset:37888
	ds_read_b128 v[218:221], v189 offset:38912
	ds_read_b128 v[222:225], v189 offset:39936
	global_load_lds_dwordx4 v[226:227], off
	v_lshl_add_u64 v[226:227], s[4:5], 0, v[170:171]
	s_mov_b32 m0, s39
	s_nop 0
	global_load_lds_dwordx4 v[226:227], off
	s_waitcnt vmcnt(8)
	s_waitcnt lgkmcnt(0)
	s_barrier
	s_setprio 3
	s_waitcnt lgkmcnt(0)
	v_mfma_f32_16x16x128_f8f6f4 v[158:161], v[2:9], v[194:201], v[158:161]
	v_mfma_f32_16x16x128_f8f6f4 v[154:157], v[10:17], v[194:201], v[154:157]
	v_mfma_f32_16x16x128_f8f6f4 v[150:153], v[2:9], v[202:209], v[150:153]
	v_mfma_f32_16x16x128_f8f6f4 v[142:145], v[10:17], v[202:209], v[142:145]
	v_mfma_f32_16x16x128_f8f6f4 v[134:137], v[2:9], v[210:217], v[134:137]
	v_mfma_f32_16x16x128_f8f6f4 v[126:129], v[10:17], v[210:217], v[126:129]
	v_mfma_f32_16x16x128_f8f6f4 v[118:121], v[2:9], v[218:225], v[118:121]
	v_mfma_f32_16x16x128_f8f6f4 v[110:113], v[10:17], v[218:225], v[110:113]
	v_mfma_f32_16x16x128_f8f6f4 v[146:149], v[18:25], v[194:201], v[146:149]
	v_mfma_f32_16x16x128_f8f6f4 v[138:141], v[26:33], v[194:201], v[138:141]
	v_mfma_f32_16x16x128_f8f6f4 v[130:133], v[18:25], v[202:209], v[130:133]
	v_mfma_f32_16x16x128_f8f6f4 v[122:125], v[26:33], v[202:209], v[122:125]
	v_mfma_f32_16x16x128_f8f6f4 v[114:117], v[18:25], v[210:217], v[114:117]
	v_mfma_f32_16x16x128_f8f6f4 v[106:109], v[26:33], v[210:217], v[106:109]
	v_mfma_f32_16x16x128_f8f6f4 v[102:105], v[18:25], v[218:225], v[102:105]
	v_mfma_f32_16x16x128_f8f6f4 v[98:101], v[26:33], v[218:225], v[98:101]
	s_setprio 0
	s_barrier
	s_mov_b32 m0, s78
	v_lshl_add_u64 v[180:181], v[180:181], 0, s[14:15]
	s_add_u32 s4, s18, 0x20080
	ds_read_b128 v[194:197], v189 offset:49152
	ds_read_b128 v[198:201], v189 offset:50176
	ds_read_b128 v[202:205], v189 offset:51200
	ds_read_b128 v[206:209], v189 offset:52224
	ds_read_b128 v[210:213], v189 offset:53248
	ds_read_b128 v[214:217], v189 offset:54272
	ds_read_b128 v[218:221], v189 offset:55296
	ds_read_b128 v[222:225], v189 offset:56320
	global_load_lds_dwordx4 v[180:181], off
	v_lshl_add_u64 v[180:181], v[182:183], 0, s[14:15]
	s_mov_b32 m0, s79
	s_addc_u32 s5, s19, 0
	global_load_lds_dwordx4 v[180:181], off
	v_lshl_add_u64 v[180:181], s[4:5], 0, v[172:173]
	s_mov_b32 m0, s80
	s_nop 0
	global_load_lds_dwordx4 v[180:181], off
	v_lshl_add_u64 v[180:181], s[4:5], 0, v[168:169]
	s_mov_b32 m0, s81
	s_nop 0
	global_load_lds_dwordx4 v[180:181], off
	v_lshl_add_u64 v[180:181], v[184:185], 0, s[14:15]
	s_mov_b32 m0, s43
	s_nop 0
	global_load_lds_dwordx4 v[180:181], off
	v_lshl_add_u64 v[180:181], v[186:187], 0, s[14:15]
	s_mov_b32 m0, s44
	s_nop 0
	global_load_lds_dwordx4 v[180:181], off
	s_waitcnt vmcnt(8)
	s_waitcnt lgkmcnt(0)
	s_barrier
	s_setprio 3
	s_waitcnt lgkmcnt(0)
	v_mfma_f32_16x16x128_f8f6f4 v[94:97], v[2:9], v[194:201], v[94:97]
	v_mfma_f32_16x16x128_f8f6f4 v[90:93], v[10:17], v[194:201], v[90:93]
	v_mfma_f32_16x16x128_f8f6f4 v[86:89], v[2:9], v[202:209], v[86:89]
	v_mfma_f32_16x16x128_f8f6f4 v[78:81], v[10:17], v[202:209], v[78:81]
	v_mfma_f32_16x16x128_f8f6f4 v[70:73], v[2:9], v[210:217], v[70:73]
	v_mfma_f32_16x16x128_f8f6f4 v[62:65], v[10:17], v[210:217], v[62:65]
	v_mfma_f32_16x16x128_f8f6f4 v[54:57], v[2:9], v[218:225], v[54:57]
	v_mfma_f32_16x16x128_f8f6f4 v[46:49], v[10:17], v[218:225], v[46:49]
	v_mfma_f32_16x16x128_f8f6f4 v[82:85], v[18:25], v[194:201], v[82:85]
	v_mfma_f32_16x16x128_f8f6f4 v[74:77], v[26:33], v[194:201], v[74:77]
	v_mfma_f32_16x16x128_f8f6f4 v[66:69], v[18:25], v[202:209], v[66:69]
	v_mfma_f32_16x16x128_f8f6f4 v[58:61], v[26:33], v[202:209], v[58:61]
	v_mfma_f32_16x16x128_f8f6f4 v[50:53], v[18:25], v[210:217], v[50:53]
	v_mfma_f32_16x16x128_f8f6f4 v[42:45], v[26:33], v[210:217], v[42:45]
	v_mfma_f32_16x16x128_f8f6f4 v[38:41], v[18:25], v[218:225], v[38:41]
	v_mfma_f32_16x16x128_f8f6f4 v[34:37], v[26:33], v[218:225], v[34:37]
	s_setprio 0
	s_barrier
	s_add_i32 s71, s71, 2
	s_add_u32 s16, s16, 0x100
	s_addc_u32 s17, s17, 0
	s_cmp_gt_u32 s71, 5
	s_cbranch_scc0 .LBB0_162
	s_cmpk_lt_u32 s25, 0x100
	s_cbranch_scc0 .LBB0_165
	s_barrier

; #define PG8_STAGE(bufoff, gbase, voff) do { _Pragma("unroll") for (int _i = 0; _i < 2; ++_i) \
;         __builtin_amdgcn_global_load_lds((const unsigned*)((const char*)(gbase) + (voff)[_i]), (PG8_LAS unsigned*)(lds + (bufoff) + ldsw + _i * 8192), 16, 0, 0); } while (0)
; #define PG8_LDA(dst, b, h) do { _Pragma("unroll") for (int m = 0; m < 4; ++m) Frag<F8>::load(dst[m], lds + PG8_SA(b, h) + aoff + m * 2048); } while (0)
; #define PG8_LDB(dst, b, h) do { _Pragma("unroll") for (int n = 0; n < 2; ++n) Frag<F8>::load(dst[n], lds + PG8_SB(b, h) + boff + n * 2048); } while (0)
; #define PG8_MMA(ai, bj, At, Bt) do { __builtin_amdgcn_s_setprio(3); _Pragma("unroll") for (int m = 0; m < 4; ++m) _Pragma("unroll") for (int n = 0; n < 2; ++n) Frag<F8>::mma(acc[ai][bj][m][n], Bt[n], At[m]); \
;         __builtin_amdgcn_s_setprio(0); } while (0)
; #define PG8_WAIT_V(n) asm volatile("s_waitcnt vmcnt(" #n ")" ::: "memory")
; #define PG8_WAIT_L(n) asm volatile("s_waitcnt lgkmcnt(" #n ")" ::: "memory")
; #define PG8_BAR __builtin_amdgcn_s_barrier()
; #define PG8_SCHED __builtin_amdgcn_sched_barrier(0)
; template <class Epi, class Sched, bool ALIGN_EPI = false, bool SP2 = false, bool F8 = false>
; __device__ __forceinline__ void gemm_phase(PG8_LAS unsigned char* lds, const Gemm g, const Sched& S, const Epi& E) {
;     ...
;             PG8_LDB(B0, 0, 0); PG8_LDB(B1, 0, 1); PG8_SCHED; PG8_LDA(At, 0, 0); PG8_STAGE(PG8_SA(1, 1), a1 + hstep, voffA);
;             PG8_WAIT_V(8); PG8_WAIT_L(0); PG8_BAR; PG8_MMA(0, 0, At, B0); PG8_MMA(0, 1, At, B1); PG8_BAR; PG8_SCHED;
;             PG8_LDA(At, 0, 1); PG8_STAGE(PG8_SB(0, 0), b2, voffB); PG8_STAGE(PG8_SB(0, 1), b2 + hstep, voffB); PG8_STAGE(PG8_SA(0, 0), a2, voffA);
;             PG8_WAIT_V(8); PG8_WAIT_L(0); PG8_BAR; PG8_MMA(1, 0, At, B0); PG8_MMA(1, 1, At, B1); PG8_BAR; PG8_SCHED;
.LBB0_437:
	v_add_u32_e32 v186, s90, v158
	v_add_u32_e32 v202, s91, v158
	s_add_u32 s0, s36, s70
	ds_read_b128 v[174:177], v186
	ds_read_b128 v[178:181], v186 offset:1024
	ds_read_b128 v[182:185], v186 offset:2048
	ds_read_b128 v[186:189], v186 offset:3072
	ds_read_b128 v[190:193], v202
	ds_read_b128 v[194:197], v202 offset:1024
	ds_read_b128 v[198:201], v202 offset:2048
	ds_read_b128 v[202:205], v202 offset:3072
	s_addc_u32 s1, s37, s71
	s_add_u32 s0, s0, 0x100
	s_addc_u32 s1, s1, 0
	s_add_u32 s23, s49, s70
	s_addc_u32 s33, s93, s71
	s_cmpk_eq_i32 s70, 0x700
	s_cselect_b32 s75, s3, s1
	s_cselect_b32 s74, s4, s0
	s_cselect_b32 s73, s5, s33
	s_cselect_b32 s72, s6, s23
	v_lshl_add_u64 v[238:239], v[146:147], 0, s[70:71]
	s_add_i32 m0, s19, 0xc000
	ds_read_b128 v[206:209], v160
	ds_read_b128 v[210:213], v160 offset:1024
	ds_read_b128 v[214:217], v160 offset:2048
	ds_read_b128 v[218:221], v160 offset:3072
	ds_read_b128 v[222:225], v160 offset:4096
	ds_read_b128 v[226:229], v160 offset:5120
	ds_read_b128 v[230:233], v160 offset:6144
	ds_read_b128 v[234:237], v160 offset:7168
	global_load_lds_dwordx4 v[238:239], off
	v_lshl_add_u64 v[238:239], v[148:149], 0, s[70:71]
	s_add_i32 m0, s19, 0xe000
	s_nop 0
	global_load_lds_dwordx4 v[238:239], off
	s_waitcnt vmcnt(8)
	s_waitcnt lgkmcnt(0)
	s_barrier
	s_setprio 3
	s_waitcnt lgkmcnt(0)
	v_mfma_f32_16x16x32_bf16 v[22:25], v[174:177], v[206:209], v[22:25]
	v_mfma_f32_16x16x32_bf16 v[30:33], v[182:185], v[206:209], v[30:33]
	v_mfma_f32_16x16x32_bf16 v[46:49], v[174:177], v[214:217], v[46:49]
	v_mfma_f32_16x16x32_bf16 v[54:57], v[182:185], v[214:217], v[54:57]
	v_mfma_f32_16x16x32_bf16 v[78:81], v[174:177], v[222:225], v[78:81]
	v_mfma_f32_16x16x32_bf16 v[86:89], v[182:185], v[222:225], v[86:89]
	v_mfma_f32_16x16x32_bf16 v[98:101], v[174:177], v[230:233], v[98:101]
	v_mfma_f32_16x16x32_bf16 v[102:105], v[182:185], v[230:233], v[102:105]
	v_mfma_f32_16x16x32_bf16 v[22:25], v[178:181], v[210:213], v[22:25]
	v_mfma_f32_16x16x32_bf16 v[30:33], v[186:189], v[210:213], v[30:33]
	v_mfma_f32_16x16x32_bf16 v[46:49], v[178:181], v[218:221], v[46:49]
	v_mfma_f32_16x16x32_bf16 v[54:57], v[186:189], v[218:221], v[54:57]
	v_mfma_f32_16x16x32_bf16 v[78:81], v[178:181], v[226:229], v[78:81]
	v_mfma_f32_16x16x32_bf16 v[86:89], v[186:189], v[226:229], v[86:89]
	v_mfma_f32_16x16x32_bf16 v[98:101], v[178:181], v[234:237], v[98:101]
	v_mfma_f32_16x16x32_bf16 v[102:105], v[186:189], v[234:237], v[102:105]
	v_mfma_f32_16x16x32_bf16 v[2:5], v[190:193], v[206:209], v[2:5]
	v_mfma_f32_16x16x32_bf16 v[6:9], v[198:201], v[206:209], v[6:9]
	v_mfma_f32_16x16x32_bf16 v[10:13], v[190:193], v[214:217], v[10:13]
	v_mfma_f32_16x16x32_bf16 v[14:17], v[198:201], v[214:217], v[14:17]
	v_mfma_f32_16x16x32_bf16 v[34:37], v[190:193], v[222:225], v[34:37]
	v_mfma_f32_16x16x32_bf16 v[38:41], v[198:201], v[222:225], v[38:41]
	v_mfma_f32_16x16x32_bf16 v[58:61], v[190:193], v[230:233], v[58:61]
	v_mfma_f32_16x16x32_bf16 v[62:65], v[198:201], v[230:233], v[62:65]
	v_mfma_f32_16x16x32_bf16 v[2:5], v[194:197], v[210:213], v[2:5]
	v_mfma_f32_16x16x32_bf16 v[6:9], v[202:205], v[210:213], v[6:9]
	v_mfma_f32_16x16x32_bf16 v[10:13], v[194:197], v[218:221], v[10:13]
	v_mfma_f32_16x16x32_bf16 v[14:17], v[202:205], v[218:221], v[14:17]
	v_mfma_f32_16x16x32_bf16 v[34:37], v[194:197], v[226:229], v[34:37]
	v_mfma_f32_16x16x32_bf16 v[38:41], v[202:205], v[226:229], v[38:41]
	v_mfma_f32_16x16x32_bf16 v[58:61], v[194:197], v[234:237], v[58:61]
	v_mfma_f32_16x16x32_bf16 v[62:65], v[202:205], v[234:237], v[62:65]
	s_setprio 0
	s_barrier
	s_add_i32 s0, s90, s83
	v_lshl_add_u64 v[238:239], s[72:73], 0, v[132:133]
	s_mov_b32 m0, s0
	ds_read_b128 v[206:209], v160 offset:16384
	ds_read_b128 v[210:213], v160 offset:17408
	ds_read_b128 v[214:217], v160 offset:18432
	ds_read_b128 v[218:221], v160 offset:19456
	ds_read_b128 v[222:225], v160 offset:20480
	ds_read_b128 v[226:229], v160 offset:21504
	ds_read_b128 v[230:233], v160 offset:22528
	ds_read_b128 v[234:237], v160 offset:23552
	global_load_lds_dwordx4 v[238:239], off
	s_add_i32 m0, s0, 0x2000
	s_add_u32 s68, s72, 0x40000
	v_lshl_add_u64 v[240:241], s[72:73], 0, v[136:137]
	s_addc_u32 s69, s73, 0
	s_add_i32 s0, s91, s83
	global_load_lds_dwordx4 v[240:241], off
	v_lshl_add_u64 v[242:243], s[68:69], 0, v[132:133]
	s_mov_b32 m0, s0
	v_lshl_add_u64 v[244:245], s[74:75], 0, v[134:135]
	global_load_lds_dwordx4 v[242:243], off
	v_lshl_add_u64 v[242:243], s[68:69], 0, v[136:137]
	s_add_i32 m0, s0, 0x2000
	s_nop 0
	global_load_lds_dwordx4 v[242:243], off
	v_lshl_add_u64 v[242:243], s[74:75], 0, v[130:131]
	s_mov_b32 m0, s19
	s_nop 0
	global_load_lds_dwordx4 v[242:243], off
	s_mov_b32 m0, s84
	s_nop 0
	global_load_lds_dwordx4 v[244:245], off
	s_waitcnt vmcnt(8)
	s_waitcnt lgkmcnt(0)
	s_barrier
; #define PG8_STAGE(bufoff, gbase, voff) do { _Pragma("unroll") for (int _i = 0; _i < 2; ++_i) \
;         __builtin_amdgcn_global_load_lds((const unsigned*)((const char*)(gbase) + (voff)[_i]), (PG8_LAS unsigned*)(lds + (bufoff) + ldsw + _i * 8192), 16, 0, 0); } while (0)
; #define PG8_LDA(dst, b, h) do { _Pragma("unroll") for (int m = 0; m < 4; ++m) Frag<F8>::load(dst[m], lds + PG8_SA(b, h) + aoff + m * 2048); } while (0)
; #define PG8_LDB(dst, b, h) do { _Pragma("unroll") for (int n = 0; n < 2; ++n) Frag<F8>::load(dst[n], lds + PG8_SB(b, h) + boff + n * 2048); } while (0)
; #define PG8_MMA(ai, bj, At, Bt) do { __builtin_amdgcn_s_setprio(3); _Pragma("unroll") for (int m = 0; m < 4; ++m) _Pragma("unroll") for (int n = 0; n < 2; ++n) Frag<F8>::mma(acc[ai][bj][m][n], Bt[n], At[m]); \
;         __builtin_amdgcn_s_setprio(0); } while (0)
; #define PG8_WAIT_V(n) asm volatile("s_waitcnt vmcnt(" #n ")" ::: "memory")
; #define PG8_WAIT_L(n) asm volatile("s_waitcnt lgkmcnt(" #n ")" ::: "memory")
; #define PG8_BAR __builtin_amdgcn_s_barrier()
; #define PG8_SCHED __builtin_amdgcn_sched_barrier(0)
; template <class Epi, class Sched, bool ALIGN_EPI = false, bool SP2 = false, bool F8 = false>
; __device__ __forceinline__ void gemm_phase(PG8_LAS unsigned char* lds, const Gemm g, const Sched& S, const Epi& E) {
;     ...
;             PG8_LDA(At, 0, 1); PG8_STAGE(PG8_SB(0, 0), b2, voffB); PG8_STAGE(PG8_SB(0, 1), b2 + hstep, voffB); PG8_STAGE(PG8_SA(0, 0), a2, voffA);
;             PG8_WAIT_V(8); PG8_WAIT_L(0); PG8_BAR; PG8_MMA(1, 0, At, B0); PG8_MMA(1, 1, At, B1); PG8_BAR; PG8_SCHED;
;             PG8_LDB(B0, 1, 0); PG8_LDB(B1, 1, 1); PG8_SCHED; PG8_LDA(At, 1, 0); PG8_STAGE(PG8_SA(0, 1), a2 + hstep, voffA);
;             PG8_WAIT_V(8); PG8_WAIT_L(0); PG8_BAR; PG8_MMA(0, 0, At, B0); PG8_MMA(0, 1, At, B1); PG8_BAR; PG8_SCHED;
;             PG8_LDA(At, 1, 1); PG8_STAGE(PG8_SB(1, 0), b3, voffB); PG8_STAGE(PG8_SB(1, 1), b3 + hstep, voffB); PG8_STAGE(PG8_SA(1, 0), a3, voffA);
	s_setprio 3
	s_waitcnt lgkmcnt(0)
	v_mfma_f32_16x16x32_bf16 v[66:69], v[174:177], v[206:209], v[66:69]
	v_mfma_f32_16x16x32_bf16 v[70:73], v[182:185], v[206:209], v[70:73]
	v_mfma_f32_16x16x32_bf16 v[90:93], v[174:177], v[214:217], v[90:93]
	v_mfma_f32_16x16x32_bf16 v[94:97], v[182:185], v[214:217], v[94:97]
	v_mfma_f32_16x16x32_bf16 v[106:109], v[174:177], v[222:225], v[106:109]
	v_mfma_f32_16x16x32_bf16 v[110:113], v[182:185], v[222:225], v[110:113]
	v_mfma_f32_16x16x32_bf16 v[114:117], v[174:177], v[230:233], v[114:117]
	v_mfma_f32_16x16x32_bf16 v[126:129], v[182:185], v[230:233], v[126:129]
	v_mfma_f32_16x16x32_bf16 v[66:69], v[178:181], v[210:213], v[66:69]
	v_mfma_f32_16x16x32_bf16 v[70:73], v[186:189], v[210:213], v[70:73]
	v_mfma_f32_16x16x32_bf16 v[90:93], v[178:181], v[218:221], v[90:93]
	v_mfma_f32_16x16x32_bf16 v[94:97], v[186:189], v[218:221], v[94:97]
	v_mfma_f32_16x16x32_bf16 v[106:109], v[178:181], v[226:229], v[106:109]
	v_mfma_f32_16x16x32_bf16 v[110:113], v[186:189], v[226:229], v[110:113]
	v_mfma_f32_16x16x32_bf16 v[114:117], v[178:181], v[234:237], v[114:117]
	v_mfma_f32_16x16x32_bf16 v[126:129], v[186:189], v[234:237], v[126:129]
	v_mfma_f32_16x16x32_bf16 v[18:21], v[190:193], v[206:209], v[18:21]
	v_mfma_f32_16x16x32_bf16 v[26:29], v[198:201], v[206:209], v[26:29]
	v_mfma_f32_16x16x32_bf16 v[42:45], v[190:193], v[214:217], v[42:45]
	v_mfma_f32_16x16x32_bf16 v[50:53], v[198:201], v[214:217], v[50:53]
	v_mfma_f32_16x16x32_bf16 v[74:77], v[190:193], v[222:225], v[74:77]
	v_mfma_f32_16x16x32_bf16 v[82:85], v[198:201], v[222:225], v[82:85]
	v_mfma_f32_16x16x32_bf16 v[122:125], v[190:193], v[230:233], v[122:125]
	v_mfma_f32_16x16x32_bf16 v[118:121], v[198:201], v[230:233], v[118:121]
	v_mfma_f32_16x16x32_bf16 v[18:21], v[194:197], v[210:213], v[18:21]
	v_mfma_f32_16x16x32_bf16 v[26:29], v[202:205], v[210:213], v[26:29]
	v_mfma_f32_16x16x32_bf16 v[42:45], v[194:197], v[218:221], v[42:45]
	v_mfma_f32_16x16x32_bf16 v[50:53], v[202:205], v[218:221], v[50:53]
	v_mfma_f32_16x16x32_bf16 v[74:77], v[194:197], v[226:229], v[74:77]
	v_mfma_f32_16x16x32_bf16 v[82:85], v[202:205], v[226:229], v[82:85]
	v_mfma_f32_16x16x32_bf16 v[122:125], v[194:197], v[234:237], v[122:125]
	v_mfma_f32_16x16x32_bf16 v[118:121], v[202:205], v[234:237], v[118:121]
	s_setprio 0
	s_barrier
	s_add_i32 s0, 0, 0x18000
	s_add_i32 s1, 0, 0x1c000
	v_add_u32_e32 v186, s0, v158
	v_add_u32_e32 v202, s1, v158
	ds_read_b128 v[174:177], v186
	ds_read_b128 v[178:181], v186 offset:1024
	ds_read_b128 v[182:185], v186 offset:2048
	ds_read_b128 v[186:189], v186 offset:3072
	ds_read_b128 v[190:193], v202
	ds_read_b128 v[194:197], v202 offset:1024
	ds_read_b128 v[198:201], v202 offset:2048
	ds_read_b128 v[202:205], v202 offset:3072
	s_add_u32 s68, s74, 0x40000
	s_addc_u32 s69, s75, 0
	s_mov_b32 m0, s85
	v_lshl_add_u64 v[246:247], s[68:69], 0, v[130:131]
	ds_read_b128 v[206:209], v160 offset:32768
	ds_read_b128 v[210:213], v160 offset:33792
	ds_read_b128 v[214:217], v160 offset:34816
	ds_read_b128 v[218:221], v160 offset:35840
	ds_read_b128 v[222:225], v160 offset:36864
	ds_read_b128 v[226:229], v160 offset:37888
	ds_read_b128 v[230:233], v160 offset:38912
	ds_read_b128 v[234:237], v160 offset:39936
	global_load_lds_dwordx4 v[246:247], off
	v_lshl_add_u64 v[246:247], s[68:69], 0, v[134:135]
	s_mov_b32 m0, s86
	s_nop 0
	global_load_lds_dwordx4 v[246:247], off
	s_waitcnt vmcnt(8)
	s_waitcnt lgkmcnt(0)
	s_barrier
	s_setprio 3
	s_waitcnt lgkmcnt(0)
	v_mfma_f32_16x16x32_bf16 v[22:25], v[174:177], v[206:209], v[22:25]
	v_mfma_f32_16x16x32_bf16 v[30:33], v[182:185], v[206:209], v[30:33]
	v_mfma_f32_16x16x32_bf16 v[46:49], v[174:177], v[214:217], v[46:49]
	v_mfma_f32_16x16x32_bf16 v[54:57], v[182:185], v[214:217], v[54:57]
	v_mfma_f32_16x16x32_bf16 v[78:81], v[174:177], v[222:225], v[78:81]
	v_mfma_f32_16x16x32_bf16 v[86:89], v[182:185], v[222:225], v[86:89]
	v_mfma_f32_16x16x32_bf16 v[98:101], v[174:177], v[230:233], v[98:101]
	v_mfma_f32_16x16x32_bf16 v[102:105], v[182:185], v[230:233], v[102:105]
	v_mfma_f32_16x16x32_bf16 v[22:25], v[178:181], v[210:213], v[22:25]
	v_mfma_f32_16x16x32_bf16 v[30:33], v[186:189], v[210:213], v[30:33]
	v_mfma_f32_16x16x32_bf16 v[46:49], v[178:181], v[218:221], v[46:49]
	v_mfma_f32_16x16x32_bf16 v[54:57], v[186:189], v[218:221], v[54:57]
	v_mfma_f32_16x16x32_bf16 v[78:81], v[178:181], v[226:229], v[78:81]
	v_mfma_f32_16x16x32_bf16 v[86:89], v[186:189], v[226:229], v[86:89]
	v_mfma_f32_16x16x32_bf16 v[98:101], v[178:181], v[234:237], v[98:101]
	v_mfma_f32_16x16x32_bf16 v[102:105], v[186:189], v[234:237], v[102:105]
	v_mfma_f32_16x16x32_bf16 v[2:5], v[190:193], v[206:209], v[2:5]
	v_mfma_f32_16x16x32_bf16 v[6:9], v[198:201], v[206:209], v[6:9]
	v_mfma_f32_16x16x32_bf16 v[10:13], v[190:193], v[214:217], v[10:13]
	v_mfma_f32_16x16x32_bf16 v[14:17], v[198:201], v[214:217], v[14:17]
	v_mfma_f32_16x16x32_bf16 v[34:37], v[190:193], v[222:225], v[34:37]
	v_mfma_f32_16x16x32_bf16 v[38:41], v[198:201], v[222:225], v[38:41]
	v_mfma_f32_16x16x32_bf16 v[58:61], v[190:193], v[230:233], v[58:61]
	v_mfma_f32_16x16x32_bf16 v[62:65], v[198:201], v[230:233], v[62:65]
	v_mfma_f32_16x16x32_bf16 v[2:5], v[194:197], v[210:213], v[2:5]
	v_mfma_f32_16x16x32_bf16 v[6:9], v[202:205], v[210:213], v[6:9]
	v_mfma_f32_16x16x32_bf16 v[10:13], v[194:197], v[218:221], v[10:13]
	v_mfma_f32_16x16x32_bf16 v[14:17], v[202:205], v[218:221], v[14:17]
	v_mfma_f32_16x16x32_bf16 v[34:37], v[194:197], v[226:229], v[34:37]
	v_mfma_f32_16x16x32_bf16 v[38:41], v[202:205], v[226:229], v[38:41]
	v_mfma_f32_16x16x32_bf16 v[58:61], v[194:197], v[234:237], v[58:61]
	v_mfma_f32_16x16x32_bf16 v[62:65], v[202:205], v[234:237], v[62:65]
	s_setprio 0
	s_barrier
; #define PG8_STAGE(bufoff, gbase, voff) do { _Pragma("unroll") for (int _i = 0; _i < 2; ++_i) \
;         __builtin_amdgcn_global_load_lds((const unsigned*)((const char*)(gbase) + (voff)[_i]), (PG8_LAS unsigned*)(lds + (bufoff) + ldsw + _i * 8192), 16, 0, 0); } while (0)
; #define PG8_LDA(dst, b, h) do { _Pragma("unroll") for (int m = 0; m < 4; ++m) Frag<F8>::load(dst[m], lds + PG8_SA(b, h) + aoff + m * 2048); } while (0)
; #define PG8_MMA(ai, bj, At, Bt) do { __builtin_amdgcn_s_setprio(3); _Pragma("unroll") for (int m = 0; m < 4; ++m) _Pragma("unroll") for (int n = 0; n < 2; ++n) Frag<F8>::mma(acc[ai][bj][m][n], Bt[n], At[m]); \
;         __builtin_amdgcn_s_setprio(0); } while (0)
; #define PG8_WAIT_V(n) asm volatile("s_waitcnt vmcnt(" #n ")" ::: "memory")
; #define PG8_WAIT_L(n) asm volatile("s_waitcnt lgkmcnt(" #n ")" ::: "memory")
; #define PG8_BAR __builtin_amdgcn_s_barrier()
; #define PG8_SCHED __builtin_amdgcn_sched_barrier(0)
; template <class Epi, class Sched, bool ALIGN_EPI = false, bool SP2 = false, bool F8 = false>
; __device__ __forceinline__ void gemm_phase(PG8_LAS unsigned char* lds, const Gemm g, const Sched& S, const Epi& E) {
;     ...
;             PG8_LDA(At, 1, 1); PG8_STAGE(PG8_SB(1, 0), b3, voffB); PG8_STAGE(PG8_SB(1, 1), b3 + hstep, voffB); PG8_STAGE(PG8_SA(1, 0), a3, voffA);
;             PG8_WAIT_V(8); PG8_WAIT_L(0); PG8_BAR; PG8_MMA(1, 0, At, B0); PG8_MMA(1, 1, At, B1); PG8_BAR; PG8_SCHED;
;     ...
;         if constexpr (ALIGN_EPI) { if (wr == 0) PG8_BAR; }
	s_add_i32 s0, s0, s83
	v_lshl_add_u64 v[238:239], v[238:239], 0, s[40:41]
	s_mov_b32 m0, s0
	ds_read_b128 v[206:209], v160 offset:49152
	ds_read_b128 v[210:213], v160 offset:50176
	ds_read_b128 v[214:217], v160 offset:51200
	ds_read_b128 v[218:221], v160 offset:52224
	ds_read_b128 v[222:225], v160 offset:53248
	ds_read_b128 v[226:229], v160 offset:54272
	ds_read_b128 v[230:233], v160 offset:55296
	ds_read_b128 v[234:237], v160 offset:56320
	global_load_lds_dwordx4 v[238:239], off
	s_add_i32 m0, s0, 0x2000
	s_add_u32 s68, s72, 0x40080
	v_lshl_add_u64 v[238:239], v[240:241], 0, s[40:41]
	s_addc_u32 s69, s73, 0
	s_add_i32 s0, s1, s83
	global_load_lds_dwordx4 v[238:239], off
	v_lshl_add_u64 v[238:239], s[68:69], 0, v[132:133]
	s_mov_b32 m0, s0
	s_nop 0
	global_load_lds_dwordx4 v[238:239], off
	v_lshl_add_u64 v[238:239], s[68:69], 0, v[136:137]
	s_add_i32 m0, s0, 0x2000
	s_nop 0
	global_load_lds_dwordx4 v[238:239], off
	v_lshl_add_u64 v[238:239], v[242:243], 0, s[40:41]
	s_mov_b32 m0, s87
	s_nop 0
	global_load_lds_dwordx4 v[238:239], off
	v_lshl_add_u64 v[238:239], v[244:245], 0, s[40:41]
	s_mov_b32 m0, s88
	s_nop 0
	global_load_lds_dwordx4 v[238:239], off
	s_waitcnt vmcnt(8)
	s_waitcnt lgkmcnt(0)
	s_barrier
	s_setprio 3
	s_waitcnt lgkmcnt(0)
	v_mfma_f32_16x16x32_bf16 v[66:69], v[174:177], v[206:209], v[66:69]
	v_mfma_f32_16x16x32_bf16 v[70:73], v[182:185], v[206:209], v[70:73]
	v_mfma_f32_16x16x32_bf16 v[90:93], v[174:177], v[214:217], v[90:93]
	v_mfma_f32_16x16x32_bf16 v[94:97], v[182:185], v[214:217], v[94:97]
	v_mfma_f32_16x16x32_bf16 v[106:109], v[174:177], v[222:225], v[106:109]
	v_mfma_f32_16x16x32_bf16 v[110:113], v[182:185], v[222:225], v[110:113]
	v_mfma_f32_16x16x32_bf16 v[114:117], v[174:177], v[230:233], v[114:117]
	v_mfma_f32_16x16x32_bf16 v[126:129], v[182:185], v[230:233], v[126:129]
	v_mfma_f32_16x16x32_bf16 v[66:69], v[178:181], v[210:213], v[66:69]
	v_mfma_f32_16x16x32_bf16 v[70:73], v[186:189], v[210:213], v[70:73]
	v_mfma_f32_16x16x32_bf16 v[90:93], v[178:181], v[218:221], v[90:93]
	v_mfma_f32_16x16x32_bf16 v[94:97], v[186:189], v[218:221], v[94:97]
	v_mfma_f32_16x16x32_bf16 v[106:109], v[178:181], v[226:229], v[106:109]
	v_mfma_f32_16x16x32_bf16 v[110:113], v[186:189], v[226:229], v[110:113]
	v_mfma_f32_16x16x32_bf16 v[114:117], v[178:181], v[234:237], v[114:117]
	v_mfma_f32_16x16x32_bf16 v[126:129], v[186:189], v[234:237], v[126:129]
	v_mfma_f32_16x16x32_bf16 v[18:21], v[190:193], v[206:209], v[18:21]
	v_mfma_f32_16x16x32_bf16 v[26:29], v[198:201], v[206:209], v[26:29]
	v_mfma_f32_16x16x32_bf16 v[42:45], v[190:193], v[214:217], v[42:45]
	v_mfma_f32_16x16x32_bf16 v[50:53], v[198:201], v[214:217], v[50:53]
	v_mfma_f32_16x16x32_bf16 v[74:77], v[190:193], v[222:225], v[74:77]
	v_mfma_f32_16x16x32_bf16 v[82:85], v[198:201], v[222:225], v[82:85]
	v_mfma_f32_16x16x32_bf16 v[122:125], v[190:193], v[230:233], v[122:125]
	v_mfma_f32_16x16x32_bf16 v[118:121], v[198:201], v[230:233], v[118:121]
	v_mfma_f32_16x16x32_bf16 v[18:21], v[194:197], v[210:213], v[18:21]
	v_mfma_f32_16x16x32_bf16 v[26:29], v[202:205], v[210:213], v[26:29]
	v_mfma_f32_16x16x32_bf16 v[42:45], v[194:197], v[218:221], v[42:45]
	v_mfma_f32_16x16x32_bf16 v[50:53], v[202:205], v[218:221], v[50:53]
	v_mfma_f32_16x16x32_bf16 v[74:77], v[194:197], v[226:229], v[74:77]
	v_mfma_f32_16x16x32_bf16 v[82:85], v[202:205], v[226:229], v[82:85]
	v_mfma_f32_16x16x32_bf16 v[122:125], v[194:197], v[234:237], v[122:125]
	v_mfma_f32_16x16x32_bf16 v[118:121], v[202:205], v[234:237], v[118:121]
	s_setprio 0
	s_barrier
	s_add_i32 s7, s7, 2
	s_add_u32 s70, s70, 0x100
	s_addc_u32 s71, s71, 0
	s_cmp_gt_u32 s7, 13
	s_cbranch_scc0 .LBB0_437
	s_and_b64 vcc, exec, s[42:43]
	s_cbranch_vccz .LBB0_440
	s_barrier

; #define PG8_STAGE(bufoff, gbase, voff) do { _Pragma("unroll") for (int _i = 0; _i < 2; ++_i) \
;         __builtin_amdgcn_global_load_lds((const unsigned*)((const char*)(gbase) + (voff)[_i]), (PG8_LAS unsigned*)(lds + (bufoff) + ldsw + _i * 8192), 16, 0, 0); } while (0)
; #define PG8_LDA(dst, b, h) do { _Pragma("unroll") for (int m = 0; m < 4; ++m) Frag<F8>::load(dst[m], lds + PG8_SA(b, h) + aoff + m * 2048); } while (0)
; #define PG8_LDB(dst, b, h) do { _Pragma("unroll") for (int n = 0; n < 2; ++n) Frag<F8>::load(dst[n], lds + PG8_SB(b, h) + boff + n * 2048); } while (0)
; #define PG8_MMA(ai, bj, At, Bt) do { __builtin_amdgcn_s_setprio(3); _Pragma("unroll") for (int m = 0; m < 4; ++m) _Pragma("unroll") for (int n = 0; n < 2; ++n) Frag<F8>::mma(acc[ai][bj][m][n], Bt[n], At[m]); \
;         __builtin_amdgcn_s_setprio(0); } while (0)
; #define PG8_WAIT_V(n) asm volatile("s_waitcnt vmcnt(" #n ")" ::: "memory")
; #define PG8_BAR __builtin_amdgcn_s_barrier()
; template <class Epi, class Sched, bool ALIGN_EPI = false, bool SP2 = false, bool F8 = false>
; __device__ __forceinline__ void gemm_phase(PG8_LAS unsigned char* lds, const Gemm g, const Sched& S, const Epi& E) {
;     ...
;         const bool has_next = S.next(ui + 1, nxt);
;         const char* nA = has_next ? (const char*)g.A + (size_t)nxt.pm * tstep + nxt.ko : cA; const char* nB = has_next ? (const char*)g.Bt + (size_t)nxt.pn * tstep + nxt.ko : cB;
;         for (int t = 0; t < nt; t += 2) {
;             const bool last = (t == nt - 2);
;             const char* a1 = cA + (size_t)(t + 1) * kstep;
;             const char* a2 = last ? nA : cA + (size_t)(t + 2) * kstep; const char* b2 = last ? nB : cB + (size_t)(t + 2) * kstep;
;             const char* a3 = a2 + kstep; const char* b3 = b2 + kstep;
;             if (last && has_next) S.a_ready(nxt);
;             if constexpr (SP2) {
;             PG8_LDB(B0, 0, 0); PG8_LDB(B1, 0, 1); PG8_SCHED; PG8_LDA(At, 0, 0); PG8_STAGE(PG8_SA(1, 1), a1 + hstep, voffA);
;             PG8_WAIT_V(8); PG8_WAIT_L(0); PG8_BAR; PG8_MMA(0, 0, At, B0); PG8_MMA(0, 1, At, B1); PG8_BAR; PG8_SCHED;
;             PG8_LDA(At, 0, 1); PG8_STAGE(PG8_SB(0, 0), b2, voffB); PG8_STAGE(PG8_SB(0, 1), b2 + hstep, voffB); PG8_STAGE(PG8_SA(0, 0), a2, voffA);
;             PG8_WAIT_V(8); PG8_WAIT_L(0); PG8_BAR; PG8_MMA(1, 0, At, B0); PG8_MMA(1, 1, At, B1); PG8_BAR; PG8_SCHED;
.LBB0_561:
	s_ashr_i32 s25, s24, 31
	s_lshl_b64 s[4:5], s[24:25], 19
	s_add_u32 s36, s50, s4
	s_addc_u32 s37, s51, s5
	s_and_b64 s[4:5], s[8:9], exec
	s_cselect_b32 s6, s37, s43
	s_cselect_b32 s7, s36, s42
	s_ashr_i32 s31, s30, 31
	s_lshl_b64 s[4:5], s[30:31], 19
	s_add_u32 s38, s52, s4
	s_addc_u32 s39, s53, s5
	s_and_b64 s[4:5], s[8:9], exec
	s_cselect_b32 s25, s39, s45
	s_cselect_b32 s31, s38, s44
	s_add_u32 s42, s42, 0x40080
	s_addc_u32 s43, s43, 0
	s_add_u32 s84, s44, 0x100
	s_addc_u32 s85, s45, 0
	s_mov_b32 s86, -2
	ds_read_b128 v[146:149], v155
	ds_read_b128 v[158:161], v155 offset:1024
	ds_read_b128 v[166:169], v155 offset:2048
	ds_read_b128 v[170:173], v155 offset:3072
	ds_read_b128 v[174:177], v156
	ds_read_b128 v[178:181], v156 offset:1024
	ds_read_b128 v[182:185], v156 offset:2048
	ds_read_b128 v[186:189], v156 offset:3072
	s_add_u32 s0, s42, 0xfffc0080
	s_addc_u32 s1, s43, -1
	s_cmp_eq_u32 s86, 12
	s_cselect_b32 s47, s6, s1
	s_cselect_b32 s46, s7, s0
	s_cselect_b32 s45, s25, s85
	s_cselect_b32 s44, s31, s84
	v_lshl_add_u64 v[222:223], s[42:43], 0, v[138:139]
	s_add_i32 m0, s41, 0xc000
	ds_read_b128 v[190:193], v157
	ds_read_b128 v[194:197], v157 offset:1024
	ds_read_b128 v[198:201], v157 offset:2048
	ds_read_b128 v[202:205], v157 offset:3072
	ds_read_b128 v[206:209], v157 offset:4096
	ds_read_b128 v[210:213], v157 offset:5120
	ds_read_b128 v[214:217], v157 offset:6144
	ds_read_b128 v[218:221], v157 offset:7168
	global_load_lds_dwordx4 v[222:223], off
	v_lshl_add_u64 v[222:223], s[42:43], 0, v[140:141]
	s_add_i32 m0, s41, 0xe000
	s_nop 0
	global_load_lds_dwordx4 v[222:223], off
	s_waitcnt vmcnt(8)
	s_waitcnt lgkmcnt(0)
	s_barrier
	s_setprio 3
	s_waitcnt lgkmcnt(0)
	v_mfma_f32_16x16x32_bf16 v[126:129], v[146:149], v[190:193], 0
	v_mfma_f32_16x16x32_bf16 v[118:121], v[166:169], v[190:193], 0
	v_mfma_f32_16x16x32_bf16 v[110:113], v[146:149], v[198:201], 0
	v_mfma_f32_16x16x32_bf16 v[102:105], v[166:169], v[198:201], 0
	v_mfma_f32_16x16x32_bf16 v[94:97], v[146:149], v[206:209], 0
	v_mfma_f32_16x16x32_bf16 v[86:89], v[166:169], v[206:209], 0
	v_mfma_f32_16x16x32_bf16 v[78:81], v[146:149], v[214:217], 0
	v_mfma_f32_16x16x32_bf16 v[70:73], v[166:169], v[214:217], 0
	v_mfma_f32_16x16x32_bf16 v[126:129], v[158:161], v[194:197], v[126:129]
	v_mfma_f32_16x16x32_bf16 v[118:121], v[170:173], v[194:197], v[118:121]
	v_mfma_f32_16x16x32_bf16 v[110:113], v[158:161], v[202:205], v[110:113]
	v_mfma_f32_16x16x32_bf16 v[102:105], v[170:173], v[202:205], v[102:105]
	v_mfma_f32_16x16x32_bf16 v[94:97], v[158:161], v[210:213], v[94:97]
	v_mfma_f32_16x16x32_bf16 v[86:89], v[170:173], v[210:213], v[86:89]
	v_mfma_f32_16x16x32_bf16 v[78:81], v[158:161], v[218:221], v[78:81]
	v_mfma_f32_16x16x32_bf16 v[70:73], v[170:173], v[218:221], v[70:73]
	v_mfma_f32_16x16x32_bf16 v[122:125], v[174:177], v[190:193], 0
	v_mfma_f32_16x16x32_bf16 v[114:117], v[182:185], v[190:193], 0
	v_mfma_f32_16x16x32_bf16 v[106:109], v[174:177], v[198:201], 0
	v_mfma_f32_16x16x32_bf16 v[98:101], v[182:185], v[198:201], 0
	v_mfma_f32_16x16x32_bf16 v[90:93], v[174:177], v[206:209], 0
	v_mfma_f32_16x16x32_bf16 v[82:85], v[182:185], v[206:209], 0
	v_mfma_f32_16x16x32_bf16 v[74:77], v[174:177], v[214:217], 0
	v_mfma_f32_16x16x32_bf16 v[66:69], v[182:185], v[214:217], 0
	v_mfma_f32_16x16x32_bf16 v[122:125], v[178:181], v[194:197], v[122:125]
	v_mfma_f32_16x16x32_bf16 v[114:117], v[186:189], v[194:197], v[114:117]
	v_mfma_f32_16x16x32_bf16 v[106:109], v[178:181], v[202:205], v[106:109]
	v_mfma_f32_16x16x32_bf16 v[98:101], v[186:189], v[202:205], v[98:101]
	v_mfma_f32_16x16x32_bf16 v[90:93], v[178:181], v[210:213], v[90:93]
	v_mfma_f32_16x16x32_bf16 v[82:85], v[186:189], v[210:213], v[82:85]
	v_mfma_f32_16x16x32_bf16 v[74:77], v[178:181], v[218:221], v[74:77]
	v_mfma_f32_16x16x32_bf16 v[66:69], v[186:189], v[218:221], v[66:69]
	s_setprio 0
	s_barrier
	s_add_i32 s0, s80, s49
	v_lshl_add_u64 v[222:223], s[44:45], 0, v[134:135]
	s_mov_b32 m0, s0
	ds_read_b128 v[190:193], v157 offset:16384
	ds_read_b128 v[194:197], v157 offset:17408
	ds_read_b128 v[198:201], v157 offset:18432
	ds_read_b128 v[202:205], v157 offset:19456
	ds_read_b128 v[206:209], v157 offset:20480
	ds_read_b128 v[210:213], v157 offset:21504
	ds_read_b128 v[214:217], v157 offset:22528
	ds_read_b128 v[218:221], v157 offset:23552
	global_load_lds_dwordx4 v[222:223], off
	s_add_i32 m0, s0, 0x2000
	s_add_u32 s4, s44, 0x40000
	v_lshl_add_u64 v[224:225], s[44:45], 0, v[130:131]
	s_addc_u32 s5, s45, 0
	s_add_i32 s0, s81, s49
	global_load_lds_dwordx4 v[224:225], off
	v_lshl_add_u64 v[226:227], s[4:5], 0, v[134:135]
	s_mov_b32 m0, s0
	v_lshl_add_u64 v[228:229], s[46:47], 0, v[132:133]
	global_load_lds_dwordx4 v[226:227], off
	v_lshl_add_u64 v[226:227], s[4:5], 0, v[130:131]
	s_add_i32 m0, s0, 0x2000
	s_nop 0
	global_load_lds_dwordx4 v[226:227], off
	v_lshl_add_u64 v[226:227], s[46:47], 0, v[136:137]
	s_mov_b32 m0, s41
	s_nop 0
	global_load_lds_dwordx4 v[226:227], off
	s_mov_b32 m0, s72
	s_nop 0
	global_load_lds_dwordx4 v[228:229], off
	s_waitcnt vmcnt(8)
	s_waitcnt lgkmcnt(0)
	s_barrier
; #define PG8_STAGE(bufoff, gbase, voff) do { _Pragma("unroll") for (int _i = 0; _i < 2; ++_i) \
;         __builtin_amdgcn_global_load_lds((const unsigned*)((const char*)(gbase) + (voff)[_i]), (PG8_LAS unsigned*)(lds + (bufoff) + ldsw + _i * 8192), 16, 0, 0); } while (0)
; #define PG8_LDA(dst, b, h) do { _Pragma("unroll") for (int m = 0; m < 4; ++m) Frag<F8>::load(dst[m], lds + PG8_SA(b, h) + aoff + m * 2048); } while (0)
; #define PG8_LDB(dst, b, h) do { _Pragma("unroll") for (int n = 0; n < 2; ++n) Frag<F8>::load(dst[n], lds + PG8_SB(b, h) + boff + n * 2048); } while (0)
; #define PG8_MMA(ai, bj, At, Bt) do { __builtin_amdgcn_s_setprio(3); _Pragma("unroll") for (int m = 0; m < 4; ++m) _Pragma("unroll") for (int n = 0; n < 2; ++n) Frag<F8>::mma(acc[ai][bj][m][n], Bt[n], At[m]); \
;         __builtin_amdgcn_s_setprio(0); } while (0)
; #define PG8_WAIT_V(n) asm volatile("s_waitcnt vmcnt(" #n ")" ::: "memory")
; #define PG8_WAIT_L(n) asm volatile("s_waitcnt lgkmcnt(" #n ")" ::: "memory")
; #define PG8_BAR __builtin_amdgcn_s_barrier()
; #define PG8_SCHED __builtin_amdgcn_sched_barrier(0)
; template <class Epi, class Sched, bool ALIGN_EPI = false, bool SP2 = false, bool F8 = false>
; __device__ __forceinline__ void gemm_phase(PG8_LAS unsigned char* lds, const Gemm g, const Sched& S, const Epi& E) {
;     ...
;             PG8_WAIT_V(8); PG8_WAIT_L(0); PG8_BAR; PG8_MMA(1, 0, At, B0); PG8_MMA(1, 1, At, B1); PG8_BAR; PG8_SCHED;
;             PG8_LDB(B0, 1, 0); PG8_LDB(B1, 1, 1); PG8_SCHED; PG8_LDA(At, 1, 0); PG8_STAGE(PG8_SA(0, 1), a2 + hstep, voffA);
;             PG8_WAIT_V(8); PG8_WAIT_L(0); PG8_BAR; PG8_MMA(0, 0, At, B0); PG8_MMA(0, 1, At, B1); PG8_BAR; PG8_SCHED;
	s_setprio 3
	s_waitcnt lgkmcnt(0)
	v_mfma_f32_16x16x32_bf16 v[62:65], v[146:149], v[190:193], 0
	v_mfma_f32_16x16x32_bf16 v[58:61], v[166:169], v[190:193], 0
	v_mfma_f32_16x16x32_bf16 v[50:53], v[146:149], v[198:201], 0
	v_mfma_f32_16x16x32_bf16 v[42:45], v[166:169], v[198:201], 0
	v_mfma_f32_16x16x32_bf16 v[34:37], v[146:149], v[206:209], 0
	v_mfma_f32_16x16x32_bf16 v[26:29], v[166:169], v[206:209], 0
	v_mfma_f32_16x16x32_bf16 v[14:17], v[146:149], v[214:217], 0
	v_mfma_f32_16x16x32_bf16 v[6:9], v[166:169], v[214:217], 0
	v_mfma_f32_16x16x32_bf16 v[62:65], v[158:161], v[194:197], v[62:65]
	v_mfma_f32_16x16x32_bf16 v[58:61], v[170:173], v[194:197], v[58:61]
	v_mfma_f32_16x16x32_bf16 v[50:53], v[158:161], v[202:205], v[50:53]
	v_mfma_f32_16x16x32_bf16 v[42:45], v[170:173], v[202:205], v[42:45]
	v_mfma_f32_16x16x32_bf16 v[34:37], v[158:161], v[210:213], v[34:37]
	v_mfma_f32_16x16x32_bf16 v[26:29], v[170:173], v[210:213], v[26:29]
	v_mfma_f32_16x16x32_bf16 v[14:17], v[158:161], v[218:221], v[14:17]
	v_mfma_f32_16x16x32_bf16 v[6:9], v[170:173], v[218:221], v[6:9]
	v_mfma_f32_16x16x32_bf16 v[54:57], v[174:177], v[190:193], 0
	v_mfma_f32_16x16x32_bf16 v[46:49], v[182:185], v[190:193], 0
	v_mfma_f32_16x16x32_bf16 v[38:41], v[174:177], v[198:201], 0
	v_mfma_f32_16x16x32_bf16 v[30:33], v[182:185], v[198:201], 0
	v_mfma_f32_16x16x32_bf16 v[22:25], v[174:177], v[206:209], 0
	v_mfma_f32_16x16x32_bf16 v[18:21], v[182:185], v[206:209], 0
	v_mfma_f32_16x16x32_bf16 v[10:13], v[174:177], v[214:217], 0
	v_mfma_f32_16x16x32_bf16 v[2:5], v[182:185], v[214:217], 0
	v_mfma_f32_16x16x32_bf16 v[54:57], v[178:181], v[194:197], v[54:57]
	v_mfma_f32_16x16x32_bf16 v[46:49], v[186:189], v[194:197], v[46:49]
	v_mfma_f32_16x16x32_bf16 v[38:41], v[178:181], v[202:205], v[38:41]
	v_mfma_f32_16x16x32_bf16 v[30:33], v[186:189], v[202:205], v[30:33]
	v_mfma_f32_16x16x32_bf16 v[22:25], v[178:181], v[210:213], v[22:25]
	v_mfma_f32_16x16x32_bf16 v[18:21], v[186:189], v[210:213], v[18:21]
	v_mfma_f32_16x16x32_bf16 v[10:13], v[178:181], v[218:221], v[10:13]
	v_mfma_f32_16x16x32_bf16 v[2:5], v[186:189], v[218:221], v[2:5]
	s_setprio 0
	s_barrier
	s_add_i32 s0, 0, 0x18000
	v_add_u32_e32 v165, s0, v151
	s_add_i32 s1, 0, 0x1c000
	ds_read_b128 v[146:149], v165
	ds_read_b128 v[158:161], v165 offset:1024
	ds_read_b128 v[166:169], v165 offset:2048
	ds_read_b128 v[170:173], v165 offset:3072
	v_add_u32_e32 v165, s1, v151
	ds_read_b128 v[174:177], v165
	ds_read_b128 v[178:181], v165 offset:1024
	ds_read_b128 v[182:185], v165 offset:2048
	ds_read_b128 v[186:189], v165 offset:3072
	s_add_u32 s4, s46, 0x40000
	s_addc_u32 s5, s47, 0
	s_mov_b32 m0, s73
	v_lshl_add_u64 v[230:231], s[4:5], 0, v[136:137]
	ds_read_b128 v[190:193], v157 offset:32768
	ds_read_b128 v[194:197], v157 offset:33792
	ds_read_b128 v[198:201], v157 offset:34816
	ds_read_b128 v[202:205], v157 offset:35840
	ds_read_b128 v[206:209], v157 offset:36864
	ds_read_b128 v[210:213], v157 offset:37888
	ds_read_b128 v[214:217], v157 offset:38912
	ds_read_b128 v[218:221], v157 offset:39936
	global_load_lds_dwordx4 v[230:231], off
	v_lshl_add_u64 v[230:231], s[4:5], 0, v[132:133]
	s_mov_b32 m0, s74
	s_nop 0
	global_load_lds_dwordx4 v[230:231], off
	s_waitcnt vmcnt(8)
	s_waitcnt lgkmcnt(0)
	s_barrier
	s_setprio 3
	s_waitcnt lgkmcnt(0)
	v_mfma_f32_16x16x32_bf16 v[126:129], v[146:149], v[190:193], v[126:129]
	v_mfma_f32_16x16x32_bf16 v[118:121], v[166:169], v[190:193], v[118:121]
	v_mfma_f32_16x16x32_bf16 v[110:113], v[146:149], v[198:201], v[110:113]
	v_mfma_f32_16x16x32_bf16 v[102:105], v[166:169], v[198:201], v[102:105]
	v_mfma_f32_16x16x32_bf16 v[94:97], v[146:149], v[206:209], v[94:97]
	v_mfma_f32_16x16x32_bf16 v[86:89], v[166:169], v[206:209], v[86:89]
	v_mfma_f32_16x16x32_bf16 v[78:81], v[146:149], v[214:217], v[78:81]
	v_mfma_f32_16x16x32_bf16 v[70:73], v[166:169], v[214:217], v[70:73]
	v_mfma_f32_16x16x32_bf16 v[126:129], v[158:161], v[194:197], v[126:129]
	v_mfma_f32_16x16x32_bf16 v[118:121], v[170:173], v[194:197], v[118:121]
	v_mfma_f32_16x16x32_bf16 v[110:113], v[158:161], v[202:205], v[110:113]
	v_mfma_f32_16x16x32_bf16 v[102:105], v[170:173], v[202:205], v[102:105]
	v_mfma_f32_16x16x32_bf16 v[94:97], v[158:161], v[210:213], v[94:97]
	v_mfma_f32_16x16x32_bf16 v[86:89], v[170:173], v[210:213], v[86:89]
	v_mfma_f32_16x16x32_bf16 v[78:81], v[158:161], v[218:221], v[78:81]
	v_mfma_f32_16x16x32_bf16 v[70:73], v[170:173], v[218:221], v[70:73]
	v_mfma_f32_16x16x32_bf16 v[122:125], v[174:177], v[190:193], v[122:125]
	v_mfma_f32_16x16x32_bf16 v[114:117], v[182:185], v[190:193], v[114:117]
	v_mfma_f32_16x16x32_bf16 v[106:109], v[174:177], v[198:201], v[106:109]
	v_mfma_f32_16x16x32_bf16 v[98:101], v[182:185], v[198:201], v[98:101]
	v_mfma_f32_16x16x32_bf16 v[90:93], v[174:177], v[206:209], v[90:93]
	v_mfma_f32_16x16x32_bf16 v[82:85], v[182:185], v[206:209], v[82:85]
	v_mfma_f32_16x16x32_bf16 v[74:77], v[174:177], v[214:217], v[74:77]
	v_mfma_f32_16x16x32_bf16 v[66:69], v[182:185], v[214:217], v[66:69]
	v_mfma_f32_16x16x32_bf16 v[122:125], v[178:181], v[194:197], v[122:125]
	v_mfma_f32_16x16x32_bf16 v[114:117], v[186:189], v[194:197], v[114:117]
	v_mfma_f32_16x16x32_bf16 v[106:109], v[178:181], v[202:205], v[106:109]
	v_mfma_f32_16x16x32_bf16 v[98:101], v[186:189], v[202:205], v[98:101]
	v_mfma_f32_16x16x32_bf16 v[90:93], v[178:181], v[210:213], v[90:93]
	v_mfma_f32_16x16x32_bf16 v[82:85], v[186:189], v[210:213], v[82:85]
	v_mfma_f32_16x16x32_bf16 v[74:77], v[178:181], v[218:221], v[74:77]
	v_mfma_f32_16x16x32_bf16 v[66:69], v[186:189], v[218:221], v[66:69]
	s_setprio 0
	s_barrier
; #define PG8_STAGE(bufoff, gbase, voff) do { _Pragma("unroll") for (int _i = 0; _i < 2; ++_i) \
;         __builtin_amdgcn_global_load_lds((const unsigned*)((const char*)(gbase) + (voff)[_i]), (PG8_LAS unsigned*)(lds + (bufoff) + ldsw + _i * 8192), 16, 0, 0); } while (0)
; #define PG8_LDA(dst, b, h) do { _Pragma("unroll") for (int m = 0; m < 4; ++m) Frag<F8>::load(dst[m], lds + PG8_SA(b, h) + aoff + m * 2048); } while (0)
; #define PG8_LDB(dst, b, h) do { _Pragma("unroll") for (int n = 0; n < 2; ++n) Frag<F8>::load(dst[n], lds + PG8_SB(b, h) + boff + n * 2048); } while (0)
; #define PG8_MMA(ai, bj, At, Bt) do { __builtin_amdgcn_s_setprio(3); _Pragma("unroll") for (int m = 0; m < 4; ++m) _Pragma("unroll") for (int n = 0; n < 2; ++n) Frag<F8>::mma(acc[ai][bj][m][n], Bt[n], At[m]); \
;         __builtin_amdgcn_s_setprio(0); } while (0)
; #define PG8_WAIT_V(n) asm volatile("s_waitcnt vmcnt(" #n ")" ::: "memory")
; #define PG8_WAIT_L(n) asm volatile("s_waitcnt lgkmcnt(" #n ")" ::: "memory")
; #define PG8_BAR __builtin_amdgcn_s_barrier()
; #define PG8_SCHED __builtin_amdgcn_sched_barrier(0)
; template <class Epi, class Sched, bool ALIGN_EPI = false, bool SP2 = false, bool F8 = false>
; __device__ __forceinline__ void gemm_phase(PG8_LAS unsigned char* lds, const Gemm g, const Sched& S, const Epi& E) {
;     ...
;             PG8_LDB(B0, 0, 0); PG8_LDB(B1, 0, 1); PG8_SCHED; PG8_LDA(At, 0, 0); PG8_STAGE(PG8_SA(1, 1), a1 + hstep, voffA);
;             PG8_WAIT_V(8); PG8_WAIT_L(0); PG8_BAR; PG8_MMA(0, 0, At, B0); PG8_MMA(0, 1, At, B1); PG8_BAR; PG8_SCHED;
;             PG8_LDA(At, 0, 1); PG8_STAGE(PG8_SB(0, 0), b2, voffB); PG8_STAGE(PG8_SB(0, 1), b2 + hstep, voffB); PG8_STAGE(PG8_SA(0, 0), a2, voffA);
;             PG8_WAIT_V(8); PG8_WAIT_L(0); PG8_BAR; PG8_MMA(1, 0, At, B0); PG8_MMA(1, 1, At, B1); PG8_BAR; PG8_SCHED;
;             PG8_LDB(B0, 1, 0); PG8_LDB(B1, 1, 1); PG8_SCHED; PG8_LDA(At, 1, 0); PG8_STAGE(PG8_SA(0, 1), a2 + hstep, voffA);
;             PG8_WAIT_V(8); PG8_WAIT_L(0); PG8_BAR; PG8_MMA(0, 0, At, B0); PG8_MMA(0, 1, At, B1); PG8_BAR; PG8_SCHED;
;             PG8_LDA(At, 1, 1); PG8_STAGE(PG8_SB(1, 0), b3, voffB); PG8_STAGE(PG8_SB(1, 1), b3 + hstep, voffB); PG8_STAGE(PG8_SA(1, 0), a3, voffA);
;             PG8_WAIT_V(8); PG8_WAIT_L(0); PG8_BAR; PG8_MMA(1, 0, At, B0); PG8_MMA(1, 1, At, B1); PG8_BAR; PG8_SCHED;
	s_add_i32 s0, s0, s49
	v_lshl_add_u64 v[222:223], v[222:223], 0, s[18:19]
	s_mov_b32 m0, s0
	ds_read_b128 v[190:193], v157 offset:49152
	ds_read_b128 v[194:197], v157 offset:50176
	ds_read_b128 v[198:201], v157 offset:51200
	ds_read_b128 v[202:205], v157 offset:52224
	ds_read_b128 v[206:209], v157 offset:53248
	ds_read_b128 v[210:213], v157 offset:54272
	ds_read_b128 v[214:217], v157 offset:55296
	ds_read_b128 v[218:221], v157 offset:56320
	global_load_lds_dwordx4 v[222:223], off
	s_add_i32 m0, s0, 0x2000
	s_add_u32 s4, s44, 0x40080
	v_lshl_add_u64 v[222:223], v[224:225], 0, s[18:19]
	s_addc_u32 s5, s45, 0
	s_add_i32 s0, s1, s49
	global_load_lds_dwordx4 v[222:223], off
	v_lshl_add_u64 v[222:223], s[4:5], 0, v[134:135]
	s_mov_b32 m0, s0
	s_nop 0
	global_load_lds_dwordx4 v[222:223], off
	v_lshl_add_u64 v[222:223], s[4:5], 0, v[130:131]
	s_add_i32 m0, s0, 0x2000
	s_nop 0
	global_load_lds_dwordx4 v[222:223], off
	v_lshl_add_u64 v[222:223], v[226:227], 0, s[18:19]
	s_mov_b32 m0, s75
	s_nop 0
	global_load_lds_dwordx4 v[222:223], off
	v_lshl_add_u64 v[222:223], v[228:229], 0, s[18:19]
	s_mov_b32 m0, s79
	s_nop 0
	global_load_lds_dwordx4 v[222:223], off
	s_waitcnt vmcnt(8)
	s_waitcnt lgkmcnt(0)
	s_barrier
	s_setprio 3
	s_waitcnt lgkmcnt(0)
	v_mfma_f32_16x16x32_bf16 v[62:65], v[146:149], v[190:193], v[62:65]
	v_mfma_f32_16x16x32_bf16 v[58:61], v[166:169], v[190:193], v[58:61]
	v_mfma_f32_16x16x32_bf16 v[50:53], v[146:149], v[198:201], v[50:53]
	v_mfma_f32_16x16x32_bf16 v[42:45], v[166:169], v[198:201], v[42:45]
	v_mfma_f32_16x16x32_bf16 v[34:37], v[146:149], v[206:209], v[34:37]
	v_mfma_f32_16x16x32_bf16 v[26:29], v[166:169], v[206:209], v[26:29]
	v_mfma_f32_16x16x32_bf16 v[14:17], v[146:149], v[214:217], v[14:17]
	v_mfma_f32_16x16x32_bf16 v[6:9], v[166:169], v[214:217], v[6:9]
	v_mfma_f32_16x16x32_bf16 v[62:65], v[158:161], v[194:197], v[62:65]
	v_mfma_f32_16x16x32_bf16 v[58:61], v[170:173], v[194:197], v[58:61]
	v_mfma_f32_16x16x32_bf16 v[50:53], v[158:161], v[202:205], v[50:53]
	v_mfma_f32_16x16x32_bf16 v[42:45], v[170:173], v[202:205], v[42:45]
	v_mfma_f32_16x16x32_bf16 v[34:37], v[158:161], v[210:213], v[34:37]
	v_mfma_f32_16x16x32_bf16 v[26:29], v[170:173], v[210:213], v[26:29]
	v_mfma_f32_16x16x32_bf16 v[14:17], v[158:161], v[218:221], v[14:17]
	v_mfma_f32_16x16x32_bf16 v[6:9], v[170:173], v[218:221], v[6:9]
	v_mfma_f32_16x16x32_bf16 v[54:57], v[174:177], v[190:193], v[54:57]
	v_mfma_f32_16x16x32_bf16 v[46:49], v[182:185], v[190:193], v[46:49]
	v_mfma_f32_16x16x32_bf16 v[38:41], v[174:177], v[198:201], v[38:41]
	v_mfma_f32_16x16x32_bf16 v[30:33], v[182:185], v[198:201], v[30:33]
	v_mfma_f32_16x16x32_bf16 v[22:25], v[174:177], v[206:209], v[22:25]
	v_mfma_f32_16x16x32_bf16 v[18:21], v[182:185], v[206:209], v[18:21]
	v_mfma_f32_16x16x32_bf16 v[10:13], v[174:177], v[214:217], v[10:13]
	v_mfma_f32_16x16x32_bf16 v[2:5], v[182:185], v[214:217], v[2:5]
	v_mfma_f32_16x16x32_bf16 v[54:57], v[178:181], v[194:197], v[54:57]
	v_mfma_f32_16x16x32_bf16 v[46:49], v[186:189], v[194:197], v[46:49]
	v_mfma_f32_16x16x32_bf16 v[38:41], v[178:181], v[202:205], v[38:41]
	v_mfma_f32_16x16x32_bf16 v[30:33], v[186:189], v[202:205], v[30:33]
	v_mfma_f32_16x16x32_bf16 v[22:25], v[178:181], v[210:213], v[22:25]
	v_mfma_f32_16x16x32_bf16 v[18:21], v[186:189], v[210:213], v[18:21]
	v_mfma_f32_16x16x32_bf16 v[10:13], v[178:181], v[218:221], v[10:13]
	v_mfma_f32_16x16x32_bf16 v[2:5], v[186:189], v[218:221], v[2:5]
	s_setprio 0
	s_barrier
	s_add_i32 s86, s86, 2
	s_add_u32 s42, s42, 0x100
	s_addc_u32 s43, s43, 0
	s_add_u32 s84, s84, 0x100
	s_addc_u32 s85, s85, 0
	s_cmp_gt_u32 s86, 13
	s_cbranch_scc1 .Lpeel_exit_1
.LBB0_562:
	ds_read_b128 v[146:149], v155
	ds_read_b128 v[158:161], v155 offset:1024
	ds_read_b128 v[166:169], v155 offset:2048
	ds_read_b128 v[170:173], v155 offset:3072
	ds_read_b128 v[174:177], v156
	ds_read_b128 v[178:181], v156 offset:1024
	ds_read_b128 v[182:185], v156 offset:2048
	ds_read_b128 v[186:189], v156 offset:3072
	s_add_u32 s0, s42, 0xfffc0080
	s_addc_u32 s1, s43, -1
	s_cmp_eq_u32 s86, 12
	s_cselect_b32 s47, s6, s1
	s_cselect_b32 s46, s7, s0
	s_cselect_b32 s45, s25, s85
	s_cselect_b32 s44, s31, s84
	v_lshl_add_u64 v[222:223], s[42:43], 0, v[138:139]
	s_add_i32 m0, s41, 0xc000
	ds_read_b128 v[190:193], v157
	ds_read_b128 v[194:197], v157 offset:1024
	ds_read_b128 v[198:201], v157 offset:2048
	ds_read_b128 v[202:205], v157 offset:3072
	ds_read_b128 v[206:209], v157 offset:4096
	ds_read_b128 v[210:213], v157 offset:5120
	ds_read_b128 v[214:217], v157 offset:6144
	ds_read_b128 v[218:221], v157 offset:7168
	global_load_lds_dwordx4 v[222:223], off
	v_lshl_add_u64 v[222:223], s[42:43], 0, v[140:141]
	s_add_i32 m0, s41, 0xe000
	s_nop 0
	global_load_lds_dwordx4 v[222:223], off
	s_waitcnt vmcnt(8)
	s_waitcnt lgkmcnt(0)
	s_barrier
; #define PG8_STAGE(bufoff, gbase, voff) do { _Pragma("unroll") for (int _i = 0; _i < 2; ++_i) \
;         __builtin_amdgcn_global_load_lds((const unsigned*)((const char*)(gbase) + (voff)[_i]), (PG8_LAS unsigned*)(lds + (bufoff) + ldsw + _i * 8192), 16, 0, 0); } while (0)
; #define PG8_LDA(dst, b, h) do { _Pragma("unroll") for (int m = 0; m < 4; ++m) Frag<F8>::load(dst[m], lds + PG8_SA(b, h) + aoff + m * 2048); } while (0)
; #define PG8_MMA(ai, bj, At, Bt) do { __builtin_amdgcn_s_setprio(3); _Pragma("unroll") for (int m = 0; m < 4; ++m) _Pragma("unroll") for (int n = 0; n < 2; ++n) Frag<F8>::mma(acc[ai][bj][m][n], Bt[n], At[m]); \
;         __builtin_amdgcn_s_setprio(0); } while (0)
; #define PG8_WAIT_V(n) asm volatile("s_waitcnt vmcnt(" #n ")" ::: "memory")
; #define PG8_WAIT_L(n) asm volatile("s_waitcnt lgkmcnt(" #n ")" ::: "memory")
; #define PG8_BAR __builtin_amdgcn_s_barrier()
; #define PG8_SCHED __builtin_amdgcn_sched_barrier(0)
; template <class Epi, class Sched, bool ALIGN_EPI = false, bool SP2 = false, bool F8 = false>
; __device__ __forceinline__ void gemm_phase(PG8_LAS unsigned char* lds, const Gemm g, const Sched& S, const Epi& E) {
;     ...
;             PG8_WAIT_V(8); PG8_WAIT_L(0); PG8_BAR; PG8_MMA(0, 0, At, B0); PG8_MMA(0, 1, At, B1); PG8_BAR; PG8_SCHED;
;             PG8_LDA(At, 0, 1); PG8_STAGE(PG8_SB(0, 0), b2, voffB); PG8_STAGE(PG8_SB(0, 1), b2 + hstep, voffB); PG8_STAGE(PG8_SA(0, 0), a2, voffA);
;             PG8_WAIT_V(8); PG8_WAIT_L(0); PG8_BAR; PG8_MMA(1, 0, At, B0); PG8_MMA(1, 1, At, B1); PG8_BAR; PG8_SCHED;
	s_setprio 3
	s_waitcnt lgkmcnt(0)
	v_mfma_f32_16x16x32_bf16 v[126:129], v[146:149], v[190:193], v[126:129]
	v_mfma_f32_16x16x32_bf16 v[118:121], v[166:169], v[190:193], v[118:121]
	v_mfma_f32_16x16x32_bf16 v[110:113], v[146:149], v[198:201], v[110:113]
	v_mfma_f32_16x16x32_bf16 v[102:105], v[166:169], v[198:201], v[102:105]
	v_mfma_f32_16x16x32_bf16 v[94:97], v[146:149], v[206:209], v[94:97]
	v_mfma_f32_16x16x32_bf16 v[86:89], v[166:169], v[206:209], v[86:89]
	v_mfma_f32_16x16x32_bf16 v[78:81], v[146:149], v[214:217], v[78:81]
	v_mfma_f32_16x16x32_bf16 v[70:73], v[166:169], v[214:217], v[70:73]
	v_mfma_f32_16x16x32_bf16 v[126:129], v[158:161], v[194:197], v[126:129]
	v_mfma_f32_16x16x32_bf16 v[118:121], v[170:173], v[194:197], v[118:121]
	v_mfma_f32_16x16x32_bf16 v[110:113], v[158:161], v[202:205], v[110:113]
	v_mfma_f32_16x16x32_bf16 v[102:105], v[170:173], v[202:205], v[102:105]
	v_mfma_f32_16x16x32_bf16 v[94:97], v[158:161], v[210:213], v[94:97]
	v_mfma_f32_16x16x32_bf16 v[86:89], v[170:173], v[210:213], v[86:89]
	v_mfma_f32_16x16x32_bf16 v[78:81], v[158:161], v[218:221], v[78:81]
	v_mfma_f32_16x16x32_bf16 v[70:73], v[170:173], v[218:221], v[70:73]
	v_mfma_f32_16x16x32_bf16 v[122:125], v[174:177], v[190:193], v[122:125]
	v_mfma_f32_16x16x32_bf16 v[114:117], v[182:185], v[190:193], v[114:117]
	v_mfma_f32_16x16x32_bf16 v[106:109], v[174:177], v[198:201], v[106:109]
	v_mfma_f32_16x16x32_bf16 v[98:101], v[182:185], v[198:201], v[98:101]
	v_mfma_f32_16x16x32_bf16 v[90:93], v[174:177], v[206:209], v[90:93]
	v_mfma_f32_16x16x32_bf16 v[82:85], v[182:185], v[206:209], v[82:85]
	v_mfma_f32_16x16x32_bf16 v[74:77], v[174:177], v[214:217], v[74:77]
	v_mfma_f32_16x16x32_bf16 v[66:69], v[182:185], v[214:217], v[66:69]
	v_mfma_f32_16x16x32_bf16 v[122:125], v[178:181], v[194:197], v[122:125]
	v_mfma_f32_16x16x32_bf16 v[114:117], v[186:189], v[194:197], v[114:117]
	v_mfma_f32_16x16x32_bf16 v[106:109], v[178:181], v[202:205], v[106:109]
	v_mfma_f32_16x16x32_bf16 v[98:101], v[186:189], v[202:205], v[98:101]
	v_mfma_f32_16x16x32_bf16 v[90:93], v[178:181], v[210:213], v[90:93]
	v_mfma_f32_16x16x32_bf16 v[82:85], v[186:189], v[210:213], v[82:85]
	v_mfma_f32_16x16x32_bf16 v[74:77], v[178:181], v[218:221], v[74:77]
	v_mfma_f32_16x16x32_bf16 v[66:69], v[186:189], v[218:221], v[66:69]
	s_setprio 0
	s_barrier
	s_add_i32 s0, s80, s49
	v_lshl_add_u64 v[222:223], s[44:45], 0, v[134:135]
	s_mov_b32 m0, s0
	ds_read_b128 v[190:193], v157 offset:16384
	ds_read_b128 v[194:197], v157 offset:17408
	ds_read_b128 v[198:201], v157 offset:18432
	ds_read_b128 v[202:205], v157 offset:19456
	ds_read_b128 v[206:209], v157 offset:20480
	ds_read_b128 v[210:213], v157 offset:21504
	ds_read_b128 v[214:217], v157 offset:22528
	ds_read_b128 v[218:221], v157 offset:23552
	global_load_lds_dwordx4 v[222:223], off
	s_add_i32 m0, s0, 0x2000
	s_add_u32 s4, s44, 0x40000
	v_lshl_add_u64 v[224:225], s[44:45], 0, v[130:131]
	s_addc_u32 s5, s45, 0
	s_add_i32 s0, s81, s49
	global_load_lds_dwordx4 v[224:225], off
	v_lshl_add_u64 v[226:227], s[4:5], 0, v[134:135]
	s_mov_b32 m0, s0
	v_lshl_add_u64 v[228:229], s[46:47], 0, v[132:133]
	global_load_lds_dwordx4 v[226:227], off
	v_lshl_add_u64 v[226:227], s[4:5], 0, v[130:131]
	s_add_i32 m0, s0, 0x2000
	s_nop 0
	global_load_lds_dwordx4 v[226:227], off
	v_lshl_add_u64 v[226:227], s[46:47], 0, v[136:137]
	s_mov_b32 m0, s41
	s_nop 0
	global_load_lds_dwordx4 v[226:227], off
	s_mov_b32 m0, s72
	s_nop 0
	global_load_lds_dwordx4 v[228:229], off
	s_waitcnt vmcnt(8)
	s_waitcnt lgkmcnt(0)
	s_barrier
	s_setprio 3
	s_waitcnt lgkmcnt(0)
	v_mfma_f32_16x16x32_bf16 v[62:65], v[146:149], v[190:193], v[62:65]
	v_mfma_f32_16x16x32_bf16 v[58:61], v[166:169], v[190:193], v[58:61]
	v_mfma_f32_16x16x32_bf16 v[50:53], v[146:149], v[198:201], v[50:53]
	v_mfma_f32_16x16x32_bf16 v[42:45], v[166:169], v[198:201], v[42:45]
	v_mfma_f32_16x16x32_bf16 v[34:37], v[146:149], v[206:209], v[34:37]
	v_mfma_f32_16x16x32_bf16 v[26:29], v[166:169], v[206:209], v[26:29]
	v_mfma_f32_16x16x32_bf16 v[14:17], v[146:149], v[214:217], v[14:17]
	v_mfma_f32_16x16x32_bf16 v[6:9], v[166:169], v[214:217], v[6:9]
	v_mfma_f32_16x16x32_bf16 v[62:65], v[158:161], v[194:197], v[62:65]
	v_mfma_f32_16x16x32_bf16 v[58:61], v[170:173], v[194:197], v[58:61]
	v_mfma_f32_16x16x32_bf16 v[50:53], v[158:161], v[202:205], v[50:53]
	v_mfma_f32_16x16x32_bf16 v[42:45], v[170:173], v[202:205], v[42:45]
	v_mfma_f32_16x16x32_bf16 v[34:37], v[158:161], v[210:213], v[34:37]
	v_mfma_f32_16x16x32_bf16 v[26:29], v[170:173], v[210:213], v[26:29]
	v_mfma_f32_16x16x32_bf16 v[14:17], v[158:161], v[218:221], v[14:17]
	v_mfma_f32_16x16x32_bf16 v[6:9], v[170:173], v[218:221], v[6:9]
	v_mfma_f32_16x16x32_bf16 v[54:57], v[174:177], v[190:193], v[54:57]
	v_mfma_f32_16x16x32_bf16 v[46:49], v[182:185], v[190:193], v[46:49]
	v_mfma_f32_16x16x32_bf16 v[38:41], v[174:177], v[198:201], v[38:41]
	v_mfma_f32_16x16x32_bf16 v[30:33], v[182:185], v[198:201], v[30:33]
	v_mfma_f32_16x16x32_bf16 v[22:25], v[174:177], v[206:209], v[22:25]
	v_mfma_f32_16x16x32_bf16 v[18:21], v[182:185], v[206:209], v[18:21]
	v_mfma_f32_16x16x32_bf16 v[10:13], v[174:177], v[214:217], v[10:13]
	v_mfma_f32_16x16x32_bf16 v[2:5], v[182:185], v[214:217], v[2:5]
	v_mfma_f32_16x16x32_bf16 v[54:57], v[178:181], v[194:197], v[54:57]
	v_mfma_f32_16x16x32_bf16 v[46:49], v[186:189], v[194:197], v[46:49]
	v_mfma_f32_16x16x32_bf16 v[38:41], v[178:181], v[202:205], v[38:41]
	v_mfma_f32_16x16x32_bf16 v[30:33], v[186:189], v[202:205], v[30:33]
	v_mfma_f32_16x16x32_bf16 v[22:25], v[178:181], v[210:213], v[22:25]
	v_mfma_f32_16x16x32_bf16 v[18:21], v[186:189], v[210:213], v[18:21]
	v_mfma_f32_16x16x32_bf16 v[10:13], v[178:181], v[218:221], v[10:13]
	v_mfma_f32_16x16x32_bf16 v[2:5], v[186:189], v[218:221], v[2:5]
	s_setprio 0
	s_barrier
; #define PG8_STAGE(bufoff, gbase, voff) do { _Pragma("unroll") for (int _i = 0; _i < 2; ++_i) \
;         __builtin_amdgcn_global_load_lds((const unsigned*)((const char*)(gbase) + (voff)[_i]), (PG8_LAS unsigned*)(lds + (bufoff) + ldsw + _i * 8192), 16, 0, 0); } while (0)
; #define PG8_LDA(dst, b, h) do { _Pragma("unroll") for (int m = 0; m < 4; ++m) Frag<F8>::load(dst[m], lds + PG8_SA(b, h) + aoff + m * 2048); } while (0)
; #define PG8_LDB(dst, b, h) do { _Pragma("unroll") for (int n = 0; n < 2; ++n) Frag<F8>::load(dst[n], lds + PG8_SB(b, h) + boff + n * 2048); } while (0)
; #define PG8_MMA(ai, bj, At, Bt) do { __builtin_amdgcn_s_setprio(3); _Pragma("unroll") for (int m = 0; m < 4; ++m) _Pragma("unroll") for (int n = 0; n < 2; ++n) Frag<F8>::mma(acc[ai][bj][m][n], Bt[n], At[m]); \
;         __builtin_amdgcn_s_setprio(0); } while (0)
; #define PG8_WAIT_V(n) asm volatile("s_waitcnt vmcnt(" #n ")" ::: "memory")
; #define PG8_WAIT_L(n) asm volatile("s_waitcnt lgkmcnt(" #n ")" ::: "memory")
; #define PG8_BAR __builtin_amdgcn_s_barrier()
; #define PG8_SCHED __builtin_amdgcn_sched_barrier(0)
; template <class Epi, class Sched, bool ALIGN_EPI = false, bool SP2 = false, bool F8 = false>
; __device__ __forceinline__ void gemm_phase(PG8_LAS unsigned char* lds, const Gemm g, const Sched& S, const Epi& E) {
;     ...
;             PG8_LDB(B0, 1, 0); PG8_LDB(B1, 1, 1); PG8_SCHED; PG8_LDA(At, 1, 0); PG8_STAGE(PG8_SA(0, 1), a2 + hstep, voffA);
;             PG8_WAIT_V(8); PG8_WAIT_L(0); PG8_BAR; PG8_MMA(0, 0, At, B0); PG8_MMA(0, 1, At, B1); PG8_BAR; PG8_SCHED;
	s_add_i32 s0, 0, 0x18000
	v_add_u32_e32 v165, s0, v151
	s_add_i32 s1, 0, 0x1c000
	ds_read_b128 v[146:149], v165
	ds_read_b128 v[158:161], v165 offset:1024
	ds_read_b128 v[166:169], v165 offset:2048
	ds_read_b128 v[170:173], v165 offset:3072
	v_add_u32_e32 v165, s1, v151
	ds_read_b128 v[174:177], v165
	ds_read_b128 v[178:181], v165 offset:1024
	ds_read_b128 v[182:185], v165 offset:2048
	ds_read_b128 v[186:189], v165 offset:3072
	s_add_u32 s4, s46, 0x40000
	s_addc_u32 s5, s47, 0
	s_mov_b32 m0, s73
	v_lshl_add_u64 v[230:231], s[4:5], 0, v[136:137]
	ds_read_b128 v[190:193], v157 offset:32768
	ds_read_b128 v[194:197], v157 offset:33792
	ds_read_b128 v[198:201], v157 offset:34816
	ds_read_b128 v[202:205], v157 offset:35840
	ds_read_b128 v[206:209], v157 offset:36864
	ds_read_b128 v[210:213], v157 offset:37888
	ds_read_b128 v[214:217], v157 offset:38912
	ds_read_b128 v[218:221], v157 offset:39936
	global_load_lds_dwordx4 v[230:231], off
	v_lshl_add_u64 v[230:231], s[4:5], 0, v[132:133]
	s_mov_b32 m0, s74
	s_nop 0
	global_load_lds_dwordx4 v[230:231], off
	s_waitcnt vmcnt(8)
	s_waitcnt lgkmcnt(0)
	s_barrier
	s_setprio 3
	s_waitcnt lgkmcnt(0)
	v_mfma_f32_16x16x32_bf16 v[126:129], v[146:149], v[190:193], v[126:129]
	v_mfma_f32_16x16x32_bf16 v[118:121], v[166:169], v[190:193], v[118:121]
	v_mfma_f32_16x16x32_bf16 v[110:113], v[146:149], v[198:201], v[110:113]
	v_mfma_f32_16x16x32_bf16 v[102:105], v[166:169], v[198:201], v[102:105]
	v_mfma_f32_16x16x32_bf16 v[94:97], v[146:149], v[206:209], v[94:97]
	v_mfma_f32_16x16x32_bf16 v[86:89], v[166:169], v[206:209], v[86:89]
	v_mfma_f32_16x16x32_bf16 v[78:81], v[146:149], v[214:217], v[78:81]
	v_mfma_f32_16x16x32_bf16 v[70:73], v[166:169], v[214:217], v[70:73]
	v_mfma_f32_16x16x32_bf16 v[126:129], v[158:161], v[194:197], v[126:129]
	v_mfma_f32_16x16x32_bf16 v[118:121], v[170:173], v[194:197], v[118:121]
	v_mfma_f32_16x16x32_bf16 v[110:113], v[158:161], v[202:205], v[110:113]
	v_mfma_f32_16x16x32_bf16 v[102:105], v[170:173], v[202:205], v[102:105]
	v_mfma_f32_16x16x32_bf16 v[94:97], v[158:161], v[210:213], v[94:97]
	v_mfma_f32_16x16x32_bf16 v[86:89], v[170:173], v[210:213], v[86:89]
	v_mfma_f32_16x16x32_bf16 v[78:81], v[158:161], v[218:221], v[78:81]
	v_mfma_f32_16x16x32_bf16 v[70:73], v[170:173], v[218:221], v[70:73]
	v_mfma_f32_16x16x32_bf16 v[122:125], v[174:177], v[190:193], v[122:125]
	v_mfma_f32_16x16x32_bf16 v[114:117], v[182:185], v[190:193], v[114:117]
	v_mfma_f32_16x16x32_bf16 v[106:109], v[174:177], v[198:201], v[106:109]
	v_mfma_f32_16x16x32_bf16 v[98:101], v[182:185], v[198:201], v[98:101]
	v_mfma_f32_16x16x32_bf16 v[90:93], v[174:177], v[206:209], v[90:93]
	v_mfma_f32_16x16x32_bf16 v[82:85], v[182:185], v[206:209], v[82:85]
	v_mfma_f32_16x16x32_bf16 v[74:77], v[174:177], v[214:217], v[74:77]
	v_mfma_f32_16x16x32_bf16 v[66:69], v[182:185], v[214:217], v[66:69]
	v_mfma_f32_16x16x32_bf16 v[122:125], v[178:181], v[194:197], v[122:125]
	v_mfma_f32_16x16x32_bf16 v[114:117], v[186:189], v[194:197], v[114:117]
	v_mfma_f32_16x16x32_bf16 v[106:109], v[178:181], v[202:205], v[106:109]
	v_mfma_f32_16x16x32_bf16 v[98:101], v[186:189], v[202:205], v[98:101]
	v_mfma_f32_16x16x32_bf16 v[90:93], v[178:181], v[210:213], v[90:93]
	v_mfma_f32_16x16x32_bf16 v[82:85], v[186:189], v[210:213], v[82:85]
	v_mfma_f32_16x16x32_bf16 v[74:77], v[178:181], v[218:221], v[74:77]
	v_mfma_f32_16x16x32_bf16 v[66:69], v[186:189], v[218:221], v[66:69]
	s_setprio 0
	s_barrier
; #define PG8_STAGE(bufoff, gbase, voff) do { _Pragma("unroll") for (int _i = 0; _i < 2; ++_i) \
;         __builtin_amdgcn_global_load_lds((const unsigned*)((const char*)(gbase) + (voff)[_i]), (PG8_LAS unsigned*)(lds + (bufoff) + ldsw + _i * 8192), 16, 0, 0); } while (0)
; #define PG8_LDA(dst, b, h) do { _Pragma("unroll") for (int m = 0; m < 4; ++m) Frag<F8>::load(dst[m], lds + PG8_SA(b, h) + aoff + m * 2048); } while (0)
; #define PG8_MMA(ai, bj, At, Bt) do { __builtin_amdgcn_s_setprio(3); _Pragma("unroll") for (int m = 0; m < 4; ++m) _Pragma("unroll") for (int n = 0; n < 2; ++n) Frag<F8>::mma(acc[ai][bj][m][n], Bt[n], At[m]); \
;         __builtin_amdgcn_s_setprio(0); } while (0)
; #define PG8_WAIT_V(n) asm volatile("s_waitcnt vmcnt(" #n ")" ::: "memory")
; #define PG8_WAIT_L(n) asm volatile("s_waitcnt lgkmcnt(" #n ")" ::: "memory")
; #define PG8_BAR __builtin_amdgcn_s_barrier()
; #define PG8_SCHED __builtin_amdgcn_sched_barrier(0)
; template <class Epi, class Sched, bool ALIGN_EPI = false, bool SP2 = false, bool F8 = false>
; __device__ __forceinline__ void gemm_phase(PG8_LAS unsigned char* lds, const Gemm g, const Sched& S, const Epi& E) {
;     ...
;             PG8_LDA(At, 1, 1); PG8_STAGE(PG8_SB(1, 0), b3, voffB); PG8_STAGE(PG8_SB(1, 1), b3 + hstep, voffB); PG8_STAGE(PG8_SA(1, 0), a3, voffA);
;             PG8_WAIT_V(8); PG8_WAIT_L(0); PG8_BAR; PG8_MMA(1, 0, At, B0); PG8_MMA(1, 1, At, B1); PG8_BAR; PG8_SCHED;
	s_add_i32 s0, s0, s49
	v_lshl_add_u64 v[222:223], v[222:223], 0, s[18:19]
	s_mov_b32 m0, s0
	ds_read_b128 v[190:193], v157 offset:49152
	ds_read_b128 v[194:197], v157 offset:50176
	ds_read_b128 v[198:201], v157 offset:51200
	ds_read_b128 v[202:205], v157 offset:52224
	ds_read_b128 v[206:209], v157 offset:53248
	ds_read_b128 v[210:213], v157 offset:54272
	ds_read_b128 v[214:217], v157 offset:55296
	ds_read_b128 v[218:221], v157 offset:56320
	global_load_lds_dwordx4 v[222:223], off
	s_add_i32 m0, s0, 0x2000
	s_add_u32 s4, s44, 0x40080
	v_lshl_add_u64 v[222:223], v[224:225], 0, s[18:19]
	s_addc_u32 s5, s45, 0
	s_add_i32 s0, s1, s49
	global_load_lds_dwordx4 v[222:223], off
	v_lshl_add_u64 v[222:223], s[4:5], 0, v[134:135]
	s_mov_b32 m0, s0
	s_nop 0
	global_load_lds_dwordx4 v[222:223], off
	v_lshl_add_u64 v[222:223], s[4:5], 0, v[130:131]
	s_add_i32 m0, s0, 0x2000
	s_nop 0
	global_load_lds_dwordx4 v[222:223], off
	v_lshl_add_u64 v[222:223], v[226:227], 0, s[18:19]
	s_mov_b32 m0, s75
	s_nop 0
	global_load_lds_dwordx4 v[222:223], off
	v_lshl_add_u64 v[222:223], v[228:229], 0, s[18:19]
	s_mov_b32 m0, s79
	s_nop 0
	global_load_lds_dwordx4 v[222:223], off
	s_waitcnt vmcnt(8)
	s_waitcnt lgkmcnt(0)
	s_barrier
	s_setprio 3
	s_waitcnt lgkmcnt(0)
	v_mfma_f32_16x16x32_bf16 v[62:65], v[146:149], v[190:193], v[62:65]
	v_mfma_f32_16x16x32_bf16 v[58:61], v[166:169], v[190:193], v[58:61]
	v_mfma_f32_16x16x32_bf16 v[50:53], v[146:149], v[198:201], v[50:53]
	v_mfma_f32_16x16x32_bf16 v[42:45], v[166:169], v[198:201], v[42:45]
	v_mfma_f32_16x16x32_bf16 v[34:37], v[146:149], v[206:209], v[34:37]
	v_mfma_f32_16x16x32_bf16 v[26:29], v[166:169], v[206:209], v[26:29]
	v_mfma_f32_16x16x32_bf16 v[14:17], v[146:149], v[214:217], v[14:17]
	v_mfma_f32_16x16x32_bf16 v[6:9], v[166:169], v[214:217], v[6:9]
	v_mfma_f32_16x16x32_bf16 v[62:65], v[158:161], v[194:197], v[62:65]
	v_mfma_f32_16x16x32_bf16 v[58:61], v[170:173], v[194:197], v[58:61]
	v_mfma_f32_16x16x32_bf16 v[50:53], v[158:161], v[202:205], v[50:53]
	v_mfma_f32_16x16x32_bf16 v[42:45], v[170:173], v[202:205], v[42:45]
	v_mfma_f32_16x16x32_bf16 v[34:37], v[158:161], v[210:213], v[34:37]
	v_mfma_f32_16x16x32_bf16 v[26:29], v[170:173], v[210:213], v[26:29]
	v_mfma_f32_16x16x32_bf16 v[14:17], v[158:161], v[218:221], v[14:17]
	v_mfma_f32_16x16x32_bf16 v[6:9], v[170:173], v[218:221], v[6:9]
	v_mfma_f32_16x16x32_bf16 v[54:57], v[174:177], v[190:193], v[54:57]
	v_mfma_f32_16x16x32_bf16 v[46:49], v[182:185], v[190:193], v[46:49]
	v_mfma_f32_16x16x32_bf16 v[38:41], v[174:177], v[198:201], v[38:41]
	v_mfma_f32_16x16x32_bf16 v[30:33], v[182:185], v[198:201], v[30:33]
	v_mfma_f32_16x16x32_bf16 v[22:25], v[174:177], v[206:209], v[22:25]
	v_mfma_f32_16x16x32_bf16 v[18:21], v[182:185], v[206:209], v[18:21]
	v_mfma_f32_16x16x32_bf16 v[10:13], v[174:177], v[214:217], v[10:13]
	v_mfma_f32_16x16x32_bf16 v[2:5], v[182:185], v[214:217], v[2:5]
	v_mfma_f32_16x16x32_bf16 v[54:57], v[178:181], v[194:197], v[54:57]
	v_mfma_f32_16x16x32_bf16 v[46:49], v[186:189], v[194:197], v[46:49]
	v_mfma_f32_16x16x32_bf16 v[38:41], v[178:181], v[202:205], v[38:41]
	v_mfma_f32_16x16x32_bf16 v[30:33], v[186:189], v[202:205], v[30:33]
	v_mfma_f32_16x16x32_bf16 v[22:25], v[178:181], v[210:213], v[22:25]
	v_mfma_f32_16x16x32_bf16 v[18:21], v[186:189], v[210:213], v[18:21]
	v_mfma_f32_16x16x32_bf16 v[10:13], v[178:181], v[218:221], v[10:13]
	v_mfma_f32_16x16x32_bf16 v[2:5], v[186:189], v[218:221], v[2:5]
	s_setprio 0
	s_barrier
	s_add_i32 s86, s86, 2
	s_add_u32 s42, s42, 0x100
	s_addc_u32 s43, s43, 0
	s_add_u32 s84, s84, 0x100
	s_addc_u32 s85, s85, 0
	s_cmp_gt_u32 s86, 13
	s_cbranch_scc0 .LBB0_562

; #define PG8_STAGE(bufoff, gbase, voff) do { _Pragma("unroll") for (int _i = 0; _i < 2; ++_i) \
;         __builtin_amdgcn_global_load_lds((const unsigned*)((const char*)(gbase) + (voff)[_i]), (PG8_LAS unsigned*)(lds + (bufoff) + ldsw + _i * 8192), 16, 0, 0); } while (0)
; #define PG8_LDA(dst, b, h) do { _Pragma("unroll") for (int m = 0; m < 4; ++m) Frag<F8>::load(dst[m], lds + PG8_SA(b, h) + aoff + m * 2048); } while (0)
; #define PG8_LDB(dst, b, h) do { _Pragma("unroll") for (int n = 0; n < 2; ++n) Frag<F8>::load(dst[n], lds + PG8_SB(b, h) + boff + n * 2048); } while (0)
; #define PG8_MMA(ai, bj, At, Bt) do { __builtin_amdgcn_s_setprio(3); _Pragma("unroll") for (int m = 0; m < 4; ++m) _Pragma("unroll") for (int n = 0; n < 2; ++n) Frag<F8>::mma(acc[ai][bj][m][n], Bt[n], At[m]); \
;         __builtin_amdgcn_s_setprio(0); } while (0)
; #define PG8_WAIT_V(n) asm volatile("s_waitcnt vmcnt(" #n ")" ::: "memory")
; #define PG8_WAIT_L(n) asm volatile("s_waitcnt lgkmcnt(" #n ")" ::: "memory")
; #define PG8_BAR __builtin_amdgcn_s_barrier()
; #define PG8_SCHED __builtin_amdgcn_sched_barrier(0)
; template <class Epi, class Sched, bool ALIGN_EPI = false, bool SP2 = false, bool F8 = false>
; __device__ __forceinline__ void gemm_phase(PG8_LAS unsigned char* lds, const Gemm g, const Sched& S, const Epi& E) {
;     ...
;             PG8_LDB(B0, 0, 0); PG8_LDB(B1, 0, 1); PG8_SCHED; PG8_LDA(At, 0, 0); PG8_STAGE(PG8_SA(1, 1), a1 + hstep, voffA);
;             PG8_WAIT_V(8); PG8_WAIT_L(0); PG8_BAR; PG8_MMA(0, 0, At, B0); PG8_MMA(0, 1, At, B1); PG8_BAR; PG8_SCHED;
;             PG8_LDA(At, 0, 1); PG8_STAGE(PG8_SB(0, 0), b2, voffB); PG8_STAGE(PG8_SB(0, 1), b2 + hstep, voffB); PG8_STAGE(PG8_SA(0, 0), a2, voffA);
;             PG8_WAIT_V(8); PG8_WAIT_L(0); PG8_BAR; PG8_MMA(1, 0, At, B0); PG8_MMA(1, 1, At, B1); PG8_BAR; PG8_SCHED;
.LBB0_674:
	v_add_u32_e32 v186, s90, v158
	v_add_u32_e32 v202, s91, v158
	s_add_u32 s0, s36, s50
	ds_read_b128 v[174:177], v186
	ds_read_b128 v[178:181], v186 offset:1024
	ds_read_b128 v[182:185], v186 offset:2048
	ds_read_b128 v[186:189], v186 offset:3072
	ds_read_b128 v[190:193], v202
	ds_read_b128 v[194:197], v202 offset:1024
	ds_read_b128 v[198:201], v202 offset:2048
	ds_read_b128 v[202:205], v202 offset:3072
	s_addc_u32 s1, s37, s51
	s_add_u32 s0, s0, 0x100
	s_addc_u32 s1, s1, 0
	s_add_u32 s4, s47, s50
	s_addc_u32 s5, s96, s51
	s_cmpk_eq_i32 s50, 0x1b00
	s_cselect_b32 s71, s49, s1
	s_cselect_b32 s70, s48, s0
	s_cselect_b32 s53, s17, s5
	s_cselect_b32 s52, s16, s4
	v_lshl_add_u64 v[238:239], v[146:147], 0, s[50:51]
	s_add_i32 m0, s83, 0xc000
	ds_read_b128 v[206:209], v160
	ds_read_b128 v[210:213], v160 offset:1024
	ds_read_b128 v[214:217], v160 offset:2048
	ds_read_b128 v[218:221], v160 offset:3072
	ds_read_b128 v[222:225], v160 offset:4096
	ds_read_b128 v[226:229], v160 offset:5120
	ds_read_b128 v[230:233], v160 offset:6144
	ds_read_b128 v[234:237], v160 offset:7168
	global_load_lds_dwordx4 v[238:239], off
	v_lshl_add_u64 v[238:239], v[148:149], 0, s[50:51]
	s_add_i32 m0, s83, 0xe000
	s_nop 0
	global_load_lds_dwordx4 v[238:239], off
	s_waitcnt vmcnt(8)
	s_waitcnt lgkmcnt(0)
	s_barrier
	s_setprio 3
	s_waitcnt lgkmcnt(0)
	v_mfma_f32_16x16x32_bf16 v[22:25], v[174:177], v[206:209], v[22:25]
	v_mfma_f32_16x16x32_bf16 v[30:33], v[182:185], v[206:209], v[30:33]
	v_mfma_f32_16x16x32_bf16 v[46:49], v[174:177], v[214:217], v[46:49]
	v_mfma_f32_16x16x32_bf16 v[54:57], v[182:185], v[214:217], v[54:57]
	v_mfma_f32_16x16x32_bf16 v[78:81], v[174:177], v[222:225], v[78:81]
	v_mfma_f32_16x16x32_bf16 v[86:89], v[182:185], v[222:225], v[86:89]
	v_mfma_f32_16x16x32_bf16 v[98:101], v[174:177], v[230:233], v[98:101]
	v_mfma_f32_16x16x32_bf16 v[102:105], v[182:185], v[230:233], v[102:105]
	v_mfma_f32_16x16x32_bf16 v[22:25], v[178:181], v[210:213], v[22:25]
	v_mfma_f32_16x16x32_bf16 v[30:33], v[186:189], v[210:213], v[30:33]
	v_mfma_f32_16x16x32_bf16 v[46:49], v[178:181], v[218:221], v[46:49]
	v_mfma_f32_16x16x32_bf16 v[54:57], v[186:189], v[218:221], v[54:57]
	v_mfma_f32_16x16x32_bf16 v[78:81], v[178:181], v[226:229], v[78:81]
	v_mfma_f32_16x16x32_bf16 v[86:89], v[186:189], v[226:229], v[86:89]
	v_mfma_f32_16x16x32_bf16 v[98:101], v[178:181], v[234:237], v[98:101]
	v_mfma_f32_16x16x32_bf16 v[102:105], v[186:189], v[234:237], v[102:105]
	v_mfma_f32_16x16x32_bf16 v[2:5], v[190:193], v[206:209], v[2:5]
	v_mfma_f32_16x16x32_bf16 v[6:9], v[198:201], v[206:209], v[6:9]
	v_mfma_f32_16x16x32_bf16 v[10:13], v[190:193], v[214:217], v[10:13]
	v_mfma_f32_16x16x32_bf16 v[14:17], v[198:201], v[214:217], v[14:17]
	v_mfma_f32_16x16x32_bf16 v[34:37], v[190:193], v[222:225], v[34:37]
	v_mfma_f32_16x16x32_bf16 v[38:41], v[198:201], v[222:225], v[38:41]
	v_mfma_f32_16x16x32_bf16 v[58:61], v[190:193], v[230:233], v[58:61]
	v_mfma_f32_16x16x32_bf16 v[62:65], v[198:201], v[230:233], v[62:65]
	v_mfma_f32_16x16x32_bf16 v[2:5], v[194:197], v[210:213], v[2:5]
	v_mfma_f32_16x16x32_bf16 v[6:9], v[202:205], v[210:213], v[6:9]
	v_mfma_f32_16x16x32_bf16 v[10:13], v[194:197], v[218:221], v[10:13]
	v_mfma_f32_16x16x32_bf16 v[14:17], v[202:205], v[218:221], v[14:17]
	v_mfma_f32_16x16x32_bf16 v[34:37], v[194:197], v[226:229], v[34:37]
	v_mfma_f32_16x16x32_bf16 v[38:41], v[202:205], v[226:229], v[38:41]
	v_mfma_f32_16x16x32_bf16 v[58:61], v[194:197], v[234:237], v[58:61]
	v_mfma_f32_16x16x32_bf16 v[62:65], v[202:205], v[234:237], v[62:65]
	s_setprio 0
	s_barrier
	s_add_i32 s0, s90, s75
	v_lshl_add_u64 v[238:239], s[52:53], 0, v[132:133]
	s_mov_b32 m0, s0
	ds_read_b128 v[206:209], v160 offset:16384
	ds_read_b128 v[210:213], v160 offset:17408
	ds_read_b128 v[214:217], v160 offset:18432
	ds_read_b128 v[218:221], v160 offset:19456
	ds_read_b128 v[222:225], v160 offset:20480
	ds_read_b128 v[226:229], v160 offset:21504
	ds_read_b128 v[230:233], v160 offset:22528
	ds_read_b128 v[234:237], v160 offset:23552
	global_load_lds_dwordx4 v[238:239], off
	s_add_i32 m0, s0, 0x2000
	s_add_u32 s4, s52, 0xe0000
	v_lshl_add_u64 v[240:241], s[52:53], 0, v[136:137]
	s_addc_u32 s5, s53, 0
	s_add_i32 s0, s91, s75
	global_load_lds_dwordx4 v[240:241], off
	v_lshl_add_u64 v[242:243], s[4:5], 0, v[132:133]
	s_mov_b32 m0, s0
	v_lshl_add_u64 v[244:245], s[70:71], 0, v[134:135]
	global_load_lds_dwordx4 v[242:243], off
	v_lshl_add_u64 v[242:243], s[4:5], 0, v[136:137]
	s_add_i32 m0, s0, 0x2000
	s_nop 0
	global_load_lds_dwordx4 v[242:243], off
	v_lshl_add_u64 v[242:243], s[70:71], 0, v[130:131]
	s_mov_b32 m0, s83
	s_nop 0
	global_load_lds_dwordx4 v[242:243], off
	s_mov_b32 m0, s84
	s_nop 0
	global_load_lds_dwordx4 v[244:245], off
	s_waitcnt vmcnt(8)
	s_waitcnt lgkmcnt(0)
	s_barrier
; #define PG8_STAGE(bufoff, gbase, voff) do { _Pragma("unroll") for (int _i = 0; _i < 2; ++_i) \
;         __builtin_amdgcn_global_load_lds((const unsigned*)((const char*)(gbase) + (voff)[_i]), (PG8_LAS unsigned*)(lds + (bufoff) + ldsw + _i * 8192), 16, 0, 0); } while (0)
; #define PG8_LDA(dst, b, h) do { _Pragma("unroll") for (int m = 0; m < 4; ++m) Frag<F8>::load(dst[m], lds + PG8_SA(b, h) + aoff + m * 2048); } while (0)
; #define PG8_LDB(dst, b, h) do { _Pragma("unroll") for (int n = 0; n < 2; ++n) Frag<F8>::load(dst[n], lds + PG8_SB(b, h) + boff + n * 2048); } while (0)
; #define PG8_MMA(ai, bj, At, Bt) do { __builtin_amdgcn_s_setprio(3); _Pragma("unroll") for (int m = 0; m < 4; ++m) _Pragma("unroll") for (int n = 0; n < 2; ++n) Frag<F8>::mma(acc[ai][bj][m][n], Bt[n], At[m]); \
;         __builtin_amdgcn_s_setprio(0); } while (0)
; #define PG8_WAIT_V(n) asm volatile("s_waitcnt vmcnt(" #n ")" ::: "memory")
; #define PG8_WAIT_L(n) asm volatile("s_waitcnt lgkmcnt(" #n ")" ::: "memory")
; #define PG8_BAR __builtin_amdgcn_s_barrier()
; #define PG8_SCHED __builtin_amdgcn_sched_barrier(0)
; template <class Epi, class Sched, bool ALIGN_EPI = false, bool SP2 = false, bool F8 = false>
; __device__ __forceinline__ void gemm_phase(PG8_LAS unsigned char* lds, const Gemm g, const Sched& S, const Epi& E) {
;     ...
;             PG8_WAIT_V(8); PG8_WAIT_L(0); PG8_BAR; PG8_MMA(1, 0, At, B0); PG8_MMA(1, 1, At, B1); PG8_BAR; PG8_SCHED;
;             PG8_LDB(B0, 1, 0); PG8_LDB(B1, 1, 1); PG8_SCHED; PG8_LDA(At, 1, 0); PG8_STAGE(PG8_SA(0, 1), a2 + hstep, voffA);
;             PG8_WAIT_V(8); PG8_WAIT_L(0); PG8_BAR; PG8_MMA(0, 0, At, B0); PG8_MMA(0, 1, At, B1); PG8_BAR; PG8_SCHED;
	s_setprio 3
	s_waitcnt lgkmcnt(0)
	v_mfma_f32_16x16x32_bf16 v[66:69], v[174:177], v[206:209], v[66:69]
	v_mfma_f32_16x16x32_bf16 v[70:73], v[182:185], v[206:209], v[70:73]
	v_mfma_f32_16x16x32_bf16 v[90:93], v[174:177], v[214:217], v[90:93]
	v_mfma_f32_16x16x32_bf16 v[94:97], v[182:185], v[214:217], v[94:97]
	v_mfma_f32_16x16x32_bf16 v[106:109], v[174:177], v[222:225], v[106:109]
	v_mfma_f32_16x16x32_bf16 v[110:113], v[182:185], v[222:225], v[110:113]
	v_mfma_f32_16x16x32_bf16 v[114:117], v[174:177], v[230:233], v[114:117]
	v_mfma_f32_16x16x32_bf16 v[126:129], v[182:185], v[230:233], v[126:129]
	v_mfma_f32_16x16x32_bf16 v[66:69], v[178:181], v[210:213], v[66:69]
	v_mfma_f32_16x16x32_bf16 v[70:73], v[186:189], v[210:213], v[70:73]
	v_mfma_f32_16x16x32_bf16 v[90:93], v[178:181], v[218:221], v[90:93]
	v_mfma_f32_16x16x32_bf16 v[94:97], v[186:189], v[218:221], v[94:97]
	v_mfma_f32_16x16x32_bf16 v[106:109], v[178:181], v[226:229], v[106:109]
	v_mfma_f32_16x16x32_bf16 v[110:113], v[186:189], v[226:229], v[110:113]
	v_mfma_f32_16x16x32_bf16 v[114:117], v[178:181], v[234:237], v[114:117]
	v_mfma_f32_16x16x32_bf16 v[126:129], v[186:189], v[234:237], v[126:129]
	v_mfma_f32_16x16x32_bf16 v[18:21], v[190:193], v[206:209], v[18:21]
	v_mfma_f32_16x16x32_bf16 v[26:29], v[198:201], v[206:209], v[26:29]
	v_mfma_f32_16x16x32_bf16 v[42:45], v[190:193], v[214:217], v[42:45]
	v_mfma_f32_16x16x32_bf16 v[50:53], v[198:201], v[214:217], v[50:53]
	v_mfma_f32_16x16x32_bf16 v[74:77], v[190:193], v[222:225], v[74:77]
	v_mfma_f32_16x16x32_bf16 v[82:85], v[198:201], v[222:225], v[82:85]
	v_mfma_f32_16x16x32_bf16 v[122:125], v[190:193], v[230:233], v[122:125]
	v_mfma_f32_16x16x32_bf16 v[118:121], v[198:201], v[230:233], v[118:121]
	v_mfma_f32_16x16x32_bf16 v[18:21], v[194:197], v[210:213], v[18:21]
	v_mfma_f32_16x16x32_bf16 v[26:29], v[202:205], v[210:213], v[26:29]
	v_mfma_f32_16x16x32_bf16 v[42:45], v[194:197], v[218:221], v[42:45]
	v_mfma_f32_16x16x32_bf16 v[50:53], v[202:205], v[218:221], v[50:53]
	v_mfma_f32_16x16x32_bf16 v[74:77], v[194:197], v[226:229], v[74:77]
	v_mfma_f32_16x16x32_bf16 v[82:85], v[202:205], v[226:229], v[82:85]
	v_mfma_f32_16x16x32_bf16 v[122:125], v[194:197], v[234:237], v[122:125]
	v_mfma_f32_16x16x32_bf16 v[118:121], v[202:205], v[234:237], v[118:121]
	s_setprio 0
	s_barrier
	s_add_i32 s0, 0, 0x18000
	s_add_i32 s1, 0, 0x1c000
	v_add_u32_e32 v186, s0, v158
	v_add_u32_e32 v202, s1, v158
	ds_read_b128 v[174:177], v186
	ds_read_b128 v[178:181], v186 offset:1024
	ds_read_b128 v[182:185], v186 offset:2048
	ds_read_b128 v[186:189], v186 offset:3072
	ds_read_b128 v[190:193], v202
	ds_read_b128 v[194:197], v202 offset:1024
	ds_read_b128 v[198:201], v202 offset:2048
	ds_read_b128 v[202:205], v202 offset:3072
	s_add_u32 s4, s70, 0xe0000
	s_addc_u32 s5, s71, 0
	s_mov_b32 m0, s85
	v_lshl_add_u64 v[246:247], s[4:5], 0, v[130:131]
	ds_read_b128 v[206:209], v160 offset:32768
	ds_read_b128 v[210:213], v160 offset:33792
	ds_read_b128 v[214:217], v160 offset:34816
	ds_read_b128 v[218:221], v160 offset:35840
	ds_read_b128 v[222:225], v160 offset:36864
	ds_read_b128 v[226:229], v160 offset:37888
	ds_read_b128 v[230:233], v160 offset:38912
	ds_read_b128 v[234:237], v160 offset:39936
	global_load_lds_dwordx4 v[246:247], off
	v_lshl_add_u64 v[246:247], s[4:5], 0, v[134:135]
	s_mov_b32 m0, s86
	s_nop 0
	global_load_lds_dwordx4 v[246:247], off
	s_waitcnt vmcnt(8)
	s_waitcnt lgkmcnt(0)
	s_barrier
	s_setprio 3
	s_waitcnt lgkmcnt(0)
	v_mfma_f32_16x16x32_bf16 v[22:25], v[174:177], v[206:209], v[22:25]
	v_mfma_f32_16x16x32_bf16 v[30:33], v[182:185], v[206:209], v[30:33]
	v_mfma_f32_16x16x32_bf16 v[46:49], v[174:177], v[214:217], v[46:49]
	v_mfma_f32_16x16x32_bf16 v[54:57], v[182:185], v[214:217], v[54:57]
	v_mfma_f32_16x16x32_bf16 v[78:81], v[174:177], v[222:225], v[78:81]
	v_mfma_f32_16x16x32_bf16 v[86:89], v[182:185], v[222:225], v[86:89]
	v_mfma_f32_16x16x32_bf16 v[98:101], v[174:177], v[230:233], v[98:101]
	v_mfma_f32_16x16x32_bf16 v[102:105], v[182:185], v[230:233], v[102:105]
	v_mfma_f32_16x16x32_bf16 v[22:25], v[178:181], v[210:213], v[22:25]
	v_mfma_f32_16x16x32_bf16 v[30:33], v[186:189], v[210:213], v[30:33]
	v_mfma_f32_16x16x32_bf16 v[46:49], v[178:181], v[218:221], v[46:49]
	v_mfma_f32_16x16x32_bf16 v[54:57], v[186:189], v[218:221], v[54:57]
	v_mfma_f32_16x16x32_bf16 v[78:81], v[178:181], v[226:229], v[78:81]
	v_mfma_f32_16x16x32_bf16 v[86:89], v[186:189], v[226:229], v[86:89]
	v_mfma_f32_16x16x32_bf16 v[98:101], v[178:181], v[234:237], v[98:101]
	v_mfma_f32_16x16x32_bf16 v[102:105], v[186:189], v[234:237], v[102:105]
	v_mfma_f32_16x16x32_bf16 v[2:5], v[190:193], v[206:209], v[2:5]
	v_mfma_f32_16x16x32_bf16 v[6:9], v[198:201], v[206:209], v[6:9]
	v_mfma_f32_16x16x32_bf16 v[10:13], v[190:193], v[214:217], v[10:13]
	v_mfma_f32_16x16x32_bf16 v[14:17], v[198:201], v[214:217], v[14:17]
	v_mfma_f32_16x16x32_bf16 v[34:37], v[190:193], v[222:225], v[34:37]
	v_mfma_f32_16x16x32_bf16 v[38:41], v[198:201], v[222:225], v[38:41]
	v_mfma_f32_16x16x32_bf16 v[58:61], v[190:193], v[230:233], v[58:61]
	v_mfma_f32_16x16x32_bf16 v[62:65], v[198:201], v[230:233], v[62:65]
	v_mfma_f32_16x16x32_bf16 v[2:5], v[194:197], v[210:213], v[2:5]
	v_mfma_f32_16x16x32_bf16 v[6:9], v[202:205], v[210:213], v[6:9]
	v_mfma_f32_16x16x32_bf16 v[10:13], v[194:197], v[218:221], v[10:13]
	v_mfma_f32_16x16x32_bf16 v[14:17], v[202:205], v[218:221], v[14:17]
	v_mfma_f32_16x16x32_bf16 v[34:37], v[194:197], v[226:229], v[34:37]
	v_mfma_f32_16x16x32_bf16 v[38:41], v[202:205], v[226:229], v[38:41]
	v_mfma_f32_16x16x32_bf16 v[58:61], v[194:197], v[234:237], v[58:61]
	v_mfma_f32_16x16x32_bf16 v[62:65], v[202:205], v[234:237], v[62:65]
	s_setprio 0
	s_barrier
; #define PG8_STAGE(bufoff, gbase, voff) do { _Pragma("unroll") for (int _i = 0; _i < 2; ++_i) \
;         __builtin_amdgcn_global_load_lds((const unsigned*)((const char*)(gbase) + (voff)[_i]), (PG8_LAS unsigned*)(lds + (bufoff) + ldsw + _i * 8192), 16, 0, 0); } while (0)
; #define PG8_LDA(dst, b, h) do { _Pragma("unroll") for (int m = 0; m < 4; ++m) Frag<F8>::load(dst[m], lds + PG8_SA(b, h) + aoff + m * 2048); } while (0)
; #define PG8_MMA(ai, bj, At, Bt) do { __builtin_amdgcn_s_setprio(3); _Pragma("unroll") for (int m = 0; m < 4; ++m) _Pragma("unroll") for (int n = 0; n < 2; ++n) Frag<F8>::mma(acc[ai][bj][m][n], Bt[n], At[m]); \
;         __builtin_amdgcn_s_setprio(0); } while (0)
; #define PG8_WAIT_V(n) asm volatile("s_waitcnt vmcnt(" #n ")" ::: "memory")
; #define PG8_WAIT_L(n) asm volatile("s_waitcnt lgkmcnt(" #n ")" ::: "memory")
; #define PG8_BAR __builtin_amdgcn_s_barrier()
; #define PG8_SCHED __builtin_amdgcn_sched_barrier(0)
; template <class Epi, class Sched, bool ALIGN_EPI = false, bool SP2 = false, bool F8 = false>
; __device__ __forceinline__ void gemm_phase(PG8_LAS unsigned char* lds, const Gemm g, const Sched& S, const Epi& E) {
;     ...
;             PG8_LDA(At, 1, 1); PG8_STAGE(PG8_SB(1, 0), b3, voffB); PG8_STAGE(PG8_SB(1, 1), b3 + hstep, voffB); PG8_STAGE(PG8_SA(1, 0), a3, voffA);
;             PG8_WAIT_V(8); PG8_WAIT_L(0); PG8_BAR; PG8_MMA(1, 0, At, B0); PG8_MMA(1, 1, At, B1); PG8_BAR; PG8_SCHED;
;     ...
;         if constexpr (ALIGN_EPI) { if (wr == 0) PG8_BAR; }
	s_add_i32 s0, s0, s75
	v_lshl_add_u64 v[238:239], v[238:239], 0, s[42:43]
	s_mov_b32 m0, s0
	ds_read_b128 v[206:209], v160 offset:49152
	ds_read_b128 v[210:213], v160 offset:50176
	ds_read_b128 v[214:217], v160 offset:51200
	ds_read_b128 v[218:221], v160 offset:52224
	ds_read_b128 v[222:225], v160 offset:53248
	ds_read_b128 v[226:229], v160 offset:54272
	ds_read_b128 v[230:233], v160 offset:55296
	ds_read_b128 v[234:237], v160 offset:56320
	global_load_lds_dwordx4 v[238:239], off
	s_add_i32 m0, s0, 0x2000
	s_add_u32 s4, s52, 0xe0080
	v_lshl_add_u64 v[238:239], v[240:241], 0, s[42:43]
	s_addc_u32 s5, s53, 0
	s_add_i32 s0, s1, s75
	global_load_lds_dwordx4 v[238:239], off
	v_lshl_add_u64 v[238:239], s[4:5], 0, v[132:133]
	s_mov_b32 m0, s0
	s_nop 0
	global_load_lds_dwordx4 v[238:239], off
	v_lshl_add_u64 v[238:239], s[4:5], 0, v[136:137]
	s_add_i32 m0, s0, 0x2000
	s_nop 0
	global_load_lds_dwordx4 v[238:239], off
	v_lshl_add_u64 v[238:239], v[242:243], 0, s[42:43]
	s_mov_b32 m0, s87
	s_nop 0
	global_load_lds_dwordx4 v[238:239], off
	v_lshl_add_u64 v[238:239], v[244:245], 0, s[42:43]
	s_mov_b32 m0, s88
	s_nop 0
	global_load_lds_dwordx4 v[238:239], off
	s_waitcnt vmcnt(8)
	s_waitcnt lgkmcnt(0)
	s_barrier
	s_setprio 3
	s_waitcnt lgkmcnt(0)
	v_mfma_f32_16x16x32_bf16 v[66:69], v[174:177], v[206:209], v[66:69]
	v_mfma_f32_16x16x32_bf16 v[70:73], v[182:185], v[206:209], v[70:73]
	v_mfma_f32_16x16x32_bf16 v[90:93], v[174:177], v[214:217], v[90:93]
	v_mfma_f32_16x16x32_bf16 v[94:97], v[182:185], v[214:217], v[94:97]
	v_mfma_f32_16x16x32_bf16 v[106:109], v[174:177], v[222:225], v[106:109]
	v_mfma_f32_16x16x32_bf16 v[110:113], v[182:185], v[222:225], v[110:113]
	v_mfma_f32_16x16x32_bf16 v[114:117], v[174:177], v[230:233], v[114:117]
	v_mfma_f32_16x16x32_bf16 v[126:129], v[182:185], v[230:233], v[126:129]
	v_mfma_f32_16x16x32_bf16 v[66:69], v[178:181], v[210:213], v[66:69]
	v_mfma_f32_16x16x32_bf16 v[70:73], v[186:189], v[210:213], v[70:73]
	v_mfma_f32_16x16x32_bf16 v[90:93], v[178:181], v[218:221], v[90:93]
	v_mfma_f32_16x16x32_bf16 v[94:97], v[186:189], v[218:221], v[94:97]
	v_mfma_f32_16x16x32_bf16 v[106:109], v[178:181], v[226:229], v[106:109]
	v_mfma_f32_16x16x32_bf16 v[110:113], v[186:189], v[226:229], v[110:113]
	v_mfma_f32_16x16x32_bf16 v[114:117], v[178:181], v[234:237], v[114:117]
	v_mfma_f32_16x16x32_bf16 v[126:129], v[186:189], v[234:237], v[126:129]
	v_mfma_f32_16x16x32_bf16 v[18:21], v[190:193], v[206:209], v[18:21]
	v_mfma_f32_16x16x32_bf16 v[26:29], v[198:201], v[206:209], v[26:29]
	v_mfma_f32_16x16x32_bf16 v[42:45], v[190:193], v[214:217], v[42:45]
	v_mfma_f32_16x16x32_bf16 v[50:53], v[198:201], v[214:217], v[50:53]
	v_mfma_f32_16x16x32_bf16 v[74:77], v[190:193], v[222:225], v[74:77]
	v_mfma_f32_16x16x32_bf16 v[82:85], v[198:201], v[222:225], v[82:85]
	v_mfma_f32_16x16x32_bf16 v[122:125], v[190:193], v[230:233], v[122:125]
	v_mfma_f32_16x16x32_bf16 v[118:121], v[198:201], v[230:233], v[118:121]
	v_mfma_f32_16x16x32_bf16 v[18:21], v[194:197], v[210:213], v[18:21]
	v_mfma_f32_16x16x32_bf16 v[26:29], v[202:205], v[210:213], v[26:29]
	v_mfma_f32_16x16x32_bf16 v[42:45], v[194:197], v[218:221], v[42:45]
	v_mfma_f32_16x16x32_bf16 v[50:53], v[202:205], v[218:221], v[50:53]
	v_mfma_f32_16x16x32_bf16 v[74:77], v[194:197], v[226:229], v[74:77]
	v_mfma_f32_16x16x32_bf16 v[82:85], v[202:205], v[226:229], v[82:85]
	v_mfma_f32_16x16x32_bf16 v[122:125], v[194:197], v[234:237], v[122:125]
	v_mfma_f32_16x16x32_bf16 v[118:121], v[202:205], v[234:237], v[118:121]
	s_setprio 0
	s_barrier
	s_add_i32 s3, s3, 2
	s_add_u32 s50, s50, 0x100
	s_addc_u32 s51, s51, 0
	s_cmp_gt_u32 s3, 53
	s_cbranch_scc0 .LBB0_674
	s_and_b64 vcc, exec, s[44:45]
	s_cbranch_vccz .LBB0_677
	s_barrier

; #define PG8_STAGE(bufoff, gbase, voff) do { _Pragma("unroll") for (int _i = 0; _i < 2; ++_i) \
;         __builtin_amdgcn_global_load_lds((const unsigned*)((const char*)(gbase) + (voff)[_i]), (PG8_LAS unsigned*)(lds + (bufoff) + ldsw + _i * 8192), 16, 0, 0); } while (0)
; #define PG8_LDA(dst, b, h) do { _Pragma("unroll") for (int m = 0; m < 4; ++m) Frag<F8>::load(dst[m], lds + PG8_SA(b, h) + aoff + m * 2048); } while (0)
; #define PG8_LDB(dst, b, h) do { _Pragma("unroll") for (int n = 0; n < 2; ++n) Frag<F8>::load(dst[n], lds + PG8_SB(b, h) + boff + n * 2048); } while (0)
; #define PG8_WAIT_V(n) asm volatile("s_waitcnt vmcnt(" #n ")" ::: "memory")
; #define PG8_WAIT_L(n) asm volatile("s_waitcnt lgkmcnt(" #n ")" ::: "memory")
; template <class Epi, class Sched, bool ALIGN_EPI = false, bool SP2 = false, bool F8 = false>
; __device__ __forceinline__ void gemm_phase(PG8_LAS unsigned char* lds, const Gemm g, const Sched& S, const Epi& E) {
;     ...
;         const bool has_next = S.next(ui + 1, nxt);
;         const char* nA = has_next ? (const char*)g.A + (size_t)nxt.pm * tstep + nxt.ko : cA; const char* nB = has_next ? (const char*)g.Bt + (size_t)nxt.pn * tstep + nxt.ko : cB;
;         for (int t = 0; t < nt; t += 2) {
;             const bool last = (t == nt - 2);
;             const char* a1 = cA + (size_t)(t + 1) * kstep;
;             const char* a2 = last ? nA : cA + (size_t)(t + 2) * kstep; const char* b2 = last ? nB : cB + (size_t)(t + 2) * kstep;
;             const char* a3 = a2 + kstep; const char* b3 = b2 + kstep;
;             if (last && has_next) S.a_ready(nxt);
;             if constexpr (SP2) {
;             PG8_LDB(B0, 0, 0); PG8_LDB(B1, 0, 1); PG8_SCHED; PG8_LDA(At, 0, 0); PG8_STAGE(PG8_SA(1, 1), a1 + hstep, voffA);
;             PG8_WAIT_V(8); PG8_WAIT_L(0); PG8_BAR; PG8_MMA(0, 0, At, B0); PG8_MMA(0, 1, At, B1); PG8_BAR; PG8_SCHED;
;             PG8_LDA(At, 0, 1); PG8_STAGE(PG8_SB(0, 0), b2, voffB); PG8_STAGE(PG8_SB(0, 1), b2 + hstep, voffB); PG8_STAGE(PG8_SA(0, 0), a2, voffA);
;             PG8_WAIT_V(8); PG8_WAIT_L(0); PG8_BAR; PG8_MMA(1, 0, At, B0); PG8_MMA(1, 1, At, B1); PG8_BAR; PG8_SCHED;
;             PG8_LDB(B0, 1, 0); PG8_LDB(B1, 1, 1); PG8_SCHED; PG8_LDA(At, 1, 0); PG8_STAGE(PG8_SA(0, 1), a2 + hstep, voffA);
;             PG8_WAIT_V(8); PG8_WAIT_L(0); PG8_BAR; PG8_MMA(0, 0, At, B0); PG8_MMA(0, 1, At, B1); PG8_BAR; PG8_SCHED;
.LBB0_801:
	s_ashr_i32 s25, s24, 31
	s_lshl_b64 s[4:5], s[24:25], 18
	s_add_u32 s36, s49, s4
	s_addc_u32 s37, s50, s5
	s_and_b64 s[4:5], s[8:9], exec
	s_cselect_b32 s25, s37, s43
	s_cselect_b32 s83, s36, s42
	s_ashr_i32 s31, s30, 31
	s_lshl_b64 s[4:5], s[30:31], 18
	s_add_u32 s38, s51, s4
	s_addc_u32 s39, s52, s5
	s_and_b64 s[4:5], s[8:9], exec
	s_cselect_b32 s31, s39, s45
	s_cselect_b32 s84, s38, s44
	s_add_u32 s42, s42, 0x20080
	s_addc_u32 s43, s43, 0
	s_add_u32 s85, s44, 0x100
	s_addc_u32 s86, s45, 0
	s_mov_b32 s87, -2
	ds_read_b128 v[18:21], v194
	ds_read_b128 v[22:25], v194 offset:1024
	ds_read_b128 v[26:29], v194 offset:2048
	ds_read_b128 v[30:33], v194 offset:3072
	ds_read_b128 v[2:5], v195
	ds_read_b128 v[6:9], v195 offset:1024
	ds_read_b128 v[10:13], v195 offset:2048
	ds_read_b128 v[14:17], v195 offset:3072
	s_add_u32 s0, s42, 0xfffe0080
	s_addc_u32 s1, s43, -1
	s_cmp_eq_u32 s87, 4
	s_cselect_b32 s47, s25, s1
	s_cselect_b32 s46, s83, s0
	s_cselect_b32 s45, s31, s86
	s_cselect_b32 s44, s84, s85
	v_lshl_add_u64 v[224:225], s[42:43], 0, v[174:175]
	s_add_i32 m0, s41, 0xc000
	ds_read_b128 v[182:185], v196
	ds_read_b128 v[186:189], v196 offset:1024
	ds_read_b128 v[200:203], v196 offset:2048
	ds_read_b128 v[204:207], v196 offset:3072
	ds_read_b128 v[208:211], v196 offset:4096
	ds_read_b128 v[212:215], v196 offset:5120
	ds_read_b128 v[216:219], v196 offset:6144
	ds_read_b128 v[220:223], v196 offset:7168
	global_load_lds_dwordx4 v[224:225], off
	v_lshl_add_u64 v[224:225], s[42:43], 0, v[176:177]
	s_add_i32 m0, s41, 0xe000
	s_nop 0
	global_load_lds_dwordx4 v[224:225], off
	s_waitcnt vmcnt(8)
	s_waitcnt lgkmcnt(0)
	s_barrier
	s_setprio 3
	s_waitcnt lgkmcnt(0)
	v_mfma_f32_16x16x128_f8f6f4 v[158:161], v[18:25], v[182:189], 0
	v_mfma_f32_16x16x128_f8f6f4 v[154:157], v[26:33], v[182:189], 0
	v_mfma_f32_16x16x128_f8f6f4 v[150:153], v[18:25], v[200:207], 0
	v_mfma_f32_16x16x128_f8f6f4 v[142:145], v[26:33], v[200:207], 0
	v_mfma_f32_16x16x128_f8f6f4 v[130:133], v[18:25], v[208:215], 0
	v_mfma_f32_16x16x128_f8f6f4 v[122:125], v[26:33], v[208:215], 0
	v_mfma_f32_16x16x128_f8f6f4 v[118:121], v[18:25], v[216:223], 0
	v_mfma_f32_16x16x128_f8f6f4 v[110:113], v[26:33], v[216:223], 0
	v_mfma_f32_16x16x128_f8f6f4 v[146:149], v[2:9], v[182:189], 0
	v_mfma_f32_16x16x128_f8f6f4 v[138:141], v[10:17], v[182:189], 0
	v_mfma_f32_16x16x128_f8f6f4 v[134:137], v[2:9], v[200:207], 0
	v_mfma_f32_16x16x128_f8f6f4 v[126:129], v[10:17], v[200:207], 0
	v_mfma_f32_16x16x128_f8f6f4 v[114:117], v[2:9], v[208:215], 0
	v_mfma_f32_16x16x128_f8f6f4 v[106:109], v[10:17], v[208:215], 0
	v_mfma_f32_16x16x128_f8f6f4 v[102:105], v[2:9], v[216:223], 0
	v_mfma_f32_16x16x128_f8f6f4 v[98:101], v[10:17], v[216:223], 0
	s_setprio 0
	s_barrier
	s_add_i32 s0, s79, s48
	v_lshl_add_u64 v[182:183], s[44:45], 0, v[170:171]
	s_mov_b32 m0, s0
	ds_read_b128 v[200:203], v196 offset:16384
	ds_read_b128 v[204:207], v196 offset:17408
	ds_read_b128 v[208:211], v196 offset:18432
	ds_read_b128 v[212:215], v196 offset:19456
	ds_read_b128 v[216:219], v196 offset:20480
	ds_read_b128 v[220:223], v196 offset:21504
	ds_read_b128 v[224:227], v196 offset:22528
	ds_read_b128 v[228:231], v196 offset:23552
	global_load_lds_dwordx4 v[182:183], off
	s_add_i32 m0, s0, 0x2000
	s_add_u32 s4, s44, 0x20000
	v_lshl_add_u64 v[184:185], s[44:45], 0, v[166:167]
	s_addc_u32 s5, s45, 0
	s_add_i32 s0, s80, s48
	global_load_lds_dwordx4 v[184:185], off
	v_lshl_add_u64 v[186:187], s[4:5], 0, v[170:171]
	s_mov_b32 m0, s0
	v_lshl_add_u64 v[188:189], s[46:47], 0, v[168:169]
	global_load_lds_dwordx4 v[186:187], off
	v_lshl_add_u64 v[186:187], s[4:5], 0, v[166:167]
	s_add_i32 m0, s0, 0x2000
	s_nop 0
	global_load_lds_dwordx4 v[186:187], off
	v_lshl_add_u64 v[186:187], s[46:47], 0, v[172:173]
	s_mov_b32 m0, s41
	s_nop 0
	global_load_lds_dwordx4 v[186:187], off
	s_mov_b32 m0, s71
	s_nop 0
	global_load_lds_dwordx4 v[188:189], off
	s_waitcnt vmcnt(8)
	s_waitcnt lgkmcnt(0)
	s_barrier
	s_setprio 3
	s_waitcnt lgkmcnt(0)
	v_mfma_f32_16x16x128_f8f6f4 v[94:97], v[18:25], v[200:207], 0
	v_mfma_f32_16x16x128_f8f6f4 v[90:93], v[26:33], v[200:207], 0
	v_mfma_f32_16x16x128_f8f6f4 v[86:89], v[18:25], v[208:215], 0
	v_mfma_f32_16x16x128_f8f6f4 v[82:85], v[26:33], v[208:215], 0
	v_mfma_f32_16x16x128_f8f6f4 v[70:73], v[18:25], v[216:223], 0
	v_mfma_f32_16x16x128_f8f6f4 v[66:69], v[26:33], v[216:223], 0
	v_mfma_f32_16x16x128_f8f6f4 v[54:57], v[18:25], v[224:231], 0
	v_mfma_f32_16x16x128_f8f6f4 v[50:53], v[26:33], v[224:231], 0
	v_mfma_f32_16x16x128_f8f6f4 v[78:81], v[2:9], v[200:207], 0
	v_mfma_f32_16x16x128_f8f6f4 v[74:77], v[10:17], v[200:207], 0
	v_mfma_f32_16x16x128_f8f6f4 v[62:65], v[2:9], v[208:215], 0
	v_mfma_f32_16x16x128_f8f6f4 v[58:61], v[10:17], v[208:215], 0
	v_mfma_f32_16x16x128_f8f6f4 v[46:49], v[2:9], v[216:223], 0
	v_mfma_f32_16x16x128_f8f6f4 v[42:45], v[10:17], v[216:223], 0
	v_mfma_f32_16x16x128_f8f6f4 v[38:41], v[2:9], v[224:231], 0
	v_mfma_f32_16x16x128_f8f6f4 v[34:37], v[10:17], v[224:231], 0
	s_setprio 0
	s_barrier
	s_add_i32 s0, 0, 0x18000
	s_add_i32 s1, 0, 0x1c000
	v_add_u32_e32 v14, s0, v190
	v_add_u32_e32 v30, s1, v190
	ds_read_b128 v[2:5], v14
	ds_read_b128 v[6:9], v14 offset:1024
	ds_read_b128 v[10:13], v14 offset:2048
	ds_read_b128 v[14:17], v14 offset:3072
	ds_read_b128 v[18:21], v30
	ds_read_b128 v[22:25], v30 offset:1024
	ds_read_b128 v[26:29], v30 offset:2048
	ds_read_b128 v[30:33], v30 offset:3072
	s_add_u32 s4, s46, 0x20000
	s_addc_u32 s5, s47, 0
	s_mov_b32 m0, s72
	v_lshl_add_u64 v[232:233], s[4:5], 0, v[172:173]
	ds_read_b128 v[200:203], v196 offset:32768
	ds_read_b128 v[204:207], v196 offset:33792
	ds_read_b128 v[208:211], v196 offset:34816
	ds_read_b128 v[212:215], v196 offset:35840
	ds_read_b128 v[216:219], v196 offset:36864
	ds_read_b128 v[220:223], v196 offset:37888
	ds_read_b128 v[224:227], v196 offset:38912
	ds_read_b128 v[228:231], v196 offset:39936
	global_load_lds_dwordx4 v[232:233], off
	v_lshl_add_u64 v[232:233], s[4:5], 0, v[168:169]
	s_mov_b32 m0, s73
	s_nop 0
	global_load_lds_dwordx4 v[232:233], off
	s_waitcnt vmcnt(8)
	s_waitcnt lgkmcnt(0)
	s_barrier
; #define PG8_STAGE(bufoff, gbase, voff) do { _Pragma("unroll") for (int _i = 0; _i < 2; ++_i) \
;         __builtin_amdgcn_global_load_lds((const unsigned*)((const char*)(gbase) + (voff)[_i]), (PG8_LAS unsigned*)(lds + (bufoff) + ldsw + _i * 8192), 16, 0, 0); } while (0)
; #define PG8_LDA(dst, b, h) do { _Pragma("unroll") for (int m = 0; m < 4; ++m) Frag<F8>::load(dst[m], lds + PG8_SA(b, h) + aoff + m * 2048); } while (0)
; #define PG8_LDB(dst, b, h) do { _Pragma("unroll") for (int n = 0; n < 2; ++n) Frag<F8>::load(dst[n], lds + PG8_SB(b, h) + boff + n * 2048); } while (0)
; #define PG8_MMA(ai, bj, At, Bt) do { __builtin_amdgcn_s_setprio(3); _Pragma("unroll") for (int m = 0; m < 4; ++m) _Pragma("unroll") for (int n = 0; n < 2; ++n) Frag<F8>::mma(acc[ai][bj][m][n], Bt[n], At[m]); \
;         __builtin_amdgcn_s_setprio(0); } while (0)
; #define PG8_WAIT_V(n) asm volatile("s_waitcnt vmcnt(" #n ")" ::: "memory")
; #define PG8_WAIT_L(n) asm volatile("s_waitcnt lgkmcnt(" #n ")" ::: "memory")
; #define PG8_BAR __builtin_amdgcn_s_barrier()
; #define PG8_SCHED __builtin_amdgcn_sched_barrier(0)
; template <class Epi, class Sched, bool ALIGN_EPI = false, bool SP2 = false, bool F8 = false>
; __device__ __forceinline__ void gemm_phase(PG8_LAS unsigned char* lds, const Gemm g, const Sched& S, const Epi& E) {
;     ...
;             PG8_LDB(B0, 0, 0); PG8_LDB(B1, 0, 1); PG8_SCHED; PG8_LDA(At, 0, 0); PG8_STAGE(PG8_SA(1, 1), a1 + hstep, voffA);
;             PG8_WAIT_V(8); PG8_WAIT_L(0); PG8_BAR; PG8_MMA(0, 0, At, B0); PG8_MMA(0, 1, At, B1); PG8_BAR; PG8_SCHED;
;             PG8_LDA(At, 0, 1); PG8_STAGE(PG8_SB(0, 0), b2, voffB); PG8_STAGE(PG8_SB(0, 1), b2 + hstep, voffB); PG8_STAGE(PG8_SA(0, 0), a2, voffA);
;             PG8_WAIT_V(8); PG8_WAIT_L(0); PG8_BAR; PG8_MMA(1, 0, At, B0); PG8_MMA(1, 1, At, B1); PG8_BAR; PG8_SCHED;
;             PG8_LDB(B0, 1, 0); PG8_LDB(B1, 1, 1); PG8_SCHED; PG8_LDA(At, 1, 0); PG8_STAGE(PG8_SA(0, 1), a2 + hstep, voffA);
;             PG8_WAIT_V(8); PG8_WAIT_L(0); PG8_BAR; PG8_MMA(0, 0, At, B0); PG8_MMA(0, 1, At, B1); PG8_BAR; PG8_SCHED;
;             PG8_LDA(At, 1, 1); PG8_STAGE(PG8_SB(1, 0), b3, voffB); PG8_STAGE(PG8_SB(1, 1), b3 + hstep, voffB); PG8_STAGE(PG8_SA(1, 0), a3, voffA);
;             PG8_WAIT_V(8); PG8_WAIT_L(0); PG8_BAR; PG8_MMA(1, 0, At, B0); PG8_MMA(1, 1, At, B1); PG8_BAR; PG8_SCHED;
	s_setprio 3
	s_waitcnt lgkmcnt(0)
	v_mfma_f32_16x16x128_f8f6f4 v[158:161], v[2:9], v[200:207], v[158:161]
	v_mfma_f32_16x16x128_f8f6f4 v[154:157], v[10:17], v[200:207], v[154:157]
	v_mfma_f32_16x16x128_f8f6f4 v[150:153], v[2:9], v[208:215], v[150:153]
	v_mfma_f32_16x16x128_f8f6f4 v[142:145], v[10:17], v[208:215], v[142:145]
	v_mfma_f32_16x16x128_f8f6f4 v[130:133], v[2:9], v[216:223], v[130:133]
	v_mfma_f32_16x16x128_f8f6f4 v[122:125], v[10:17], v[216:223], v[122:125]
	v_mfma_f32_16x16x128_f8f6f4 v[118:121], v[2:9], v[224:231], v[118:121]
	v_mfma_f32_16x16x128_f8f6f4 v[110:113], v[10:17], v[224:231], v[110:113]
	v_mfma_f32_16x16x128_f8f6f4 v[146:149], v[18:25], v[200:207], v[146:149]
	v_mfma_f32_16x16x128_f8f6f4 v[138:141], v[26:33], v[200:207], v[138:141]
	v_mfma_f32_16x16x128_f8f6f4 v[134:137], v[18:25], v[208:215], v[134:137]
	v_mfma_f32_16x16x128_f8f6f4 v[126:129], v[26:33], v[208:215], v[126:129]
	v_mfma_f32_16x16x128_f8f6f4 v[114:117], v[18:25], v[216:223], v[114:117]
	v_mfma_f32_16x16x128_f8f6f4 v[106:109], v[26:33], v[216:223], v[106:109]
	v_mfma_f32_16x16x128_f8f6f4 v[102:105], v[18:25], v[224:231], v[102:105]
	v_mfma_f32_16x16x128_f8f6f4 v[98:101], v[26:33], v[224:231], v[98:101]
	s_setprio 0
	s_barrier
	s_add_i32 s0, s0, s48
	v_lshl_add_u64 v[182:183], v[182:183], 0, s[18:19]
	s_mov_b32 m0, s0
	ds_read_b128 v[200:203], v196 offset:49152
	ds_read_b128 v[204:207], v196 offset:50176
	ds_read_b128 v[208:211], v196 offset:51200
	ds_read_b128 v[212:215], v196 offset:52224
	ds_read_b128 v[216:219], v196 offset:53248
	ds_read_b128 v[220:223], v196 offset:54272
	ds_read_b128 v[224:227], v196 offset:55296
	ds_read_b128 v[228:231], v196 offset:56320
	global_load_lds_dwordx4 v[182:183], off
	s_add_i32 m0, s0, 0x2000
	s_add_u32 s4, s44, 0x20080
	v_lshl_add_u64 v[182:183], v[184:185], 0, s[18:19]
	s_addc_u32 s5, s45, 0
	s_add_i32 s0, s1, s48
	global_load_lds_dwordx4 v[182:183], off
	v_lshl_add_u64 v[182:183], s[4:5], 0, v[170:171]
	s_mov_b32 m0, s0
	s_nop 0
	global_load_lds_dwordx4 v[182:183], off
	v_lshl_add_u64 v[182:183], s[4:5], 0, v[166:167]
	s_add_i32 m0, s0, 0x2000
	s_nop 0
	global_load_lds_dwordx4 v[182:183], off
	v_lshl_add_u64 v[182:183], v[186:187], 0, s[18:19]
	s_mov_b32 m0, s74
	s_nop 0
	global_load_lds_dwordx4 v[182:183], off
	v_lshl_add_u64 v[182:183], v[188:189], 0, s[18:19]
	s_mov_b32 m0, s75
	s_nop 0
	global_load_lds_dwordx4 v[182:183], off
	s_waitcnt vmcnt(8)
	s_waitcnt lgkmcnt(0)
	s_barrier
	s_setprio 3
	s_waitcnt lgkmcnt(0)
	v_mfma_f32_16x16x128_f8f6f4 v[94:97], v[2:9], v[200:207], v[94:97]
	v_mfma_f32_16x16x128_f8f6f4 v[90:93], v[10:17], v[200:207], v[90:93]
	v_mfma_f32_16x16x128_f8f6f4 v[86:89], v[2:9], v[208:215], v[86:89]
	v_mfma_f32_16x16x128_f8f6f4 v[82:85], v[10:17], v[208:215], v[82:85]
	v_mfma_f32_16x16x128_f8f6f4 v[70:73], v[2:9], v[216:223], v[70:73]
	v_mfma_f32_16x16x128_f8f6f4 v[66:69], v[10:17], v[216:223], v[66:69]
	v_mfma_f32_16x16x128_f8f6f4 v[54:57], v[2:9], v[224:231], v[54:57]
	v_mfma_f32_16x16x128_f8f6f4 v[50:53], v[10:17], v[224:231], v[50:53]
	v_mfma_f32_16x16x128_f8f6f4 v[78:81], v[18:25], v[200:207], v[78:81]
	v_mfma_f32_16x16x128_f8f6f4 v[74:77], v[26:33], v[200:207], v[74:77]
	v_mfma_f32_16x16x128_f8f6f4 v[62:65], v[18:25], v[208:215], v[62:65]
	v_mfma_f32_16x16x128_f8f6f4 v[58:61], v[26:33], v[208:215], v[58:61]
	v_mfma_f32_16x16x128_f8f6f4 v[46:49], v[18:25], v[216:223], v[46:49]
	v_mfma_f32_16x16x128_f8f6f4 v[42:45], v[26:33], v[216:223], v[42:45]
	v_mfma_f32_16x16x128_f8f6f4 v[38:41], v[18:25], v[224:231], v[38:41]
	v_mfma_f32_16x16x128_f8f6f4 v[34:37], v[26:33], v[224:231], v[34:37]
	s_setprio 0
	s_barrier
	s_add_i32 s87, s87, 2
	s_add_u32 s42, s42, 0x100
	s_addc_u32 s43, s43, 0
	s_add_u32 s85, s85, 0x100
	s_addc_u32 s86, s86, 0
	s_cmp_gt_u32 s87, 5
	s_cbranch_scc1 .Lpeel_exit_2
.LBB0_802:
	ds_read_b128 v[18:21], v194
	ds_read_b128 v[22:25], v194 offset:1024
	ds_read_b128 v[26:29], v194 offset:2048
	ds_read_b128 v[30:33], v194 offset:3072
	ds_read_b128 v[2:5], v195
	ds_read_b128 v[6:9], v195 offset:1024
	ds_read_b128 v[10:13], v195 offset:2048
	ds_read_b128 v[14:17], v195 offset:3072
	s_add_u32 s0, s42, 0xfffe0080
	s_addc_u32 s1, s43, -1
	s_cmp_eq_u32 s87, 4
	s_cselect_b32 s47, s25, s1
	s_cselect_b32 s46, s83, s0
	s_cselect_b32 s45, s31, s86
	s_cselect_b32 s44, s84, s85
	v_lshl_add_u64 v[224:225], s[42:43], 0, v[174:175]
	s_add_i32 m0, s41, 0xc000
	ds_read_b128 v[182:185], v196
	ds_read_b128 v[186:189], v196 offset:1024
	ds_read_b128 v[200:203], v196 offset:2048
	ds_read_b128 v[204:207], v196 offset:3072
	ds_read_b128 v[208:211], v196 offset:4096
	ds_read_b128 v[212:215], v196 offset:5120
	ds_read_b128 v[216:219], v196 offset:6144
	ds_read_b128 v[220:223], v196 offset:7168
	global_load_lds_dwordx4 v[224:225], off
	v_lshl_add_u64 v[224:225], s[42:43], 0, v[176:177]
	s_add_i32 m0, s41, 0xe000
	s_nop 0
	global_load_lds_dwordx4 v[224:225], off
	s_waitcnt vmcnt(8)
	s_waitcnt lgkmcnt(0)
	s_barrier
	s_setprio 3
	s_waitcnt lgkmcnt(0)
	v_mfma_f32_16x16x128_f8f6f4 v[158:161], v[18:25], v[182:189], v[158:161]
	v_mfma_f32_16x16x128_f8f6f4 v[154:157], v[26:33], v[182:189], v[154:157]
	v_mfma_f32_16x16x128_f8f6f4 v[150:153], v[18:25], v[200:207], v[150:153]
	v_mfma_f32_16x16x128_f8f6f4 v[142:145], v[26:33], v[200:207], v[142:145]
	v_mfma_f32_16x16x128_f8f6f4 v[130:133], v[18:25], v[208:215], v[130:133]
	v_mfma_f32_16x16x128_f8f6f4 v[122:125], v[26:33], v[208:215], v[122:125]
	v_mfma_f32_16x16x128_f8f6f4 v[118:121], v[18:25], v[216:223], v[118:121]
	v_mfma_f32_16x16x128_f8f6f4 v[110:113], v[26:33], v[216:223], v[110:113]
	v_mfma_f32_16x16x128_f8f6f4 v[146:149], v[2:9], v[182:189], v[146:149]
	v_mfma_f32_16x16x128_f8f6f4 v[138:141], v[10:17], v[182:189], v[138:141]
	v_mfma_f32_16x16x128_f8f6f4 v[134:137], v[2:9], v[200:207], v[134:137]
	v_mfma_f32_16x16x128_f8f6f4 v[126:129], v[10:17], v[200:207], v[126:129]
	v_mfma_f32_16x16x128_f8f6f4 v[114:117], v[2:9], v[208:215], v[114:117]
	v_mfma_f32_16x16x128_f8f6f4 v[106:109], v[10:17], v[208:215], v[106:109]
	v_mfma_f32_16x16x128_f8f6f4 v[102:105], v[2:9], v[216:223], v[102:105]
	v_mfma_f32_16x16x128_f8f6f4 v[98:101], v[10:17], v[216:223], v[98:101]
	s_setprio 0
	s_barrier
; #define PG8_STAGE(bufoff, gbase, voff) do { _Pragma("unroll") for (int _i = 0; _i < 2; ++_i) \
;         __builtin_amdgcn_global_load_lds((const unsigned*)((const char*)(gbase) + (voff)[_i]), (PG8_LAS unsigned*)(lds + (bufoff) + ldsw + _i * 8192), 16, 0, 0); } while (0)
; #define PG8_LDA(dst, b, h) do { _Pragma("unroll") for (int m = 0; m < 4; ++m) Frag<F8>::load(dst[m], lds + PG8_SA(b, h) + aoff + m * 2048); } while (0)
; #define PG8_LDB(dst, b, h) do { _Pragma("unroll") for (int n = 0; n < 2; ++n) Frag<F8>::load(dst[n], lds + PG8_SB(b, h) + boff + n * 2048); } while (0)
; #define PG8_MMA(ai, bj, At, Bt) do { __builtin_amdgcn_s_setprio(3); _Pragma("unroll") for (int m = 0; m < 4; ++m) _Pragma("unroll") for (int n = 0; n < 2; ++n) Frag<F8>::mma(acc[ai][bj][m][n], Bt[n], At[m]); \
;         __builtin_amdgcn_s_setprio(0); } while (0)
; #define PG8_WAIT_V(n) asm volatile("s_waitcnt vmcnt(" #n ")" ::: "memory")
; #define PG8_WAIT_L(n) asm volatile("s_waitcnt lgkmcnt(" #n ")" ::: "memory")
; #define PG8_BAR __builtin_amdgcn_s_barrier()
; #define PG8_SCHED __builtin_amdgcn_sched_barrier(0)
; template <class Epi, class Sched, bool ALIGN_EPI = false, bool SP2 = false, bool F8 = false>
; __device__ __forceinline__ void gemm_phase(PG8_LAS unsigned char* lds, const Gemm g, const Sched& S, const Epi& E) {
;     ...
;             PG8_LDB(B0, 1, 0); PG8_LDB(B1, 1, 1); PG8_SCHED; PG8_LDA(At, 1, 0); PG8_STAGE(PG8_SA(0, 1), a2 + hstep, voffA);
;             PG8_WAIT_V(8); PG8_WAIT_L(0); PG8_BAR; PG8_MMA(0, 0, At, B0); PG8_MMA(0, 1, At, B1); PG8_BAR; PG8_SCHED;
;             PG8_LDA(At, 1, 1); PG8_STAGE(PG8_SB(1, 0), b3, voffB); PG8_STAGE(PG8_SB(1, 1), b3 + hstep, voffB); PG8_STAGE(PG8_SA(1, 0), a3, voffA);
;             PG8_WAIT_V(8); PG8_WAIT_L(0); PG8_BAR; PG8_MMA(1, 0, At, B0); PG8_MMA(1, 1, At, B1); PG8_BAR; PG8_SCHED;
	s_add_i32 s0, s79, s48
	v_lshl_add_u64 v[182:183], s[44:45], 0, v[170:171]
	s_mov_b32 m0, s0
	ds_read_b128 v[200:203], v196 offset:16384
	ds_read_b128 v[204:207], v196 offset:17408
	ds_read_b128 v[208:211], v196 offset:18432
	ds_read_b128 v[212:215], v196 offset:19456
	ds_read_b128 v[216:219], v196 offset:20480
	ds_read_b128 v[220:223], v196 offset:21504
	ds_read_b128 v[224:227], v196 offset:22528
	ds_read_b128 v[228:231], v196 offset:23552
	global_load_lds_dwordx4 v[182:183], off
	s_add_i32 m0, s0, 0x2000
	s_add_u32 s4, s44, 0x20000
	v_lshl_add_u64 v[184:185], s[44:45], 0, v[166:167]
	s_addc_u32 s5, s45, 0
	s_add_i32 s0, s80, s48
	global_load_lds_dwordx4 v[184:185], off
	v_lshl_add_u64 v[186:187], s[4:5], 0, v[170:171]
	s_mov_b32 m0, s0
	v_lshl_add_u64 v[188:189], s[46:47], 0, v[168:169]
	global_load_lds_dwordx4 v[186:187], off
	v_lshl_add_u64 v[186:187], s[4:5], 0, v[166:167]
	s_add_i32 m0, s0, 0x2000
	s_nop 0
	global_load_lds_dwordx4 v[186:187], off
	v_lshl_add_u64 v[186:187], s[46:47], 0, v[172:173]
	s_mov_b32 m0, s41
	s_nop 0
	global_load_lds_dwordx4 v[186:187], off
	s_mov_b32 m0, s71
	s_nop 0
	global_load_lds_dwordx4 v[188:189], off
	s_waitcnt vmcnt(8)
	s_waitcnt lgkmcnt(0)
	s_barrier
	s_setprio 3
	s_waitcnt lgkmcnt(0)
	v_mfma_f32_16x16x128_f8f6f4 v[94:97], v[18:25], v[200:207], v[94:97]
	v_mfma_f32_16x16x128_f8f6f4 v[90:93], v[26:33], v[200:207], v[90:93]
	v_mfma_f32_16x16x128_f8f6f4 v[86:89], v[18:25], v[208:215], v[86:89]
	v_mfma_f32_16x16x128_f8f6f4 v[82:85], v[26:33], v[208:215], v[82:85]
	v_mfma_f32_16x16x128_f8f6f4 v[70:73], v[18:25], v[216:223], v[70:73]
	v_mfma_f32_16x16x128_f8f6f4 v[66:69], v[26:33], v[216:223], v[66:69]
	v_mfma_f32_16x16x128_f8f6f4 v[54:57], v[18:25], v[224:231], v[54:57]
	v_mfma_f32_16x16x128_f8f6f4 v[50:53], v[26:33], v[224:231], v[50:53]
	v_mfma_f32_16x16x128_f8f6f4 v[78:81], v[2:9], v[200:207], v[78:81]
	v_mfma_f32_16x16x128_f8f6f4 v[74:77], v[10:17], v[200:207], v[74:77]
	v_mfma_f32_16x16x128_f8f6f4 v[62:65], v[2:9], v[208:215], v[62:65]
	v_mfma_f32_16x16x128_f8f6f4 v[58:61], v[10:17], v[208:215], v[58:61]
	v_mfma_f32_16x16x128_f8f6f4 v[46:49], v[2:9], v[216:223], v[46:49]
	v_mfma_f32_16x16x128_f8f6f4 v[42:45], v[10:17], v[216:223], v[42:45]
	v_mfma_f32_16x16x128_f8f6f4 v[38:41], v[2:9], v[224:231], v[38:41]
	v_mfma_f32_16x16x128_f8f6f4 v[34:37], v[10:17], v[224:231], v[34:37]
	s_setprio 0
	s_barrier
	s_add_i32 s0, 0, 0x18000
	s_add_i32 s1, 0, 0x1c000
	v_add_u32_e32 v14, s0, v190
	v_add_u32_e32 v30, s1, v190
	ds_read_b128 v[2:5], v14
	ds_read_b128 v[6:9], v14 offset:1024
	ds_read_b128 v[10:13], v14 offset:2048
	ds_read_b128 v[14:17], v14 offset:3072
	ds_read_b128 v[18:21], v30
	ds_read_b128 v[22:25], v30 offset:1024
	ds_read_b128 v[26:29], v30 offset:2048
	ds_read_b128 v[30:33], v30 offset:3072
	s_add_u32 s4, s46, 0x20000
	s_addc_u32 s5, s47, 0
	s_mov_b32 m0, s72
	v_lshl_add_u64 v[232:233], s[4:5], 0, v[172:173]
	ds_read_b128 v[200:203], v196 offset:32768
	ds_read_b128 v[204:207], v196 offset:33792
	ds_read_b128 v[208:211], v196 offset:34816
	ds_read_b128 v[212:215], v196 offset:35840
	ds_read_b128 v[216:219], v196 offset:36864
	ds_read_b128 v[220:223], v196 offset:37888
	ds_read_b128 v[224:227], v196 offset:38912
	ds_read_b128 v[228:231], v196 offset:39936
	global_load_lds_dwordx4 v[232:233], off
	v_lshl_add_u64 v[232:233], s[4:5], 0, v[168:169]
	s_mov_b32 m0, s73
	s_nop 0
	global_load_lds_dwordx4 v[232:233], off
	s_waitcnt vmcnt(8)
	s_waitcnt lgkmcnt(0)
	s_barrier
; #define PG8_STAGE(bufoff, gbase, voff) do { _Pragma("unroll") for (int _i = 0; _i < 2; ++_i) \
;         __builtin_amdgcn_global_load_lds((const unsigned*)((const char*)(gbase) + (voff)[_i]), (PG8_LAS unsigned*)(lds + (bufoff) + ldsw + _i * 8192), 16, 0, 0); } while (0)
; #define PG8_LDA(dst, b, h) do { _Pragma("unroll") for (int m = 0; m < 4; ++m) Frag<F8>::load(dst[m], lds + PG8_SA(b, h) + aoff + m * 2048); } while (0)
; #define PG8_MMA(ai, bj, At, Bt) do { __builtin_amdgcn_s_setprio(3); _Pragma("unroll") for (int m = 0; m < 4; ++m) _Pragma("unroll") for (int n = 0; n < 2; ++n) Frag<F8>::mma(acc[ai][bj][m][n], Bt[n], At[m]); \
;         __builtin_amdgcn_s_setprio(0); } while (0)
; #define PG8_WAIT_V(n) asm volatile("s_waitcnt vmcnt(" #n ")" ::: "memory")
; #define PG8_WAIT_L(n) asm volatile("s_waitcnt lgkmcnt(" #n ")" ::: "memory")
; #define PG8_BAR __builtin_amdgcn_s_barrier()
; #define PG8_SCHED __builtin_amdgcn_sched_barrier(0)
; template <class Epi, class Sched, bool ALIGN_EPI = false, bool SP2 = false, bool F8 = false>
; __device__ __forceinline__ void gemm_phase(PG8_LAS unsigned char* lds, const Gemm g, const Sched& S, const Epi& E) {
;     ...
;         for (int t = 0; t < nt; t += 2) {
;     ...
;             PG8_LDA(At, 1, 1); PG8_STAGE(PG8_SB(1, 0), b3, voffB); PG8_STAGE(PG8_SB(1, 1), b3 + hstep, voffB); PG8_STAGE(PG8_SA(1, 0), a3, voffA);
;             PG8_WAIT_V(8); PG8_WAIT_L(0); PG8_BAR; PG8_MMA(1, 0, At, B0); PG8_MMA(1, 1, At, B1); PG8_BAR; PG8_SCHED;
	s_setprio 3
	s_waitcnt lgkmcnt(0)
	v_mfma_f32_16x16x128_f8f6f4 v[158:161], v[2:9], v[200:207], v[158:161]
	v_mfma_f32_16x16x128_f8f6f4 v[154:157], v[10:17], v[200:207], v[154:157]
	v_mfma_f32_16x16x128_f8f6f4 v[150:153], v[2:9], v[208:215], v[150:153]
	v_mfma_f32_16x16x128_f8f6f4 v[142:145], v[10:17], v[208:215], v[142:145]
	v_mfma_f32_16x16x128_f8f6f4 v[130:133], v[2:9], v[216:223], v[130:133]
	v_mfma_f32_16x16x128_f8f6f4 v[122:125], v[10:17], v[216:223], v[122:125]
	v_mfma_f32_16x16x128_f8f6f4 v[118:121], v[2:9], v[224:231], v[118:121]
	v_mfma_f32_16x16x128_f8f6f4 v[110:113], v[10:17], v[224:231], v[110:113]
	v_mfma_f32_16x16x128_f8f6f4 v[146:149], v[18:25], v[200:207], v[146:149]
	v_mfma_f32_16x16x128_f8f6f4 v[138:141], v[26:33], v[200:207], v[138:141]
	v_mfma_f32_16x16x128_f8f6f4 v[134:137], v[18:25], v[208:215], v[134:137]
	v_mfma_f32_16x16x128_f8f6f4 v[126:129], v[26:33], v[208:215], v[126:129]
	v_mfma_f32_16x16x128_f8f6f4 v[114:117], v[18:25], v[216:223], v[114:117]
	v_mfma_f32_16x16x128_f8f6f4 v[106:109], v[26:33], v[216:223], v[106:109]
	v_mfma_f32_16x16x128_f8f6f4 v[102:105], v[18:25], v[224:231], v[102:105]
	v_mfma_f32_16x16x128_f8f6f4 v[98:101], v[26:33], v[224:231], v[98:101]
	s_setprio 0
	s_barrier
	s_add_i32 s0, s0, s48
	v_lshl_add_u64 v[182:183], v[182:183], 0, s[18:19]
	s_mov_b32 m0, s0
	ds_read_b128 v[200:203], v196 offset:49152
	ds_read_b128 v[204:207], v196 offset:50176
	ds_read_b128 v[208:211], v196 offset:51200
	ds_read_b128 v[212:215], v196 offset:52224
	ds_read_b128 v[216:219], v196 offset:53248
	ds_read_b128 v[220:223], v196 offset:54272
	ds_read_b128 v[224:227], v196 offset:55296
	ds_read_b128 v[228:231], v196 offset:56320
	global_load_lds_dwordx4 v[182:183], off
	s_add_i32 m0, s0, 0x2000
	s_add_u32 s4, s44, 0x20080
	v_lshl_add_u64 v[182:183], v[184:185], 0, s[18:19]
	s_addc_u32 s5, s45, 0
	s_add_i32 s0, s1, s48
	global_load_lds_dwordx4 v[182:183], off
	v_lshl_add_u64 v[182:183], s[4:5], 0, v[170:171]
	s_mov_b32 m0, s0
	s_nop 0
	global_load_lds_dwordx4 v[182:183], off
	v_lshl_add_u64 v[182:183], s[4:5], 0, v[166:167]
	s_add_i32 m0, s0, 0x2000
	s_nop 0
	global_load_lds_dwordx4 v[182:183], off
	v_lshl_add_u64 v[182:183], v[186:187], 0, s[18:19]
	s_mov_b32 m0, s74
	s_nop 0
	global_load_lds_dwordx4 v[182:183], off
	v_lshl_add_u64 v[182:183], v[188:189], 0, s[18:19]
	s_mov_b32 m0, s75
	s_nop 0
	global_load_lds_dwordx4 v[182:183], off
	s_waitcnt vmcnt(8)
	s_waitcnt lgkmcnt(0)
	s_barrier
	s_setprio 3
	s_waitcnt lgkmcnt(0)
	v_mfma_f32_16x16x128_f8f6f4 v[94:97], v[2:9], v[200:207], v[94:97]
	v_mfma_f32_16x16x128_f8f6f4 v[90:93], v[10:17], v[200:207], v[90:93]
	v_mfma_f32_16x16x128_f8f6f4 v[86:89], v[2:9], v[208:215], v[86:89]
	v_mfma_f32_16x16x128_f8f6f4 v[82:85], v[10:17], v[208:215], v[82:85]
	v_mfma_f32_16x16x128_f8f6f4 v[70:73], v[2:9], v[216:223], v[70:73]
	v_mfma_f32_16x16x128_f8f6f4 v[66:69], v[10:17], v[216:223], v[66:69]
	v_mfma_f32_16x16x128_f8f6f4 v[54:57], v[2:9], v[224:231], v[54:57]
	v_mfma_f32_16x16x128_f8f6f4 v[50:53], v[10:17], v[224:231], v[50:53]
	v_mfma_f32_16x16x128_f8f6f4 v[78:81], v[18:25], v[200:207], v[78:81]
	v_mfma_f32_16x16x128_f8f6f4 v[74:77], v[26:33], v[200:207], v[74:77]
	v_mfma_f32_16x16x128_f8f6f4 v[62:65], v[18:25], v[208:215], v[62:65]
	v_mfma_f32_16x16x128_f8f6f4 v[58:61], v[26:33], v[208:215], v[58:61]
	v_mfma_f32_16x16x128_f8f6f4 v[46:49], v[18:25], v[216:223], v[46:49]
	v_mfma_f32_16x16x128_f8f6f4 v[42:45], v[26:33], v[216:223], v[42:45]
	v_mfma_f32_16x16x128_f8f6f4 v[38:41], v[18:25], v[224:231], v[38:41]
	v_mfma_f32_16x16x128_f8f6f4 v[34:37], v[26:33], v[224:231], v[34:37]
	s_setprio 0
	s_barrier
	s_add_i32 s87, s87, 2
	s_add_u32 s42, s42, 0x100
	s_addc_u32 s43, s43, 0
	s_add_u32 s85, s85, 0x100
	s_addc_u32 s86, s86, 0
	s_cmp_gt_u32 s87, 5
	s_cbranch_scc0 .LBB0_802

; #define PG8_STAGE(bufoff, gbase, voff) do { _Pragma("unroll") for (int _i = 0; _i < 2; ++_i) \
;         __builtin_amdgcn_global_load_lds((const unsigned*)((const char*)(gbase) + (voff)[_i]), (PG8_LAS unsigned*)(lds + (bufoff) + ldsw + _i * 8192), 16, 0, 0); } while (0)
; #define PG8_LDA(dst, b, h) do { _Pragma("unroll") for (int m = 0; m < 4; ++m) Frag<F8>::load(dst[m], lds + PG8_SA(b, h) + aoff + m * 2048); } while (0)
; #define PG8_LDB(dst, b, h) do { _Pragma("unroll") for (int n = 0; n < 2; ++n) Frag<F8>::load(dst[n], lds + PG8_SB(b, h) + boff + n * 2048); } while (0)
; #define PG8_MMA(ai, bj, At, Bt) do { __builtin_amdgcn_s_setprio(3); _Pragma("unroll") for (int m = 0; m < 4; ++m) _Pragma("unroll") for (int n = 0; n < 2; ++n) Frag<F8>::mma(acc[ai][bj][m][n], Bt[n], At[m]); \
;         __builtin_amdgcn_s_setprio(0); } while (0)
; #define PG8_WAIT_V(n) asm volatile("s_waitcnt vmcnt(" #n ")" ::: "memory")
; #define PG8_WAIT_L(n) asm volatile("s_waitcnt lgkmcnt(" #n ")" ::: "memory")
; #define PG8_BAR __builtin_amdgcn_s_barrier()
; #define PG8_SCHED __builtin_amdgcn_sched_barrier(0)
; template <class Epi, class Sched, bool ALIGN_EPI = false, bool SP2 = false, bool F8 = false>
; __device__ __forceinline__ void gemm_phase(PG8_LAS unsigned char* lds, const Gemm g, const Sched& S, const Epi& E) {
;     ...
;             PG8_LDB(B0, 0, 0); PG8_SCHED; PG8_LDA(At, 0, 0); PG8_STAGE(PG8_SA(1, 1), a1 + hstep, voffA);
;             PG8_WAIT_L(8); PG8_BAR; PG8_WAIT_L(0); PG8_MMA(0, 0, At, B0); PG8_BAR; PG8_SCHED;
;             PG8_LDB(B1, 0, 1); PG8_STAGE(PG8_SB(0, 0), b2, voffB);
;             PG8_BAR; PG8_WAIT_L(0); PG8_MMA(0, 1, At, B1); PG8_BAR;
;             PG8_LDA(At, 0, 1); PG8_STAGE(PG8_SA(0, 0), a2, voffA);
;             PG8_BAR; PG8_WAIT_L(0); PG8_MMA(1, 0, At, B0); PG8_BAR; PG8_SCHED;
;             PG8_STAGE(PG8_SB(0, 1), b2 + hstep, voffB);
;             PG8_WAIT_V(6); PG8_BAR; PG8_MMA(1, 1, At, B1); PG8_BAR;
.LBB0_1066:
	v_add_u32_e32 v160, s72, v157
	ds_read_b128 v[164:167], v160
	ds_read_b128 v[168:171], v160 offset:1024
	ds_read_b128 v[172:175], v160 offset:2048
	ds_read_b128 v[176:179], v160 offset:3072
	v_add_u32_e32 v160, s73, v157
	s_add_u32 s0, s20, s44
	ds_read_b128 v[180:183], v160
	ds_read_b128 v[184:187], v160 offset:1024
	ds_read_b128 v[188:191], v160 offset:2048
	ds_read_b128 v[192:195], v160 offset:3072
	s_addc_u32 s1, s21, s45
	s_add_u32 s0, s0, 0x100
	s_addc_u32 s1, s1, 0
	s_add_u32 s37, s3, s44
	s_addc_u32 s39, s4, s45
	s_cmpk_eq_i32 s44, 0x300
	s_cselect_b32 s49, s5, s1
	s_cselect_b32 s48, s6, s0
	s_cselect_b32 s47, s7, s39
	s_cselect_b32 s46, s31, s37
	v_lshl_add_u64 v[160:161], v[146:147], 0, s[44:45]
	s_add_i32 m0, s17, 0xc000
	ds_read_b128 v[196:199], v159
	ds_read_b128 v[200:203], v159 offset:1024
	ds_read_b128 v[204:207], v159 offset:2048
	ds_read_b128 v[208:211], v159 offset:3072
	ds_read_b128 v[212:215], v159 offset:4096
	ds_read_b128 v[216:219], v159 offset:5120
	ds_read_b128 v[220:223], v159 offset:6144
	ds_read_b128 v[224:227], v159 offset:7168
	global_load_lds_dwordx4 v[160:161], off
	v_lshl_add_u64 v[160:161], v[148:149], 0, s[44:45]
	s_add_i32 m0, s17, 0xe000
	s_nop 0
	global_load_lds_dwordx4 v[160:161], off
	s_waitcnt vmcnt(8)
	s_waitcnt lgkmcnt(0)
	s_barrier
	s_setprio 3
	s_waitcnt lgkmcnt(0)
	v_mfma_f32_16x16x32_bf16 v[54:57], v[164:167], v[196:199], v[54:57]
	v_mfma_f32_16x16x32_bf16 v[50:53], v[172:175], v[196:199], v[50:53]
	v_mfma_f32_16x16x32_bf16 v[70:73], v[164:167], v[204:207], v[70:73]
	v_mfma_f32_16x16x32_bf16 v[66:69], v[172:175], v[204:207], v[66:69]
	v_mfma_f32_16x16x32_bf16 v[78:81], v[164:167], v[212:215], v[78:81]
	v_mfma_f32_16x16x32_bf16 v[74:77], v[172:175], v[212:215], v[74:77]
	v_mfma_f32_16x16x32_bf16 v[86:89], v[164:167], v[220:223], v[86:89]
	v_mfma_f32_16x16x32_bf16 v[82:85], v[172:175], v[220:223], v[82:85]
	v_mfma_f32_16x16x32_bf16 v[54:57], v[168:171], v[200:203], v[54:57]
	v_mfma_f32_16x16x32_bf16 v[50:53], v[176:179], v[200:203], v[50:53]
	v_mfma_f32_16x16x32_bf16 v[70:73], v[168:171], v[208:211], v[70:73]
	v_mfma_f32_16x16x32_bf16 v[66:69], v[176:179], v[208:211], v[66:69]
	v_mfma_f32_16x16x32_bf16 v[78:81], v[168:171], v[216:219], v[78:81]
	v_mfma_f32_16x16x32_bf16 v[74:77], v[176:179], v[216:219], v[74:77]
	v_mfma_f32_16x16x32_bf16 v[86:89], v[168:171], v[224:227], v[86:89]
	v_mfma_f32_16x16x32_bf16 v[82:85], v[176:179], v[224:227], v[82:85]
	v_mfma_f32_16x16x32_bf16 v[14:17], v[180:183], v[196:199], v[14:17]
	v_mfma_f32_16x16x32_bf16 v[10:13], v[188:191], v[196:199], v[10:13]
	v_mfma_f32_16x16x32_bf16 v[22:25], v[180:183], v[204:207], v[22:25]
	v_mfma_f32_16x16x32_bf16 v[18:21], v[188:191], v[204:207], v[18:21]
	v_mfma_f32_16x16x32_bf16 v[30:33], v[180:183], v[212:215], v[30:33]
	v_mfma_f32_16x16x32_bf16 v[26:29], v[188:191], v[212:215], v[26:29]
	v_mfma_f32_16x16x32_bf16 v[46:49], v[180:183], v[220:223], v[46:49]
	v_mfma_f32_16x16x32_bf16 v[42:45], v[188:191], v[220:223], v[42:45]
	v_mfma_f32_16x16x32_bf16 v[14:17], v[184:187], v[200:203], v[14:17]
	v_mfma_f32_16x16x32_bf16 v[10:13], v[192:195], v[200:203], v[10:13]
	v_mfma_f32_16x16x32_bf16 v[22:25], v[184:187], v[208:211], v[22:25]
	v_mfma_f32_16x16x32_bf16 v[18:21], v[192:195], v[208:211], v[18:21]
	v_mfma_f32_16x16x32_bf16 v[30:33], v[184:187], v[216:219], v[30:33]
	v_mfma_f32_16x16x32_bf16 v[26:29], v[192:195], v[216:219], v[26:29]
	v_mfma_f32_16x16x32_bf16 v[46:49], v[184:187], v[224:227], v[46:49]
	v_mfma_f32_16x16x32_bf16 v[42:45], v[192:195], v[224:227], v[42:45]
	s_setprio 0
	s_barrier
	s_add_i32 s0, s72, s57
	v_lshl_add_u64 v[160:161], s[46:47], 0, v[132:133]
	s_mov_b32 m0, s0
	ds_read_b128 v[196:199], v159 offset:16384
	ds_read_b128 v[200:203], v159 offset:17408
	ds_read_b128 v[204:207], v159 offset:18432
	ds_read_b128 v[208:211], v159 offset:19456
	ds_read_b128 v[212:215], v159 offset:20480
	ds_read_b128 v[216:219], v159 offset:21504
	ds_read_b128 v[220:223], v159 offset:22528
	ds_read_b128 v[224:227], v159 offset:23552
	global_load_lds_dwordx4 v[160:161], off
	s_add_i32 m0, s0, 0x2000
	s_add_u32 s68, s46, 0x20000
	v_lshl_add_u64 v[228:229], s[46:47], 0, v[136:137]
	s_addc_u32 s69, s47, 0
	s_add_i32 s0, s73, s57
	global_load_lds_dwordx4 v[228:229], off
	v_lshl_add_u64 v[230:231], s[68:69], 0, v[132:133]
	s_mov_b32 m0, s0
	v_lshl_add_u64 v[232:233], s[48:49], 0, v[134:135]
	global_load_lds_dwordx4 v[230:231], off
	v_lshl_add_u64 v[230:231], s[68:69], 0, v[136:137]
	s_add_i32 m0, s0, 0x2000
	s_nop 0
	global_load_lds_dwordx4 v[230:231], off
	v_lshl_add_u64 v[230:231], s[48:49], 0, v[130:131]
	s_mov_b32 m0, s17
	s_nop 0
	global_load_lds_dwordx4 v[230:231], off
	s_mov_b32 m0, s59
	s_nop 0
	global_load_lds_dwordx4 v[232:233], off
	s_waitcnt vmcnt(8)
	s_waitcnt lgkmcnt(0)
	s_barrier
; #define PG8_STAGE(bufoff, gbase, voff) do { _Pragma("unroll") for (int _i = 0; _i < 2; ++_i) \
;         __builtin_amdgcn_global_load_lds((const unsigned*)((const char*)(gbase) + (voff)[_i]), (PG8_LAS unsigned*)(lds + (bufoff) + ldsw + _i * 8192), 16, 0, 0); } while (0)
; #define PG8_LDA(dst, b, h) do { _Pragma("unroll") for (int m = 0; m < 4; ++m) Frag<F8>::load(dst[m], lds + PG8_SA(b, h) + aoff + m * 2048); } while (0)
; #define PG8_LDB(dst, b, h) do { _Pragma("unroll") for (int n = 0; n < 2; ++n) Frag<F8>::load(dst[n], lds + PG8_SB(b, h) + boff + n * 2048); } while (0)
; #define PG8_MMA(ai, bj, At, Bt) do { __builtin_amdgcn_s_setprio(3); _Pragma("unroll") for (int m = 0; m < 4; ++m) _Pragma("unroll") for (int n = 0; n < 2; ++n) Frag<F8>::mma(acc[ai][bj][m][n], Bt[n], At[m]); \
;         __builtin_amdgcn_s_setprio(0); } while (0)
; #define PG8_WAIT_V(n) asm volatile("s_waitcnt vmcnt(" #n ")" ::: "memory")
; #define PG8_WAIT_L(n) asm volatile("s_waitcnt lgkmcnt(" #n ")" ::: "memory")
; #define PG8_BAR __builtin_amdgcn_s_barrier()
; #define PG8_SCHED __builtin_amdgcn_sched_barrier(0)
; template <class Epi, class Sched, bool ALIGN_EPI = false, bool SP2 = false, bool F8 = false>
; __device__ __forceinline__ void gemm_phase(PG8_LAS unsigned char* lds, const Gemm g, const Sched& S, const Epi& E) {
;     ...
;             PG8_LDB(B1, 0, 1); PG8_STAGE(PG8_SB(0, 0), b2, voffB);
;             PG8_BAR; PG8_WAIT_L(0); PG8_MMA(0, 1, At, B1); PG8_BAR;
;             PG8_LDA(At, 0, 1); PG8_STAGE(PG8_SA(0, 0), a2, voffA);
;             PG8_BAR; PG8_WAIT_L(0); PG8_MMA(1, 0, At, B0); PG8_BAR; PG8_SCHED;
;             PG8_STAGE(PG8_SB(0, 1), b2 + hstep, voffB);
;             PG8_WAIT_V(6); PG8_BAR; PG8_MMA(1, 1, At, B1); PG8_BAR;
;             PG8_LDB(B0, 1, 0); PG8_SCHED; PG8_LDA(At, 1, 0); PG8_STAGE(PG8_SA(0, 1), a2 + hstep, voffA);
	s_setprio 3
	s_waitcnt lgkmcnt(0)
	v_mfma_f32_16x16x32_bf16 v[38:41], v[164:167], v[196:199], v[38:41]
	v_mfma_f32_16x16x32_bf16 v[34:37], v[172:175], v[196:199], v[34:37]
	v_mfma_f32_16x16x32_bf16 v[62:65], v[164:167], v[204:207], v[62:65]
	v_mfma_f32_16x16x32_bf16 v[58:61], v[172:175], v[204:207], v[58:61]
	v_mfma_f32_16x16x32_bf16 v[118:121], v[164:167], v[212:215], v[118:121]
	v_mfma_f32_16x16x32_bf16 v[114:117], v[172:175], v[212:215], v[114:117]
	v_mfma_f32_16x16x32_bf16 v[126:129], v[164:167], v[220:223], v[126:129]
	v_mfma_f32_16x16x32_bf16 v[122:125], v[172:175], v[220:223], v[122:125]
	v_mfma_f32_16x16x32_bf16 v[38:41], v[168:171], v[200:203], v[38:41]
	v_mfma_f32_16x16x32_bf16 v[34:37], v[176:179], v[200:203], v[34:37]
	v_mfma_f32_16x16x32_bf16 v[62:65], v[168:171], v[208:211], v[62:65]
	v_mfma_f32_16x16x32_bf16 v[58:61], v[176:179], v[208:211], v[58:61]
	v_mfma_f32_16x16x32_bf16 v[118:121], v[168:171], v[216:219], v[118:121]
	v_mfma_f32_16x16x32_bf16 v[114:117], v[176:179], v[216:219], v[114:117]
	v_mfma_f32_16x16x32_bf16 v[126:129], v[168:171], v[224:227], v[126:129]
	v_mfma_f32_16x16x32_bf16 v[122:125], v[176:179], v[224:227], v[122:125]
	v_mfma_f32_16x16x32_bf16 v[6:9], v[180:183], v[196:199], v[6:9]
	v_mfma_f32_16x16x32_bf16 v[2:5], v[188:191], v[196:199], v[2:5]
	v_mfma_f32_16x16x32_bf16 v[94:97], v[180:183], v[204:207], v[94:97]
	v_mfma_f32_16x16x32_bf16 v[90:93], v[188:191], v[204:207], v[90:93]
	v_mfma_f32_16x16x32_bf16 v[102:105], v[180:183], v[212:215], v[102:105]
	v_mfma_f32_16x16x32_bf16 v[98:101], v[188:191], v[212:215], v[98:101]
	v_mfma_f32_16x16x32_bf16 v[110:113], v[180:183], v[220:223], v[110:113]
	v_mfma_f32_16x16x32_bf16 v[106:109], v[188:191], v[220:223], v[106:109]
	v_mfma_f32_16x16x32_bf16 v[6:9], v[184:187], v[200:203], v[6:9]
	v_mfma_f32_16x16x32_bf16 v[2:5], v[192:195], v[200:203], v[2:5]
	v_mfma_f32_16x16x32_bf16 v[94:97], v[184:187], v[208:211], v[94:97]
	v_mfma_f32_16x16x32_bf16 v[90:93], v[192:195], v[208:211], v[90:93]
	v_mfma_f32_16x16x32_bf16 v[102:105], v[184:187], v[216:219], v[102:105]
	v_mfma_f32_16x16x32_bf16 v[98:101], v[192:195], v[216:219], v[98:101]
	v_mfma_f32_16x16x32_bf16 v[110:113], v[184:187], v[224:227], v[110:113]
	v_mfma_f32_16x16x32_bf16 v[106:109], v[192:195], v[224:227], v[106:109]
	s_setprio 0
	s_barrier
	s_add_i32 s0, 0, 0x18000
	s_add_i32 s1, 0, 0x1c000
	v_add_u32_e32 v176, s0, v157
	v_add_u32_e32 v192, s1, v157
	ds_read_b128 v[164:167], v176
	ds_read_b128 v[168:171], v176 offset:1024
	ds_read_b128 v[172:175], v176 offset:2048
	ds_read_b128 v[176:179], v176 offset:3072
	ds_read_b128 v[180:183], v192
	ds_read_b128 v[184:187], v192 offset:1024
	ds_read_b128 v[188:191], v192 offset:2048
	ds_read_b128 v[192:195], v192 offset:3072
	s_add_u32 s48, s48, 0x20000
	s_addc_u32 s49, s49, 0
	s_mov_b32 m0, s60
	v_lshl_add_u64 v[234:235], s[48:49], 0, v[130:131]
	ds_read_b128 v[196:199], v159 offset:32768
	ds_read_b128 v[200:203], v159 offset:33792
	ds_read_b128 v[204:207], v159 offset:34816
	ds_read_b128 v[208:211], v159 offset:35840
	ds_read_b128 v[212:215], v159 offset:36864
	ds_read_b128 v[216:219], v159 offset:37888
	ds_read_b128 v[220:223], v159 offset:38912
	ds_read_b128 v[224:227], v159 offset:39936
	global_load_lds_dwordx4 v[234:235], off
	v_lshl_add_u64 v[234:235], s[48:49], 0, v[134:135]
	s_mov_b32 m0, s61
	s_nop 0
	global_load_lds_dwordx4 v[234:235], off
	s_waitcnt vmcnt(8)
	s_waitcnt lgkmcnt(0)
	s_barrier
	s_setprio 3
	s_waitcnt lgkmcnt(0)
	v_mfma_f32_16x16x32_bf16 v[54:57], v[164:167], v[196:199], v[54:57]
	v_mfma_f32_16x16x32_bf16 v[50:53], v[172:175], v[196:199], v[50:53]
	v_mfma_f32_16x16x32_bf16 v[70:73], v[164:167], v[204:207], v[70:73]
	v_mfma_f32_16x16x32_bf16 v[66:69], v[172:175], v[204:207], v[66:69]
	v_mfma_f32_16x16x32_bf16 v[78:81], v[164:167], v[212:215], v[78:81]
	v_mfma_f32_16x16x32_bf16 v[74:77], v[172:175], v[212:215], v[74:77]
	v_mfma_f32_16x16x32_bf16 v[86:89], v[164:167], v[220:223], v[86:89]
	v_mfma_f32_16x16x32_bf16 v[82:85], v[172:175], v[220:223], v[82:85]
	v_mfma_f32_16x16x32_bf16 v[54:57], v[168:171], v[200:203], v[54:57]
	v_mfma_f32_16x16x32_bf16 v[50:53], v[176:179], v[200:203], v[50:53]
	v_mfma_f32_16x16x32_bf16 v[70:73], v[168:171], v[208:211], v[70:73]
	v_mfma_f32_16x16x32_bf16 v[66:69], v[176:179], v[208:211], v[66:69]
	v_mfma_f32_16x16x32_bf16 v[78:81], v[168:171], v[216:219], v[78:81]
	v_mfma_f32_16x16x32_bf16 v[74:77], v[176:179], v[216:219], v[74:77]
	v_mfma_f32_16x16x32_bf16 v[86:89], v[168:171], v[224:227], v[86:89]
	v_mfma_f32_16x16x32_bf16 v[82:85], v[176:179], v[224:227], v[82:85]
	v_mfma_f32_16x16x32_bf16 v[14:17], v[180:183], v[196:199], v[14:17]
	v_mfma_f32_16x16x32_bf16 v[10:13], v[188:191], v[196:199], v[10:13]
	v_mfma_f32_16x16x32_bf16 v[22:25], v[180:183], v[204:207], v[22:25]
	v_mfma_f32_16x16x32_bf16 v[18:21], v[188:191], v[204:207], v[18:21]
	v_mfma_f32_16x16x32_bf16 v[30:33], v[180:183], v[212:215], v[30:33]
	v_mfma_f32_16x16x32_bf16 v[26:29], v[188:191], v[212:215], v[26:29]
	v_mfma_f32_16x16x32_bf16 v[46:49], v[180:183], v[220:223], v[46:49]
	v_mfma_f32_16x16x32_bf16 v[42:45], v[188:191], v[220:223], v[42:45]
	v_mfma_f32_16x16x32_bf16 v[14:17], v[184:187], v[200:203], v[14:17]
	v_mfma_f32_16x16x32_bf16 v[10:13], v[192:195], v[200:203], v[10:13]
	v_mfma_f32_16x16x32_bf16 v[22:25], v[184:187], v[208:211], v[22:25]
	v_mfma_f32_16x16x32_bf16 v[18:21], v[192:195], v[208:211], v[18:21]
	v_mfma_f32_16x16x32_bf16 v[30:33], v[184:187], v[216:219], v[30:33]
	v_mfma_f32_16x16x32_bf16 v[26:29], v[192:195], v[216:219], v[26:29]
	v_mfma_f32_16x16x32_bf16 v[46:49], v[184:187], v[224:227], v[46:49]
	v_mfma_f32_16x16x32_bf16 v[42:45], v[192:195], v[224:227], v[42:45]
	s_setprio 0
	s_barrier
; #define PG8_STAGE(bufoff, gbase, voff) do { _Pragma("unroll") for (int _i = 0; _i < 2; ++_i) \
;         __builtin_amdgcn_global_load_lds((const unsigned*)((const char*)(gbase) + (voff)[_i]), (PG8_LAS unsigned*)(lds + (bufoff) + ldsw + _i * 8192), 16, 0, 0); } while (0)
; #define PG8_LDA(dst, b, h) do { _Pragma("unroll") for (int m = 0; m < 4; ++m) Frag<F8>::load(dst[m], lds + PG8_SA(b, h) + aoff + m * 2048); } while (0)
; #define PG8_LDB(dst, b, h) do { _Pragma("unroll") for (int n = 0; n < 2; ++n) Frag<F8>::load(dst[n], lds + PG8_SB(b, h) + boff + n * 2048); } while (0)
; #define PG8_MMA(ai, bj, At, Bt) do { __builtin_amdgcn_s_setprio(3); _Pragma("unroll") for (int m = 0; m < 4; ++m) _Pragma("unroll") for (int n = 0; n < 2; ++n) Frag<F8>::mma(acc[ai][bj][m][n], Bt[n], At[m]); \
;         __builtin_amdgcn_s_setprio(0); } while (0)
; #define PG8_WAIT_V(n) asm volatile("s_waitcnt vmcnt(" #n ")" ::: "memory")
; #define PG8_WAIT_L(n) asm volatile("s_waitcnt lgkmcnt(" #n ")" ::: "memory")
; #define PG8_BAR __builtin_amdgcn_s_barrier()
; #define PG8_SCHED __builtin_amdgcn_sched_barrier(0)
; template <class Epi, class Sched, bool ALIGN_EPI = false, bool SP2 = false, bool F8 = false>
; __device__ __forceinline__ void gemm_phase(PG8_LAS unsigned char* lds, const Gemm g, const Sched& S, const Epi& E) {
;     ...
;             PG8_LDB(B0, 1, 0); PG8_SCHED; PG8_LDA(At, 1, 0); PG8_STAGE(PG8_SA(0, 1), a2 + hstep, voffA);
;             PG8_WAIT_L(8); PG8_BAR; PG8_WAIT_L(0); PG8_MMA(0, 0, At, B0); PG8_BAR; PG8_SCHED;
;             PG8_LDB(B1, 1, 1); PG8_STAGE(PG8_SB(1, 0), b3, voffB);
;             PG8_BAR; PG8_WAIT_L(0); PG8_MMA(0, 1, At, B1); PG8_BAR;
;             PG8_LDA(At, 1, 1); PG8_STAGE(PG8_SA(1, 0), a3, voffA);
;             PG8_BAR; PG8_WAIT_L(0); PG8_MMA(1, 0, At, B0); PG8_BAR; PG8_SCHED;
;             PG8_STAGE(PG8_SB(1, 1), b3 + hstep, voffB);
;             PG8_WAIT_V(6); PG8_BAR; PG8_MMA(1, 1, At, B1); PG8_BAR;
;             }
;         }
;         if constexpr (ALIGN_EPI) { if (wr == 0) PG8_BAR; }
	s_add_i32 s0, s0, s57
	v_lshl_add_u64 v[160:161], v[160:161], 0, s[22:23]
	s_mov_b32 m0, s0
	ds_read_b128 v[196:199], v159 offset:49152
	ds_read_b128 v[200:203], v159 offset:50176
	ds_read_b128 v[204:207], v159 offset:51200
	ds_read_b128 v[208:211], v159 offset:52224
	ds_read_b128 v[212:215], v159 offset:53248
	ds_read_b128 v[216:219], v159 offset:54272
	ds_read_b128 v[220:223], v159 offset:55296
	ds_read_b128 v[224:227], v159 offset:56320
	global_load_lds_dwordx4 v[160:161], off
	s_add_i32 m0, s0, 0x2000
	s_add_u32 s46, s46, 0x20080
	v_lshl_add_u64 v[160:161], v[228:229], 0, s[22:23]
	s_addc_u32 s47, s47, 0
	s_add_i32 s0, s1, s57
	global_load_lds_dwordx4 v[160:161], off
	v_lshl_add_u64 v[160:161], s[46:47], 0, v[132:133]
	s_mov_b32 m0, s0
	s_nop 0
	global_load_lds_dwordx4 v[160:161], off
	v_lshl_add_u64 v[160:161], s[46:47], 0, v[136:137]
	s_add_i32 m0, s0, 0x2000
	s_nop 0
	global_load_lds_dwordx4 v[160:161], off
	v_lshl_add_u64 v[160:161], v[230:231], 0, s[22:23]
	s_mov_b32 m0, s70
	s_nop 0
	global_load_lds_dwordx4 v[160:161], off
	v_lshl_add_u64 v[160:161], v[232:233], 0, s[22:23]
	s_mov_b32 m0, s71
	s_nop 0
	global_load_lds_dwordx4 v[160:161], off
	s_waitcnt vmcnt(8)
	s_waitcnt lgkmcnt(0)
	s_barrier
	s_setprio 3
	s_waitcnt lgkmcnt(0)
	v_mfma_f32_16x16x32_bf16 v[38:41], v[164:167], v[196:199], v[38:41]
	v_mfma_f32_16x16x32_bf16 v[34:37], v[172:175], v[196:199], v[34:37]
	v_mfma_f32_16x16x32_bf16 v[62:65], v[164:167], v[204:207], v[62:65]
	v_mfma_f32_16x16x32_bf16 v[58:61], v[172:175], v[204:207], v[58:61]
	v_mfma_f32_16x16x32_bf16 v[118:121], v[164:167], v[212:215], v[118:121]
	v_mfma_f32_16x16x32_bf16 v[114:117], v[172:175], v[212:215], v[114:117]
	v_mfma_f32_16x16x32_bf16 v[126:129], v[164:167], v[220:223], v[126:129]
	v_mfma_f32_16x16x32_bf16 v[122:125], v[172:175], v[220:223], v[122:125]
	v_mfma_f32_16x16x32_bf16 v[38:41], v[168:171], v[200:203], v[38:41]
	v_mfma_f32_16x16x32_bf16 v[34:37], v[176:179], v[200:203], v[34:37]
	v_mfma_f32_16x16x32_bf16 v[62:65], v[168:171], v[208:211], v[62:65]
	v_mfma_f32_16x16x32_bf16 v[58:61], v[176:179], v[208:211], v[58:61]
	v_mfma_f32_16x16x32_bf16 v[118:121], v[168:171], v[216:219], v[118:121]
	v_mfma_f32_16x16x32_bf16 v[114:117], v[176:179], v[216:219], v[114:117]
	v_mfma_f32_16x16x32_bf16 v[126:129], v[168:171], v[224:227], v[126:129]
	v_mfma_f32_16x16x32_bf16 v[122:125], v[176:179], v[224:227], v[122:125]
	v_mfma_f32_16x16x32_bf16 v[6:9], v[180:183], v[196:199], v[6:9]
	v_mfma_f32_16x16x32_bf16 v[2:5], v[188:191], v[196:199], v[2:5]
	v_mfma_f32_16x16x32_bf16 v[94:97], v[180:183], v[204:207], v[94:97]
	v_mfma_f32_16x16x32_bf16 v[90:93], v[188:191], v[204:207], v[90:93]
	v_mfma_f32_16x16x32_bf16 v[102:105], v[180:183], v[212:215], v[102:105]
	v_mfma_f32_16x16x32_bf16 v[98:101], v[188:191], v[212:215], v[98:101]
	v_mfma_f32_16x16x32_bf16 v[110:113], v[180:183], v[220:223], v[110:113]
	v_mfma_f32_16x16x32_bf16 v[106:109], v[188:191], v[220:223], v[106:109]
	v_mfma_f32_16x16x32_bf16 v[6:9], v[184:187], v[200:203], v[6:9]
	v_mfma_f32_16x16x32_bf16 v[2:5], v[192:195], v[200:203], v[2:5]
	v_mfma_f32_16x16x32_bf16 v[94:97], v[184:187], v[208:211], v[94:97]
	v_mfma_f32_16x16x32_bf16 v[90:93], v[192:195], v[208:211], v[90:93]
	v_mfma_f32_16x16x32_bf16 v[102:105], v[184:187], v[216:219], v[102:105]
	v_mfma_f32_16x16x32_bf16 v[98:101], v[192:195], v[216:219], v[98:101]
	v_mfma_f32_16x16x32_bf16 v[110:113], v[184:187], v[224:227], v[110:113]
	v_mfma_f32_16x16x32_bf16 v[106:109], v[192:195], v[224:227], v[106:109]
	s_setprio 0
	s_barrier
	s_add_i32 s33, s33, 2
	s_add_u32 s44, s44, 0x100
	s_addc_u32 s45, s45, 0
	s_cmp_gt_u32 s33, 5
	s_cbranch_scc0 .LBB0_1066
	s_and_b64 vcc, exec, s[24:25]
	s_cbranch_vccz .LBB0_1069
	s_barrier

; #define PG8_STAGE(bufoff, gbase, voff) do { _Pragma("unroll") for (int _i = 0; _i < 2; ++_i) \
;         __builtin_amdgcn_global_load_lds((const unsigned*)((const char*)(gbase) + (voff)[_i]), (PG8_LAS unsigned*)(lds + (bufoff) + ldsw + _i * 8192), 16, 0, 0); } while (0)
; #define PG8_LDA(dst, b, h) do { _Pragma("unroll") for (int m = 0; m < 4; ++m) Frag<F8>::load(dst[m], lds + PG8_SA(b, h) + aoff + m * 2048); } while (0)
; #define PG8_BAR __builtin_amdgcn_s_barrier()
; template <class Epi, class Sched, bool ALIGN_EPI = false, bool SP2 = false, bool F8 = false>
; __device__ __forceinline__ void gemm_phase(PG8_LAS unsigned char* lds, const Gemm g, const Sched& S, const Epi& E) {
;     ...
;         const bool has_next = S.next(ui + 1, nxt);
;         const char* nA = has_next ? (const char*)g.A + (size_t)nxt.pm * tstep + nxt.ko : cA; const char* nB = has_next ? (const char*)g.Bt + (size_t)nxt.pn * tstep + nxt.ko : cB;
;         for (int t = 0; t < nt; t += 2) {
;             const bool last = (t == nt - 2);
;             const char* a1 = cA + (size_t)(t + 1) * kstep;
;             const char* a2 = last ? nA : cA + (size_t)(t + 2) * kstep; const char* b2 = last ? nB : cB + (size_t)(t + 2) * kstep;
;             const char* a3 = a2 + kstep; const char* b3 = b2 + kstep;
;             if (last && has_next) S.a_ready(nxt);
;             if constexpr (SP2) {
;             PG8_LDB(B0, 0, 0); PG8_LDB(B1, 0, 1); PG8_SCHED; PG8_LDA(At, 0, 0); PG8_STAGE(PG8_SA(1, 1), a1 + hstep, voffA);
;             PG8_WAIT_V(8); PG8_WAIT_L(0); PG8_BAR; PG8_MMA(0, 0, At, B0); PG8_MMA(0, 1, At, B1); PG8_BAR; PG8_SCHED;
;             PG8_LDA(At, 0, 1); PG8_STAGE(PG8_SB(0, 0), b2, voffB); PG8_STAGE(PG8_SB(0, 1), b2 + hstep, voffB); PG8_STAGE(PG8_SA(0, 0), a2, voffA);
;             PG8_WAIT_V(8); PG8_WAIT_L(0); PG8_BAR; PG8_MMA(1, 0, At, B0); PG8_MMA(1, 1, At, B1); PG8_BAR; PG8_SCHED;
;             PG8_LDB(B0, 1, 0); PG8_LDB(B1, 1, 1); PG8_SCHED; PG8_LDA(At, 1, 0); PG8_STAGE(PG8_SA(0, 1), a2 + hstep, voffA);
;             PG8_WAIT_V(8); PG8_WAIT_L(0); PG8_BAR; PG8_MMA(0, 0, At, B0); PG8_MMA(0, 1, At, B1); PG8_BAR; PG8_SCHED;
;             PG8_LDA(At, 1, 1); PG8_STAGE(PG8_SB(1, 0), b3, voffB); PG8_STAGE(PG8_SB(1, 1), b3 + hstep, voffB); PG8_STAGE(PG8_SA(1, 0), a3, voffA);
;             PG8_WAIT_V(8); PG8_WAIT_L(0); PG8_BAR; PG8_MMA(1, 0, At, B0); PG8_MMA(1, 1, At, B1); PG8_BAR; PG8_SCHED;
.LBB0_1309:
	s_ashr_i32 s25, s24, 31
	s_lshl_b64 s[4:5], s[24:25], 18
	s_add_u32 s30, s48, s4
	s_addc_u32 s31, s49, s5
	s_and_b64 s[4:5], s[22:23], exec
	s_cselect_b32 s25, s31, s43
	s_cselect_b32 s77, s30, s42
	s_ashr_i32 s27, s26, 31
	s_lshl_b64 s[4:5], s[26:27], 18
	s_add_u32 s36, s50, s4
	s_addc_u32 s37, s51, s5
	s_and_b64 s[4:5], s[22:23], exec
	s_cselect_b32 s27, s37, s45
	s_cselect_b32 s78, s36, s44
	s_add_u32 s42, s42, 0x20080
	s_addc_u32 s43, s43, 0
	s_add_u32 s79, s44, 0x100
	s_addc_u32 s80, s45, 0
	s_mov_b32 s81, -2
	ds_read_b128 v[18:21], v186
	ds_read_b128 v[22:25], v186 offset:1024
	ds_read_b128 v[26:29], v186 offset:2048
	ds_read_b128 v[30:33], v186 offset:3072
	ds_read_b128 v[2:5], v187
	ds_read_b128 v[6:9], v187 offset:1024
	ds_read_b128 v[10:13], v187 offset:2048
	ds_read_b128 v[14:17], v187 offset:3072
	s_add_u32 s0, s42, 0xfffe0080
	s_addc_u32 s1, s43, -1
	s_cmp_eq_u32 s81, 4
	s_cselect_b32 s47, s25, s1
	s_cselect_b32 s46, s77, s0
	s_cselect_b32 s45, s27, s80
	s_cselect_b32 s44, s78, s79
	v_lshl_add_u64 v[214:215], s[42:43], 0, v[172:173]
	s_add_i32 m0, s39, 0xc000
	ds_read_b128 v[176:179], v188
	ds_read_b128 v[180:183], v188 offset:1024
	ds_read_b128 v[190:193], v188 offset:2048
	ds_read_b128 v[194:197], v188 offset:3072
	ds_read_b128 v[198:201], v188 offset:4096
	ds_read_b128 v[202:205], v188 offset:5120
	ds_read_b128 v[206:209], v188 offset:6144
	ds_read_b128 v[210:213], v188 offset:7168
	global_load_lds_dwordx4 v[214:215], off
	v_lshl_add_u64 v[214:215], s[42:43], 0, v[174:175]
	s_add_i32 m0, s39, 0xe000
	s_nop 0
	global_load_lds_dwordx4 v[214:215], off
	s_waitcnt vmcnt(8)
	s_waitcnt lgkmcnt(0)
	s_barrier
	s_setprio 3
	s_waitcnt lgkmcnt(0)
	v_mfma_f32_16x16x128_f8f6f4 v[158:161], v[18:25], v[176:183], 0
	v_mfma_f32_16x16x128_f8f6f4 v[150:153], v[26:33], v[176:183], 0
	v_mfma_f32_16x16x128_f8f6f4 v[142:145], v[18:25], v[190:197], 0
	v_mfma_f32_16x16x128_f8f6f4 v[134:137], v[26:33], v[190:197], 0
	v_mfma_f32_16x16x128_f8f6f4 v[126:129], v[18:25], v[198:205], 0
	v_mfma_f32_16x16x128_f8f6f4 v[118:121], v[26:33], v[198:205], 0
	v_mfma_f32_16x16x128_f8f6f4 v[110:113], v[18:25], v[206:213], 0
	v_mfma_f32_16x16x128_f8f6f4 v[102:105], v[26:33], v[206:213], 0
	v_mfma_f32_16x16x128_f8f6f4 v[154:157], v[2:9], v[176:183], 0
	v_mfma_f32_16x16x128_f8f6f4 v[146:149], v[10:17], v[176:183], 0
	v_mfma_f32_16x16x128_f8f6f4 v[138:141], v[2:9], v[190:197], 0
	v_mfma_f32_16x16x128_f8f6f4 v[130:133], v[10:17], v[190:197], 0
	v_mfma_f32_16x16x128_f8f6f4 v[122:125], v[2:9], v[198:205], 0
	v_mfma_f32_16x16x128_f8f6f4 v[114:117], v[10:17], v[198:205], 0
	v_mfma_f32_16x16x128_f8f6f4 v[106:109], v[2:9], v[206:213], 0
	v_mfma_f32_16x16x128_f8f6f4 v[98:101], v[10:17], v[206:213], 0
	s_setprio 0
	s_barrier
	s_add_i32 s0, s74, s52
	v_lshl_add_u64 v[176:177], s[44:45], 0, v[168:169]
	s_mov_b32 m0, s0
	ds_read_b128 v[190:193], v188 offset:16384
	ds_read_b128 v[194:197], v188 offset:17408
	ds_read_b128 v[198:201], v188 offset:18432
	ds_read_b128 v[202:205], v188 offset:19456
	ds_read_b128 v[206:209], v188 offset:20480
	ds_read_b128 v[210:213], v188 offset:21504
	ds_read_b128 v[214:217], v188 offset:22528
	ds_read_b128 v[218:221], v188 offset:23552
	global_load_lds_dwordx4 v[176:177], off
	s_add_i32 m0, s0, 0x2000
	s_add_u32 s4, s44, 0x20000
	v_lshl_add_u64 v[178:179], s[44:45], 0, v[164:165]
	s_addc_u32 s5, s45, 0
	s_add_i32 s0, s75, s52
	global_load_lds_dwordx4 v[178:179], off
	v_lshl_add_u64 v[180:181], s[4:5], 0, v[168:169]
	s_mov_b32 m0, s0
	v_lshl_add_u64 v[182:183], s[46:47], 0, v[166:167]
	global_load_lds_dwordx4 v[180:181], off
	v_lshl_add_u64 v[180:181], s[4:5], 0, v[164:165]
	s_add_i32 m0, s0, 0x2000
	s_nop 0
	global_load_lds_dwordx4 v[180:181], off
	v_lshl_add_u64 v[180:181], s[46:47], 0, v[170:171]
	s_mov_b32 m0, s39
	s_nop 0
	global_load_lds_dwordx4 v[180:181], off
	s_mov_b32 m0, s41
	s_nop 0
	global_load_lds_dwordx4 v[182:183], off
	s_waitcnt vmcnt(8)
	s_waitcnt lgkmcnt(0)
	s_barrier
	s_setprio 3
	s_waitcnt lgkmcnt(0)
	v_mfma_f32_16x16x128_f8f6f4 v[94:97], v[18:25], v[190:197], 0
	v_mfma_f32_16x16x128_f8f6f4 v[86:89], v[26:33], v[190:197], 0
	v_mfma_f32_16x16x128_f8f6f4 v[78:81], v[18:25], v[198:205], 0
	v_mfma_f32_16x16x128_f8f6f4 v[70:73], v[26:33], v[198:205], 0
	v_mfma_f32_16x16x128_f8f6f4 v[62:65], v[18:25], v[206:213], 0
	v_mfma_f32_16x16x128_f8f6f4 v[54:57], v[26:33], v[206:213], 0
	v_mfma_f32_16x16x128_f8f6f4 v[46:49], v[18:25], v[214:221], 0
	v_mfma_f32_16x16x128_f8f6f4 v[38:41], v[26:33], v[214:221], 0
	v_mfma_f32_16x16x128_f8f6f4 v[90:93], v[2:9], v[190:197], 0
	v_mfma_f32_16x16x128_f8f6f4 v[82:85], v[10:17], v[190:197], 0
	v_mfma_f32_16x16x128_f8f6f4 v[74:77], v[2:9], v[198:205], 0
	v_mfma_f32_16x16x128_f8f6f4 v[66:69], v[10:17], v[198:205], 0
	v_mfma_f32_16x16x128_f8f6f4 v[58:61], v[2:9], v[206:213], 0
	v_mfma_f32_16x16x128_f8f6f4 v[50:53], v[10:17], v[206:213], 0
	v_mfma_f32_16x16x128_f8f6f4 v[42:45], v[2:9], v[214:221], 0
	v_mfma_f32_16x16x128_f8f6f4 v[34:37], v[10:17], v[214:221], 0
	s_setprio 0
	s_barrier
	s_add_i32 s0, 0, 0x18000
	s_add_i32 s1, 0, 0x1c000
	v_add_u32_e32 v14, s0, v184
	v_add_u32_e32 v30, s1, v184
	ds_read_b128 v[2:5], v14
	ds_read_b128 v[6:9], v14 offset:1024
	ds_read_b128 v[10:13], v14 offset:2048
	ds_read_b128 v[14:17], v14 offset:3072
	ds_read_b128 v[18:21], v30
	ds_read_b128 v[22:25], v30 offset:1024
	ds_read_b128 v[26:29], v30 offset:2048
	ds_read_b128 v[30:33], v30 offset:3072
	s_add_u32 s4, s46, 0x20000
	s_addc_u32 s5, s47, 0
	s_mov_b32 m0, s58
	v_lshl_add_u64 v[222:223], s[4:5], 0, v[170:171]
	ds_read_b128 v[190:193], v188 offset:32768
	ds_read_b128 v[194:197], v188 offset:33792
	ds_read_b128 v[198:201], v188 offset:34816
	ds_read_b128 v[202:205], v188 offset:35840
	ds_read_b128 v[206:209], v188 offset:36864
	ds_read_b128 v[210:213], v188 offset:37888
	ds_read_b128 v[214:217], v188 offset:38912
	ds_read_b128 v[218:221], v188 offset:39936
	global_load_lds_dwordx4 v[222:223], off
	v_lshl_add_u64 v[222:223], s[4:5], 0, v[166:167]
	s_mov_b32 m0, s59
	s_nop 0
	global_load_lds_dwordx4 v[222:223], off
	s_waitcnt vmcnt(8)
	s_waitcnt lgkmcnt(0)
	s_barrier
; #define PG8_STAGE(bufoff, gbase, voff) do { _Pragma("unroll") for (int _i = 0; _i < 2; ++_i) \
;         __builtin_amdgcn_global_load_lds((const unsigned*)((const char*)(gbase) + (voff)[_i]), (PG8_LAS unsigned*)(lds + (bufoff) + ldsw + _i * 8192), 16, 0, 0); } while (0)
; #define PG8_LDA(dst, b, h) do { _Pragma("unroll") for (int m = 0; m < 4; ++m) Frag<F8>::load(dst[m], lds + PG8_SA(b, h) + aoff + m * 2048); } while (0)
; #define PG8_LDB(dst, b, h) do { _Pragma("unroll") for (int n = 0; n < 2; ++n) Frag<F8>::load(dst[n], lds + PG8_SB(b, h) + boff + n * 2048); } while (0)
; #define PG8_MMA(ai, bj, At, Bt) do { __builtin_amdgcn_s_setprio(3); _Pragma("unroll") for (int m = 0; m < 4; ++m) _Pragma("unroll") for (int n = 0; n < 2; ++n) Frag<F8>::mma(acc[ai][bj][m][n], Bt[n], At[m]); \
;         __builtin_amdgcn_s_setprio(0); } while (0)
; #define PG8_WAIT_V(n) asm volatile("s_waitcnt vmcnt(" #n ")" ::: "memory")
; #define PG8_WAIT_L(n) asm volatile("s_waitcnt lgkmcnt(" #n ")" ::: "memory")
; #define PG8_BAR __builtin_amdgcn_s_barrier()
; #define PG8_SCHED __builtin_amdgcn_sched_barrier(0)
; template <class Epi, class Sched, bool ALIGN_EPI = false, bool SP2 = false, bool F8 = false>
; __device__ __forceinline__ void gemm_phase(PG8_LAS unsigned char* lds, const Gemm g, const Sched& S, const Epi& E) {
;     ...
;             PG8_WAIT_V(8); PG8_WAIT_L(0); PG8_BAR; PG8_MMA(1, 0, At, B0); PG8_MMA(1, 1, At, B1); PG8_BAR; PG8_SCHED;
;             PG8_LDB(B0, 1, 0); PG8_LDB(B1, 1, 1); PG8_SCHED; PG8_LDA(At, 1, 0); PG8_STAGE(PG8_SA(0, 1), a2 + hstep, voffA);
;             PG8_WAIT_V(8); PG8_WAIT_L(0); PG8_BAR; PG8_MMA(0, 0, At, B0); PG8_MMA(0, 1, At, B1); PG8_BAR; PG8_SCHED;
;             PG8_LDA(At, 1, 1); PG8_STAGE(PG8_SB(1, 0), b3, voffB); PG8_STAGE(PG8_SB(1, 1), b3 + hstep, voffB); PG8_STAGE(PG8_SA(1, 0), a3, voffA);
;             PG8_WAIT_V(8); PG8_WAIT_L(0); PG8_BAR; PG8_MMA(1, 0, At, B0); PG8_MMA(1, 1, At, B1); PG8_BAR; PG8_SCHED;
	s_setprio 3
	s_waitcnt lgkmcnt(0)
	v_mfma_f32_16x16x128_f8f6f4 v[158:161], v[2:9], v[190:197], v[158:161]
	v_mfma_f32_16x16x128_f8f6f4 v[150:153], v[10:17], v[190:197], v[150:153]
	v_mfma_f32_16x16x128_f8f6f4 v[142:145], v[2:9], v[198:205], v[142:145]
	v_mfma_f32_16x16x128_f8f6f4 v[134:137], v[10:17], v[198:205], v[134:137]
	v_mfma_f32_16x16x128_f8f6f4 v[126:129], v[2:9], v[206:213], v[126:129]
	v_mfma_f32_16x16x128_f8f6f4 v[118:121], v[10:17], v[206:213], v[118:121]
	v_mfma_f32_16x16x128_f8f6f4 v[110:113], v[2:9], v[214:221], v[110:113]
	v_mfma_f32_16x16x128_f8f6f4 v[102:105], v[10:17], v[214:221], v[102:105]
	v_mfma_f32_16x16x128_f8f6f4 v[154:157], v[18:25], v[190:197], v[154:157]
	v_mfma_f32_16x16x128_f8f6f4 v[146:149], v[26:33], v[190:197], v[146:149]
	v_mfma_f32_16x16x128_f8f6f4 v[138:141], v[18:25], v[198:205], v[138:141]
	v_mfma_f32_16x16x128_f8f6f4 v[130:133], v[26:33], v[198:205], v[130:133]
	v_mfma_f32_16x16x128_f8f6f4 v[122:125], v[18:25], v[206:213], v[122:125]
	v_mfma_f32_16x16x128_f8f6f4 v[114:117], v[26:33], v[206:213], v[114:117]
	v_mfma_f32_16x16x128_f8f6f4 v[106:109], v[18:25], v[214:221], v[106:109]
	v_mfma_f32_16x16x128_f8f6f4 v[98:101], v[26:33], v[214:221], v[98:101]
	s_setprio 0
	s_barrier
	s_add_i32 s0, s0, s52
	v_lshl_add_u64 v[176:177], v[176:177], 0, s[14:15]
	s_mov_b32 m0, s0
	ds_read_b128 v[190:193], v188 offset:49152
	ds_read_b128 v[194:197], v188 offset:50176
	ds_read_b128 v[198:201], v188 offset:51200
	ds_read_b128 v[202:205], v188 offset:52224
	ds_read_b128 v[206:209], v188 offset:53248
	ds_read_b128 v[210:213], v188 offset:54272
	ds_read_b128 v[214:217], v188 offset:55296
	ds_read_b128 v[218:221], v188 offset:56320
	global_load_lds_dwordx4 v[176:177], off
	s_add_i32 m0, s0, 0x2000
	s_add_u32 s4, s44, 0x20080
	v_lshl_add_u64 v[176:177], v[178:179], 0, s[14:15]
	s_addc_u32 s5, s45, 0
	s_add_i32 s0, s1, s52
	global_load_lds_dwordx4 v[176:177], off
	v_lshl_add_u64 v[176:177], s[4:5], 0, v[168:169]
	s_mov_b32 m0, s0
	s_nop 0
	global_load_lds_dwordx4 v[176:177], off
	v_lshl_add_u64 v[176:177], s[4:5], 0, v[164:165]
	s_add_i32 m0, s0, 0x2000
	s_nop 0
	global_load_lds_dwordx4 v[176:177], off
	v_lshl_add_u64 v[176:177], v[180:181], 0, s[14:15]
	s_mov_b32 m0, s60
	s_nop 0
	global_load_lds_dwordx4 v[176:177], off
	v_lshl_add_u64 v[176:177], v[182:183], 0, s[14:15]
	s_mov_b32 m0, s61
	s_nop 0
	global_load_lds_dwordx4 v[176:177], off
	s_waitcnt vmcnt(8)
	s_waitcnt lgkmcnt(0)
	s_barrier
	s_setprio 3
	s_waitcnt lgkmcnt(0)
	v_mfma_f32_16x16x128_f8f6f4 v[94:97], v[2:9], v[190:197], v[94:97]
	v_mfma_f32_16x16x128_f8f6f4 v[86:89], v[10:17], v[190:197], v[86:89]
	v_mfma_f32_16x16x128_f8f6f4 v[78:81], v[2:9], v[198:205], v[78:81]
	v_mfma_f32_16x16x128_f8f6f4 v[70:73], v[10:17], v[198:205], v[70:73]
	v_mfma_f32_16x16x128_f8f6f4 v[62:65], v[2:9], v[206:213], v[62:65]
	v_mfma_f32_16x16x128_f8f6f4 v[54:57], v[10:17], v[206:213], v[54:57]
	v_mfma_f32_16x16x128_f8f6f4 v[46:49], v[2:9], v[214:221], v[46:49]
	v_mfma_f32_16x16x128_f8f6f4 v[38:41], v[10:17], v[214:221], v[38:41]
	v_mfma_f32_16x16x128_f8f6f4 v[90:93], v[18:25], v[190:197], v[90:93]
	v_mfma_f32_16x16x128_f8f6f4 v[82:85], v[26:33], v[190:197], v[82:85]
	v_mfma_f32_16x16x128_f8f6f4 v[74:77], v[18:25], v[198:205], v[74:77]
	v_mfma_f32_16x16x128_f8f6f4 v[66:69], v[26:33], v[198:205], v[66:69]
	v_mfma_f32_16x16x128_f8f6f4 v[58:61], v[18:25], v[206:213], v[58:61]
	v_mfma_f32_16x16x128_f8f6f4 v[50:53], v[26:33], v[206:213], v[50:53]
	v_mfma_f32_16x16x128_f8f6f4 v[42:45], v[18:25], v[214:221], v[42:45]
	v_mfma_f32_16x16x128_f8f6f4 v[34:37], v[26:33], v[214:221], v[34:37]
	s_setprio 0
	s_barrier
	s_add_i32 s81, s81, 2
	s_add_u32 s42, s42, 0x100
	s_addc_u32 s43, s43, 0
	s_add_u32 s79, s79, 0x100
	s_addc_u32 s80, s80, 0
	s_cmp_gt_u32 s81, 5
	s_cbranch_scc1 .Lpeel_exit_3
.LBB0_1310:
	ds_read_b128 v[18:21], v186
	ds_read_b128 v[22:25], v186 offset:1024
	ds_read_b128 v[26:29], v186 offset:2048
	ds_read_b128 v[30:33], v186 offset:3072
	ds_read_b128 v[2:5], v187
	ds_read_b128 v[6:9], v187 offset:1024
	ds_read_b128 v[10:13], v187 offset:2048
	ds_read_b128 v[14:17], v187 offset:3072
	s_add_u32 s0, s42, 0xfffe0080
	s_addc_u32 s1, s43, -1
	s_cmp_eq_u32 s81, 4
	s_cselect_b32 s47, s25, s1
	s_cselect_b32 s46, s77, s0
	s_cselect_b32 s45, s27, s80
	s_cselect_b32 s44, s78, s79
	v_lshl_add_u64 v[214:215], s[42:43], 0, v[172:173]
	s_add_i32 m0, s39, 0xc000
	ds_read_b128 v[176:179], v188
	ds_read_b128 v[180:183], v188 offset:1024
	ds_read_b128 v[190:193], v188 offset:2048
	ds_read_b128 v[194:197], v188 offset:3072
	ds_read_b128 v[198:201], v188 offset:4096
	ds_read_b128 v[202:205], v188 offset:5120
	ds_read_b128 v[206:209], v188 offset:6144
	ds_read_b128 v[210:213], v188 offset:7168
	global_load_lds_dwordx4 v[214:215], off
	v_lshl_add_u64 v[214:215], s[42:43], 0, v[174:175]
	s_add_i32 m0, s39, 0xe000
	s_nop 0
	global_load_lds_dwordx4 v[214:215], off
	s_waitcnt vmcnt(8)
	s_waitcnt lgkmcnt(0)
	s_barrier
	s_setprio 3
	s_waitcnt lgkmcnt(0)
	v_mfma_f32_16x16x128_f8f6f4 v[158:161], v[18:25], v[176:183], v[158:161]
	v_mfma_f32_16x16x128_f8f6f4 v[150:153], v[26:33], v[176:183], v[150:153]
	v_mfma_f32_16x16x128_f8f6f4 v[142:145], v[18:25], v[190:197], v[142:145]
	v_mfma_f32_16x16x128_f8f6f4 v[134:137], v[26:33], v[190:197], v[134:137]
	v_mfma_f32_16x16x128_f8f6f4 v[126:129], v[18:25], v[198:205], v[126:129]
	v_mfma_f32_16x16x128_f8f6f4 v[118:121], v[26:33], v[198:205], v[118:121]
	v_mfma_f32_16x16x128_f8f6f4 v[110:113], v[18:25], v[206:213], v[110:113]
	v_mfma_f32_16x16x128_f8f6f4 v[102:105], v[26:33], v[206:213], v[102:105]
	v_mfma_f32_16x16x128_f8f6f4 v[154:157], v[2:9], v[176:183], v[154:157]
	v_mfma_f32_16x16x128_f8f6f4 v[146:149], v[10:17], v[176:183], v[146:149]
	v_mfma_f32_16x16x128_f8f6f4 v[138:141], v[2:9], v[190:197], v[138:141]
	v_mfma_f32_16x16x128_f8f6f4 v[130:133], v[10:17], v[190:197], v[130:133]
	v_mfma_f32_16x16x128_f8f6f4 v[122:125], v[2:9], v[198:205], v[122:125]
	v_mfma_f32_16x16x128_f8f6f4 v[114:117], v[10:17], v[198:205], v[114:117]
	v_mfma_f32_16x16x128_f8f6f4 v[106:109], v[2:9], v[206:213], v[106:109]
	v_mfma_f32_16x16x128_f8f6f4 v[98:101], v[10:17], v[206:213], v[98:101]
	s_setprio 0
	s_barrier
; #define PG8_STAGE(bufoff, gbase, voff) do { _Pragma("unroll") for (int _i = 0; _i < 2; ++_i) \
;         __builtin_amdgcn_global_load_lds((const unsigned*)((const char*)(gbase) + (voff)[_i]), (PG8_LAS unsigned*)(lds + (bufoff) + ldsw + _i * 8192), 16, 0, 0); } while (0)
; #define PG8_LDA(dst, b, h) do { _Pragma("unroll") for (int m = 0; m < 4; ++m) Frag<F8>::load(dst[m], lds + PG8_SA(b, h) + aoff + m * 2048); } while (0)
; #define PG8_LDB(dst, b, h) do { _Pragma("unroll") for (int n = 0; n < 2; ++n) Frag<F8>::load(dst[n], lds + PG8_SB(b, h) + boff + n * 2048); } while (0)
; #define PG8_MMA(ai, bj, At, Bt) do { __builtin_amdgcn_s_setprio(3); _Pragma("unroll") for (int m = 0; m < 4; ++m) _Pragma("unroll") for (int n = 0; n < 2; ++n) Frag<F8>::mma(acc[ai][bj][m][n], Bt[n], At[m]); \
;         __builtin_amdgcn_s_setprio(0); } while (0)
; #define PG8_WAIT_V(n) asm volatile("s_waitcnt vmcnt(" #n ")" ::: "memory")
; #define PG8_WAIT_L(n) asm volatile("s_waitcnt lgkmcnt(" #n ")" ::: "memory")
; #define PG8_BAR __builtin_amdgcn_s_barrier()
; #define PG8_SCHED __builtin_amdgcn_sched_barrier(0)
; template <class Epi, class Sched, bool ALIGN_EPI = false, bool SP2 = false, bool F8 = false>
; __device__ __forceinline__ void gemm_phase(PG8_LAS unsigned char* lds, const Gemm g, const Sched& S, const Epi& E) {
;     ...
;             PG8_LDB(B0, 1, 0); PG8_LDB(B1, 1, 1); PG8_SCHED; PG8_LDA(At, 1, 0); PG8_STAGE(PG8_SA(0, 1), a2 + hstep, voffA);
;             PG8_WAIT_V(8); PG8_WAIT_L(0); PG8_BAR; PG8_MMA(0, 0, At, B0); PG8_MMA(0, 1, At, B1); PG8_BAR; PG8_SCHED;
;             PG8_LDA(At, 1, 1); PG8_STAGE(PG8_SB(1, 0), b3, voffB); PG8_STAGE(PG8_SB(1, 1), b3 + hstep, voffB); PG8_STAGE(PG8_SA(1, 0), a3, voffA);
;             PG8_WAIT_V(8); PG8_WAIT_L(0); PG8_BAR; PG8_MMA(1, 0, At, B0); PG8_MMA(1, 1, At, B1); PG8_BAR; PG8_SCHED;
	s_add_i32 s0, s74, s52
	v_lshl_add_u64 v[176:177], s[44:45], 0, v[168:169]
	s_mov_b32 m0, s0
	ds_read_b128 v[190:193], v188 offset:16384
	ds_read_b128 v[194:197], v188 offset:17408
	ds_read_b128 v[198:201], v188 offset:18432
	ds_read_b128 v[202:205], v188 offset:19456
	ds_read_b128 v[206:209], v188 offset:20480
	ds_read_b128 v[210:213], v188 offset:21504
	ds_read_b128 v[214:217], v188 offset:22528
	ds_read_b128 v[218:221], v188 offset:23552
	global_load_lds_dwordx4 v[176:177], off
	s_add_i32 m0, s0, 0x2000
	s_add_u32 s4, s44, 0x20000
	v_lshl_add_u64 v[178:179], s[44:45], 0, v[164:165]
	s_addc_u32 s5, s45, 0
	s_add_i32 s0, s75, s52
	global_load_lds_dwordx4 v[178:179], off
	v_lshl_add_u64 v[180:181], s[4:5], 0, v[168:169]
	s_mov_b32 m0, s0
	v_lshl_add_u64 v[182:183], s[46:47], 0, v[166:167]
	global_load_lds_dwordx4 v[180:181], off
	v_lshl_add_u64 v[180:181], s[4:5], 0, v[164:165]
	s_add_i32 m0, s0, 0x2000
	s_nop 0
	global_load_lds_dwordx4 v[180:181], off
	v_lshl_add_u64 v[180:181], s[46:47], 0, v[170:171]
	s_mov_b32 m0, s39
	s_nop 0
	global_load_lds_dwordx4 v[180:181], off
	s_mov_b32 m0, s41
	s_nop 0
	global_load_lds_dwordx4 v[182:183], off
	s_waitcnt vmcnt(8)
	s_waitcnt lgkmcnt(0)
	s_barrier
	s_setprio 3
	s_waitcnt lgkmcnt(0)
	v_mfma_f32_16x16x128_f8f6f4 v[94:97], v[18:25], v[190:197], v[94:97]
	v_mfma_f32_16x16x128_f8f6f4 v[86:89], v[26:33], v[190:197], v[86:89]
	v_mfma_f32_16x16x128_f8f6f4 v[78:81], v[18:25], v[198:205], v[78:81]
	v_mfma_f32_16x16x128_f8f6f4 v[70:73], v[26:33], v[198:205], v[70:73]
	v_mfma_f32_16x16x128_f8f6f4 v[62:65], v[18:25], v[206:213], v[62:65]
	v_mfma_f32_16x16x128_f8f6f4 v[54:57], v[26:33], v[206:213], v[54:57]
	v_mfma_f32_16x16x128_f8f6f4 v[46:49], v[18:25], v[214:221], v[46:49]
	v_mfma_f32_16x16x128_f8f6f4 v[38:41], v[26:33], v[214:221], v[38:41]
	v_mfma_f32_16x16x128_f8f6f4 v[90:93], v[2:9], v[190:197], v[90:93]
	v_mfma_f32_16x16x128_f8f6f4 v[82:85], v[10:17], v[190:197], v[82:85]
	v_mfma_f32_16x16x128_f8f6f4 v[74:77], v[2:9], v[198:205], v[74:77]
	v_mfma_f32_16x16x128_f8f6f4 v[66:69], v[10:17], v[198:205], v[66:69]
	v_mfma_f32_16x16x128_f8f6f4 v[58:61], v[2:9], v[206:213], v[58:61]
	v_mfma_f32_16x16x128_f8f6f4 v[50:53], v[10:17], v[206:213], v[50:53]
	v_mfma_f32_16x16x128_f8f6f4 v[42:45], v[2:9], v[214:221], v[42:45]
	v_mfma_f32_16x16x128_f8f6f4 v[34:37], v[10:17], v[214:221], v[34:37]
	s_setprio 0
	s_barrier
	s_add_i32 s0, 0, 0x18000
	s_add_i32 s1, 0, 0x1c000
	v_add_u32_e32 v14, s0, v184
	v_add_u32_e32 v30, s1, v184
	ds_read_b128 v[2:5], v14
	ds_read_b128 v[6:9], v14 offset:1024
	ds_read_b128 v[10:13], v14 offset:2048
	ds_read_b128 v[14:17], v14 offset:3072
	ds_read_b128 v[18:21], v30
	ds_read_b128 v[22:25], v30 offset:1024
	ds_read_b128 v[26:29], v30 offset:2048
	ds_read_b128 v[30:33], v30 offset:3072
	s_add_u32 s4, s46, 0x20000
	s_addc_u32 s5, s47, 0
	s_mov_b32 m0, s58
	v_lshl_add_u64 v[222:223], s[4:5], 0, v[170:171]
	ds_read_b128 v[190:193], v188 offset:32768
	ds_read_b128 v[194:197], v188 offset:33792
	ds_read_b128 v[198:201], v188 offset:34816
	ds_read_b128 v[202:205], v188 offset:35840
	ds_read_b128 v[206:209], v188 offset:36864
	ds_read_b128 v[210:213], v188 offset:37888
	ds_read_b128 v[214:217], v188 offset:38912
	ds_read_b128 v[218:221], v188 offset:39936
	global_load_lds_dwordx4 v[222:223], off
	v_lshl_add_u64 v[222:223], s[4:5], 0, v[166:167]
	s_mov_b32 m0, s59
	s_nop 0
	global_load_lds_dwordx4 v[222:223], off
	s_waitcnt vmcnt(8)
	s_waitcnt lgkmcnt(0)
	s_barrier
; #define PG8_STAGE(bufoff, gbase, voff) do { _Pragma("unroll") for (int _i = 0; _i < 2; ++_i) \
;         __builtin_amdgcn_global_load_lds((const unsigned*)((const char*)(gbase) + (voff)[_i]), (PG8_LAS unsigned*)(lds + (bufoff) + ldsw + _i * 8192), 16, 0, 0); } while (0)
; #define PG8_LDA(dst, b, h) do { _Pragma("unroll") for (int m = 0; m < 4; ++m) Frag<F8>::load(dst[m], lds + PG8_SA(b, h) + aoff + m * 2048); } while (0)
; #define PG8_MMA(ai, bj, At, Bt) do { __builtin_amdgcn_s_setprio(3); _Pragma("unroll") for (int m = 0; m < 4; ++m) _Pragma("unroll") for (int n = 0; n < 2; ++n) Frag<F8>::mma(acc[ai][bj][m][n], Bt[n], At[m]); \
;         __builtin_amdgcn_s_setprio(0); } while (0)
; #define PG8_WAIT_V(n) asm volatile("s_waitcnt vmcnt(" #n ")" ::: "memory")
; #define PG8_WAIT_L(n) asm volatile("s_waitcnt lgkmcnt(" #n ")" ::: "memory")
; #define PG8_BAR __builtin_amdgcn_s_barrier()
; #define PG8_SCHED __builtin_amdgcn_sched_barrier(0)
; template <class Epi, class Sched, bool ALIGN_EPI = false, bool SP2 = false, bool F8 = false>
; __device__ __forceinline__ void gemm_phase(PG8_LAS unsigned char* lds, const Gemm g, const Sched& S, const Epi& E) {
;     ...
;         for (int t = 0; t < nt; t += 2) {
;     ...
;             PG8_LDA(At, 1, 1); PG8_STAGE(PG8_SB(1, 0), b3, voffB); PG8_STAGE(PG8_SB(1, 1), b3 + hstep, voffB); PG8_STAGE(PG8_SA(1, 0), a3, voffA);
;             PG8_WAIT_V(8); PG8_WAIT_L(0); PG8_BAR; PG8_MMA(1, 0, At, B0); PG8_MMA(1, 1, At, B1); PG8_BAR; PG8_SCHED;
	s_setprio 3
	s_waitcnt lgkmcnt(0)
	v_mfma_f32_16x16x128_f8f6f4 v[158:161], v[2:9], v[190:197], v[158:161]
	v_mfma_f32_16x16x128_f8f6f4 v[150:153], v[10:17], v[190:197], v[150:153]
	v_mfma_f32_16x16x128_f8f6f4 v[142:145], v[2:9], v[198:205], v[142:145]
	v_mfma_f32_16x16x128_f8f6f4 v[134:137], v[10:17], v[198:205], v[134:137]
	v_mfma_f32_16x16x128_f8f6f4 v[126:129], v[2:9], v[206:213], v[126:129]
	v_mfma_f32_16x16x128_f8f6f4 v[118:121], v[10:17], v[206:213], v[118:121]
	v_mfma_f32_16x16x128_f8f6f4 v[110:113], v[2:9], v[214:221], v[110:113]
	v_mfma_f32_16x16x128_f8f6f4 v[102:105], v[10:17], v[214:221], v[102:105]
	v_mfma_f32_16x16x128_f8f6f4 v[154:157], v[18:25], v[190:197], v[154:157]
	v_mfma_f32_16x16x128_f8f6f4 v[146:149], v[26:33], v[190:197], v[146:149]
	v_mfma_f32_16x16x128_f8f6f4 v[138:141], v[18:25], v[198:205], v[138:141]
	v_mfma_f32_16x16x128_f8f6f4 v[130:133], v[26:33], v[198:205], v[130:133]
	v_mfma_f32_16x16x128_f8f6f4 v[122:125], v[18:25], v[206:213], v[122:125]
	v_mfma_f32_16x16x128_f8f6f4 v[114:117], v[26:33], v[206:213], v[114:117]
	v_mfma_f32_16x16x128_f8f6f4 v[106:109], v[18:25], v[214:221], v[106:109]
	v_mfma_f32_16x16x128_f8f6f4 v[98:101], v[26:33], v[214:221], v[98:101]
	s_setprio 0
	s_barrier
	s_add_i32 s0, s0, s52
	v_lshl_add_u64 v[176:177], v[176:177], 0, s[14:15]
	s_mov_b32 m0, s0
	ds_read_b128 v[190:193], v188 offset:49152
	ds_read_b128 v[194:197], v188 offset:50176
	ds_read_b128 v[198:201], v188 offset:51200
	ds_read_b128 v[202:205], v188 offset:52224
	ds_read_b128 v[206:209], v188 offset:53248
	ds_read_b128 v[210:213], v188 offset:54272
	ds_read_b128 v[214:217], v188 offset:55296
	ds_read_b128 v[218:221], v188 offset:56320
	global_load_lds_dwordx4 v[176:177], off
	s_add_i32 m0, s0, 0x2000
	s_add_u32 s4, s44, 0x20080
	v_lshl_add_u64 v[176:177], v[178:179], 0, s[14:15]
	s_addc_u32 s5, s45, 0
	s_add_i32 s0, s1, s52
	global_load_lds_dwordx4 v[176:177], off
	v_lshl_add_u64 v[176:177], s[4:5], 0, v[168:169]
	s_mov_b32 m0, s0
	s_nop 0
	global_load_lds_dwordx4 v[176:177], off
	v_lshl_add_u64 v[176:177], s[4:5], 0, v[164:165]
	s_add_i32 m0, s0, 0x2000
	s_nop 0
	global_load_lds_dwordx4 v[176:177], off
	v_lshl_add_u64 v[176:177], v[180:181], 0, s[14:15]
	s_mov_b32 m0, s60
	s_nop 0
	global_load_lds_dwordx4 v[176:177], off
	v_lshl_add_u64 v[176:177], v[182:183], 0, s[14:15]
	s_mov_b32 m0, s61
	s_nop 0
	global_load_lds_dwordx4 v[176:177], off
	s_waitcnt vmcnt(8)
	s_waitcnt lgkmcnt(0)
	s_barrier
	s_setprio 3
	s_waitcnt lgkmcnt(0)
	v_mfma_f32_16x16x128_f8f6f4 v[94:97], v[2:9], v[190:197], v[94:97]
	v_mfma_f32_16x16x128_f8f6f4 v[86:89], v[10:17], v[190:197], v[86:89]
	v_mfma_f32_16x16x128_f8f6f4 v[78:81], v[2:9], v[198:205], v[78:81]
	v_mfma_f32_16x16x128_f8f6f4 v[70:73], v[10:17], v[198:205], v[70:73]
	v_mfma_f32_16x16x128_f8f6f4 v[62:65], v[2:9], v[206:213], v[62:65]
	v_mfma_f32_16x16x128_f8f6f4 v[54:57], v[10:17], v[206:213], v[54:57]
	v_mfma_f32_16x16x128_f8f6f4 v[46:49], v[2:9], v[214:221], v[46:49]
	v_mfma_f32_16x16x128_f8f6f4 v[38:41], v[10:17], v[214:221], v[38:41]
	v_mfma_f32_16x16x128_f8f6f4 v[90:93], v[18:25], v[190:197], v[90:93]
	v_mfma_f32_16x16x128_f8f6f4 v[82:85], v[26:33], v[190:197], v[82:85]
	v_mfma_f32_16x16x128_f8f6f4 v[74:77], v[18:25], v[198:205], v[74:77]
	v_mfma_f32_16x16x128_f8f6f4 v[66:69], v[26:33], v[198:205], v[66:69]
	v_mfma_f32_16x16x128_f8f6f4 v[58:61], v[18:25], v[206:213], v[58:61]
	v_mfma_f32_16x16x128_f8f6f4 v[50:53], v[26:33], v[206:213], v[50:53]
	v_mfma_f32_16x16x128_f8f6f4 v[42:45], v[18:25], v[214:221], v[42:45]
	v_mfma_f32_16x16x128_f8f6f4 v[34:37], v[26:33], v[214:221], v[34:37]
	s_setprio 0
	s_barrier
	s_add_i32 s81, s81, 2
	s_add_u32 s42, s42, 0x100
	s_addc_u32 s43, s43, 0
	s_add_u32 s79, s79, 0x100
	s_addc_u32 s80, s80, 0
	s_cmp_gt_u32 s81, 5
	s_cbranch_scc0 .LBB0_1310

; #define PG8_STAGE(bufoff, gbase, voff) do { _Pragma("unroll") for (int _i = 0; _i < 2; ++_i) \
;         __builtin_amdgcn_global_load_lds((const unsigned*)((const char*)(gbase) + (voff)[_i]), (PG8_LAS unsigned*)(lds + (bufoff) + ldsw + _i * 8192), 16, 0, 0); } while (0)
; #define PG8_LDA(dst, b, h) do { _Pragma("unroll") for (int m = 0; m < 4; ++m) Frag<F8>::load(dst[m], lds + PG8_SA(b, h) + aoff + m * 2048); } while (0)
; #define PG8_BAR __builtin_amdgcn_s_barrier()
; template <class Epi, class Sched, bool ALIGN_EPI = false, bool SP2 = false, bool F8 = false>
; __device__ __forceinline__ void gemm_phase(PG8_LAS unsigned char* lds, const Gemm g, const Sched& S, const Epi& E) {
;     ...
;         const bool has_next = S.next(ui + 1, nxt);
;         const char* nA = has_next ? (const char*)g.A + (size_t)nxt.pm * tstep + nxt.ko : cA; const char* nB = has_next ? (const char*)g.Bt + (size_t)nxt.pn * tstep + nxt.ko : cB;
;         for (int t = 0; t < nt; t += 2) {
;             const bool last = (t == nt - 2);
;             const char* a1 = cA + (size_t)(t + 1) * kstep;
;             const char* a2 = last ? nA : cA + (size_t)(t + 2) * kstep; const char* b2 = last ? nB : cB + (size_t)(t + 2) * kstep;
;             const char* a3 = a2 + kstep; const char* b3 = b2 + kstep;
;             if (last && has_next) S.a_ready(nxt);
;             if constexpr (SP2) {
;             PG8_LDB(B0, 0, 0); PG8_LDB(B1, 0, 1); PG8_SCHED; PG8_LDA(At, 0, 0); PG8_STAGE(PG8_SA(1, 1), a1 + hstep, voffA);
;             PG8_WAIT_V(8); PG8_WAIT_L(0); PG8_BAR; PG8_MMA(0, 0, At, B0); PG8_MMA(0, 1, At, B1); PG8_BAR; PG8_SCHED;
;             PG8_LDA(At, 0, 1); PG8_STAGE(PG8_SB(0, 0), b2, voffB); PG8_STAGE(PG8_SB(0, 1), b2 + hstep, voffB); PG8_STAGE(PG8_SA(0, 0), a2, voffA);
;             PG8_WAIT_V(8); PG8_WAIT_L(0); PG8_BAR; PG8_MMA(1, 0, At, B0); PG8_MMA(1, 1, At, B1); PG8_BAR; PG8_SCHED;
;             PG8_LDB(B0, 1, 0); PG8_LDB(B1, 1, 1); PG8_SCHED; PG8_LDA(At, 1, 0); PG8_STAGE(PG8_SA(0, 1), a2 + hstep, voffA);
;             PG8_WAIT_V(8); PG8_WAIT_L(0); PG8_BAR; PG8_MMA(0, 0, At, B0); PG8_MMA(0, 1, At, B1); PG8_BAR; PG8_SCHED;
;             PG8_LDA(At, 1, 1); PG8_STAGE(PG8_SB(1, 0), b3, voffB); PG8_STAGE(PG8_SB(1, 1), b3 + hstep, voffB); PG8_STAGE(PG8_SA(1, 0), a3, voffA);
;             PG8_WAIT_V(8); PG8_WAIT_L(0); PG8_BAR; PG8_MMA(1, 0, At, B0); PG8_MMA(1, 1, At, B1); PG8_BAR; PG8_SCHED;
.LBB0_1391:
	v_lshl_add_u64 v[180:181], v[2:3], 0, s[24:25]
	s_mov_b32 s76, -2
	ds_read_b128 v[18:21], v192
	ds_read_b128 v[22:25], v192 offset:1024
	ds_read_b128 v[26:29], v192 offset:2048
	ds_read_b128 v[30:33], v192 offset:3072
	ds_read_b128 v[2:5], v193
	ds_read_b128 v[6:9], v193 offset:1024
	ds_read_b128 v[10:13], v193 offset:2048
	ds_read_b128 v[14:17], v193 offset:3072
	s_add_u32 s30, s36, 0x100
	s_addc_u32 s31, s37, 0
	s_cmp_eq_u32 s76, 24
	s_cselect_b64 vcc, -1, 0
	s_cselect_b32 s39, s27, s31
	s_cselect_b32 s38, s26, s30
	v_cndmask_b32_e32 v183, v181, v179, vcc
	v_cndmask_b32_e32 v182, v180, v178, vcc
	s_mov_b32 m0, s56
	v_lshl_add_u64 v[224:225], s[36:37], 0, v[174:175]
	ds_read_b128 v[184:187], v194
	ds_read_b128 v[188:191], v194 offset:1024
	ds_read_b128 v[200:203], v194 offset:2048
	ds_read_b128 v[204:207], v194 offset:3072
	ds_read_b128 v[208:211], v194 offset:4096
	ds_read_b128 v[212:215], v194 offset:5120
	ds_read_b128 v[216:219], v194 offset:6144
	ds_read_b128 v[220:223], v194 offset:7168
	global_load_lds_dwordx4 v[224:225], off
	v_lshl_add_u64 v[224:225], s[36:37], 0, v[176:177]
	s_mov_b32 m0, s57
	s_nop 0
	global_load_lds_dwordx4 v[224:225], off
	s_waitcnt vmcnt(8)
	s_waitcnt lgkmcnt(0)
	s_barrier
	s_setprio 3
	s_waitcnt lgkmcnt(0)
	v_mfma_f32_16x16x128_f8f6f4 v[158:161], v[18:25], v[184:191], 0
	v_mfma_f32_16x16x128_f8f6f4 v[154:157], v[26:33], v[184:191], 0
	v_mfma_f32_16x16x128_f8f6f4 v[142:145], v[18:25], v[200:207], 0
	v_mfma_f32_16x16x128_f8f6f4 v[138:141], v[26:33], v[200:207], 0
	v_mfma_f32_16x16x128_f8f6f4 v[126:129], v[18:25], v[208:215], 0
	v_mfma_f32_16x16x128_f8f6f4 v[122:125], v[26:33], v[208:215], 0
	v_mfma_f32_16x16x128_f8f6f4 v[110:113], v[18:25], v[216:223], 0
	v_mfma_f32_16x16x128_f8f6f4 v[106:109], v[26:33], v[216:223], 0
	v_mfma_f32_16x16x128_f8f6f4 v[150:153], v[2:9], v[184:191], 0
	v_mfma_f32_16x16x128_f8f6f4 v[146:149], v[10:17], v[184:191], 0
	v_mfma_f32_16x16x128_f8f6f4 v[134:137], v[2:9], v[200:207], 0
	v_mfma_f32_16x16x128_f8f6f4 v[130:133], v[10:17], v[200:207], 0
	v_mfma_f32_16x16x128_f8f6f4 v[118:121], v[2:9], v[208:215], 0
	v_mfma_f32_16x16x128_f8f6f4 v[114:117], v[10:17], v[208:215], 0
	v_mfma_f32_16x16x128_f8f6f4 v[102:105], v[2:9], v[216:223], 0
	v_mfma_f32_16x16x128_f8f6f4 v[98:101], v[10:17], v[216:223], 0
	s_setprio 0
	s_barrier
	s_mov_b32 m0, s58
	v_lshl_add_u64 v[184:185], v[182:183], 0, v[166:167]
	ds_read_b128 v[200:203], v194 offset:16384
	ds_read_b128 v[204:207], v194 offset:17408
	ds_read_b128 v[208:211], v194 offset:18432
	ds_read_b128 v[212:215], v194 offset:19456
	ds_read_b128 v[216:219], v194 offset:20480
	ds_read_b128 v[220:223], v194 offset:21504
	ds_read_b128 v[224:227], v194 offset:22528
	ds_read_b128 v[228:231], v194 offset:23552
	global_load_lds_dwordx4 v[184:185], off
	v_lshl_add_u64 v[186:187], v[182:183], 0, v[170:171]
	s_mov_b32 m0, s59
	v_lshl_add_u64 v[188:189], v[182:183], 0, s[10:11]
	global_load_lds_dwordx4 v[186:187], off
	v_lshl_add_u64 v[190:191], v[188:189], 0, v[166:167]
	s_mov_b32 m0, s60
	v_lshl_add_u64 v[188:189], v[188:189], 0, v[170:171]
	global_load_lds_dwordx4 v[190:191], off
	s_mov_b32 m0, s61
	v_lshl_add_u64 v[190:191], s[38:39], 0, v[168:169]
	global_load_lds_dwordx4 v[188:189], off
	v_lshl_add_u64 v[188:189], s[38:39], 0, v[164:165]
	s_mov_b32 m0, s45
	s_nop 0
	global_load_lds_dwordx4 v[188:189], off
	s_mov_b32 m0, s46
	s_nop 0
	global_load_lds_dwordx4 v[190:191], off
	s_waitcnt vmcnt(8)
	s_waitcnt lgkmcnt(0)
	s_barrier
	s_setprio 3
	s_waitcnt lgkmcnt(0)
	v_mfma_f32_16x16x128_f8f6f4 v[94:97], v[18:25], v[200:207], 0
	v_mfma_f32_16x16x128_f8f6f4 v[90:93], v[26:33], v[200:207], 0
	v_mfma_f32_16x16x128_f8f6f4 v[78:81], v[18:25], v[208:215], 0
	v_mfma_f32_16x16x128_f8f6f4 v[74:77], v[26:33], v[208:215], 0
	v_mfma_f32_16x16x128_f8f6f4 v[62:65], v[18:25], v[216:223], 0
	v_mfma_f32_16x16x128_f8f6f4 v[58:61], v[26:33], v[216:223], 0
	v_mfma_f32_16x16x128_f8f6f4 v[46:49], v[18:25], v[224:231], 0
	v_mfma_f32_16x16x128_f8f6f4 v[42:45], v[26:33], v[224:231], 0
	v_mfma_f32_16x16x128_f8f6f4 v[86:89], v[2:9], v[200:207], 0
	v_mfma_f32_16x16x128_f8f6f4 v[82:85], v[10:17], v[200:207], 0
	v_mfma_f32_16x16x128_f8f6f4 v[70:73], v[2:9], v[208:215], 0
	v_mfma_f32_16x16x128_f8f6f4 v[66:69], v[10:17], v[208:215], 0
	v_mfma_f32_16x16x128_f8f6f4 v[54:57], v[2:9], v[216:223], 0
	v_mfma_f32_16x16x128_f8f6f4 v[50:53], v[10:17], v[216:223], 0
	v_mfma_f32_16x16x128_f8f6f4 v[38:41], v[2:9], v[224:231], 0
	v_mfma_f32_16x16x128_f8f6f4 v[34:37], v[10:17], v[224:231], 0
	s_setprio 0
	s_barrier
	ds_read_b128 v[2:5], v196
	ds_read_b128 v[6:9], v196 offset:1024
	ds_read_b128 v[10:13], v196 offset:2048
	ds_read_b128 v[14:17], v196 offset:3072
	ds_read_b128 v[18:21], v197
	ds_read_b128 v[22:25], v197 offset:1024
	ds_read_b128 v[26:29], v197 offset:2048
	ds_read_b128 v[30:33], v197 offset:3072
	s_add_u32 s4, s38, 0x70000
	s_addc_u32 s5, s39, 0
	s_mov_b32 m0, s47
	v_lshl_add_u64 v[232:233], s[4:5], 0, v[164:165]
	ds_read_b128 v[200:203], v194 offset:32768
	ds_read_b128 v[204:207], v194 offset:33792
	ds_read_b128 v[208:211], v194 offset:34816
	ds_read_b128 v[212:215], v194 offset:35840
	ds_read_b128 v[216:219], v194 offset:36864
	ds_read_b128 v[220:223], v194 offset:37888
	ds_read_b128 v[224:227], v194 offset:38912
	ds_read_b128 v[228:231], v194 offset:39936
	global_load_lds_dwordx4 v[232:233], off
	v_lshl_add_u64 v[232:233], s[4:5], 0, v[168:169]
	s_mov_b32 m0, s48
	s_nop 0
	global_load_lds_dwordx4 v[232:233], off
	s_waitcnt vmcnt(8)
	s_waitcnt lgkmcnt(0)
	s_barrier
; #define PG8_STAGE(bufoff, gbase, voff) do { _Pragma("unroll") for (int _i = 0; _i < 2; ++_i) \
;         __builtin_amdgcn_global_load_lds((const unsigned*)((const char*)(gbase) + (voff)[_i]), (PG8_LAS unsigned*)(lds + (bufoff) + ldsw + _i * 8192), 16, 0, 0); } while (0)
; #define PG8_LDA(dst, b, h) do { _Pragma("unroll") for (int m = 0; m < 4; ++m) Frag<F8>::load(dst[m], lds + PG8_SA(b, h) + aoff + m * 2048); } while (0)
; #define PG8_LDB(dst, b, h) do { _Pragma("unroll") for (int n = 0; n < 2; ++n) Frag<F8>::load(dst[n], lds + PG8_SB(b, h) + boff + n * 2048); } while (0)
; #define PG8_MMA(ai, bj, At, Bt) do { __builtin_amdgcn_s_setprio(3); _Pragma("unroll") for (int m = 0; m < 4; ++m) _Pragma("unroll") for (int n = 0; n < 2; ++n) Frag<F8>::mma(acc[ai][bj][m][n], Bt[n], At[m]); \
;         __builtin_amdgcn_s_setprio(0); } while (0)
; #define PG8_WAIT_V(n) asm volatile("s_waitcnt vmcnt(" #n ")" ::: "memory")
; #define PG8_WAIT_L(n) asm volatile("s_waitcnt lgkmcnt(" #n ")" ::: "memory")
; #define PG8_BAR __builtin_amdgcn_s_barrier()
; #define PG8_SCHED __builtin_amdgcn_sched_barrier(0)
; template <class Epi, class Sched, bool ALIGN_EPI = false, bool SP2 = false, bool F8 = false>
; __device__ __forceinline__ void gemm_phase(PG8_LAS unsigned char* lds, const Gemm g, const Sched& S, const Epi& E) {
;     ...
;             PG8_WAIT_V(8); PG8_WAIT_L(0); PG8_BAR; PG8_MMA(1, 0, At, B0); PG8_MMA(1, 1, At, B1); PG8_BAR; PG8_SCHED;
;             PG8_LDB(B0, 1, 0); PG8_LDB(B1, 1, 1); PG8_SCHED; PG8_LDA(At, 1, 0); PG8_STAGE(PG8_SA(0, 1), a2 + hstep, voffA);
;             PG8_WAIT_V(8); PG8_WAIT_L(0); PG8_BAR; PG8_MMA(0, 0, At, B0); PG8_MMA(0, 1, At, B1); PG8_BAR; PG8_SCHED;
;             PG8_LDA(At, 1, 1); PG8_STAGE(PG8_SB(1, 0), b3, voffB); PG8_STAGE(PG8_SB(1, 1), b3 + hstep, voffB); PG8_STAGE(PG8_SA(1, 0), a3, voffA);
;             PG8_WAIT_V(8); PG8_WAIT_L(0); PG8_BAR; PG8_MMA(1, 0, At, B0); PG8_MMA(1, 1, At, B1); PG8_BAR; PG8_SCHED;
	s_setprio 3
	s_waitcnt lgkmcnt(0)
	v_mfma_f32_16x16x128_f8f6f4 v[158:161], v[2:9], v[200:207], v[158:161]
	v_mfma_f32_16x16x128_f8f6f4 v[154:157], v[10:17], v[200:207], v[154:157]
	v_mfma_f32_16x16x128_f8f6f4 v[142:145], v[2:9], v[208:215], v[142:145]
	v_mfma_f32_16x16x128_f8f6f4 v[138:141], v[10:17], v[208:215], v[138:141]
	v_mfma_f32_16x16x128_f8f6f4 v[126:129], v[2:9], v[216:223], v[126:129]
	v_mfma_f32_16x16x128_f8f6f4 v[122:125], v[10:17], v[216:223], v[122:125]
	v_mfma_f32_16x16x128_f8f6f4 v[110:113], v[2:9], v[224:231], v[110:113]
	v_mfma_f32_16x16x128_f8f6f4 v[106:109], v[10:17], v[224:231], v[106:109]
	v_mfma_f32_16x16x128_f8f6f4 v[150:153], v[18:25], v[200:207], v[150:153]
	v_mfma_f32_16x16x128_f8f6f4 v[146:149], v[26:33], v[200:207], v[146:149]
	v_mfma_f32_16x16x128_f8f6f4 v[134:137], v[18:25], v[208:215], v[134:137]
	v_mfma_f32_16x16x128_f8f6f4 v[130:133], v[26:33], v[208:215], v[130:133]
	v_mfma_f32_16x16x128_f8f6f4 v[118:121], v[18:25], v[216:223], v[118:121]
	v_mfma_f32_16x16x128_f8f6f4 v[114:117], v[26:33], v[216:223], v[114:117]
	v_mfma_f32_16x16x128_f8f6f4 v[102:105], v[18:25], v[224:231], v[102:105]
	v_mfma_f32_16x16x128_f8f6f4 v[98:101], v[26:33], v[224:231], v[98:101]
	s_setprio 0
	s_barrier
	s_mov_b32 m0, s67
	v_lshl_add_u64 v[184:185], v[184:185], 0, s[18:19]
	ds_read_b128 v[200:203], v194 offset:49152
	ds_read_b128 v[204:207], v194 offset:50176
	ds_read_b128 v[208:211], v194 offset:51200
	ds_read_b128 v[212:215], v194 offset:52224
	ds_read_b128 v[216:219], v194 offset:53248
	ds_read_b128 v[220:223], v194 offset:54272
	ds_read_b128 v[224:227], v194 offset:55296
	ds_read_b128 v[228:231], v194 offset:56320
	global_load_lds_dwordx4 v[184:185], off
	v_lshl_add_u64 v[184:185], v[186:187], 0, s[18:19]
	s_mov_b32 m0, s70
	v_lshl_add_u64 v[182:183], v[182:183], 0, s[20:21]
	global_load_lds_dwordx4 v[184:185], off
	v_lshl_add_u64 v[184:185], v[182:183], 0, v[166:167]
	s_mov_b32 m0, s71
	v_lshl_add_u64 v[182:183], v[182:183], 0, v[170:171]
	global_load_lds_dwordx4 v[184:185], off
	s_mov_b32 m0, s72
	s_nop 0
	global_load_lds_dwordx4 v[182:183], off
	v_lshl_add_u64 v[182:183], v[188:189], 0, s[18:19]
	s_mov_b32 m0, s49
	s_nop 0
	global_load_lds_dwordx4 v[182:183], off
	v_lshl_add_u64 v[182:183], v[190:191], 0, s[18:19]
	s_mov_b32 m0, s50
	s_nop 0
	global_load_lds_dwordx4 v[182:183], off
	s_waitcnt vmcnt(8)
	s_waitcnt lgkmcnt(0)
	s_barrier
	s_setprio 3
	s_waitcnt lgkmcnt(0)
	v_mfma_f32_16x16x128_f8f6f4 v[94:97], v[2:9], v[200:207], v[94:97]
	v_mfma_f32_16x16x128_f8f6f4 v[90:93], v[10:17], v[200:207], v[90:93]
	v_mfma_f32_16x16x128_f8f6f4 v[78:81], v[2:9], v[208:215], v[78:81]
	v_mfma_f32_16x16x128_f8f6f4 v[74:77], v[10:17], v[208:215], v[74:77]
	v_mfma_f32_16x16x128_f8f6f4 v[62:65], v[2:9], v[216:223], v[62:65]
	v_mfma_f32_16x16x128_f8f6f4 v[58:61], v[10:17], v[216:223], v[58:61]
	v_mfma_f32_16x16x128_f8f6f4 v[46:49], v[2:9], v[224:231], v[46:49]
	v_mfma_f32_16x16x128_f8f6f4 v[42:45], v[10:17], v[224:231], v[42:45]
	v_mfma_f32_16x16x128_f8f6f4 v[86:89], v[18:25], v[200:207], v[86:89]
	v_mfma_f32_16x16x128_f8f6f4 v[82:85], v[26:33], v[200:207], v[82:85]
	v_mfma_f32_16x16x128_f8f6f4 v[70:73], v[18:25], v[208:215], v[70:73]
	v_mfma_f32_16x16x128_f8f6f4 v[66:69], v[26:33], v[208:215], v[66:69]
	v_mfma_f32_16x16x128_f8f6f4 v[54:57], v[18:25], v[216:223], v[54:57]
	v_mfma_f32_16x16x128_f8f6f4 v[50:53], v[26:33], v[216:223], v[50:53]
	v_mfma_f32_16x16x128_f8f6f4 v[38:41], v[18:25], v[224:231], v[38:41]
	v_mfma_f32_16x16x128_f8f6f4 v[34:37], v[26:33], v[224:231], v[34:37]
	s_setprio 0
	s_barrier
	s_add_i32 s76, s76, 2
	v_lshl_add_u64 v[180:181], v[180:181], 0, s[24:25]
	s_cmp_gt_u32 s76, 25
	s_mov_b64 s[36:37], s[30:31]
	s_cbranch_scc1 .Lpeel_exit_4
.LBB0_1392:
	ds_read_b128 v[18:21], v192
	ds_read_b128 v[22:25], v192 offset:1024
	ds_read_b128 v[26:29], v192 offset:2048
	ds_read_b128 v[30:33], v192 offset:3072
	ds_read_b128 v[2:5], v193
	ds_read_b128 v[6:9], v193 offset:1024
	ds_read_b128 v[10:13], v193 offset:2048
	ds_read_b128 v[14:17], v193 offset:3072
	s_add_u32 s30, s36, 0x100
	s_addc_u32 s31, s37, 0
	s_cmp_eq_u32 s76, 24
	s_cselect_b64 vcc, -1, 0
	s_cselect_b32 s39, s27, s31
	s_cselect_b32 s38, s26, s30
	v_cndmask_b32_e32 v183, v181, v179, vcc
	v_cndmask_b32_e32 v182, v180, v178, vcc
	s_mov_b32 m0, s56
	v_lshl_add_u64 v[224:225], s[36:37], 0, v[174:175]
	ds_read_b128 v[184:187], v194
	ds_read_b128 v[188:191], v194 offset:1024
	ds_read_b128 v[200:203], v194 offset:2048
	ds_read_b128 v[204:207], v194 offset:3072
	ds_read_b128 v[208:211], v194 offset:4096
	ds_read_b128 v[212:215], v194 offset:5120
	ds_read_b128 v[216:219], v194 offset:6144
	ds_read_b128 v[220:223], v194 offset:7168
	global_load_lds_dwordx4 v[224:225], off
	v_lshl_add_u64 v[224:225], s[36:37], 0, v[176:177]
	s_mov_b32 m0, s57
	s_nop 0
	global_load_lds_dwordx4 v[224:225], off
	s_waitcnt vmcnt(8)
	s_waitcnt lgkmcnt(0)
	s_barrier
	s_setprio 3
	s_waitcnt lgkmcnt(0)
	v_mfma_f32_16x16x128_f8f6f4 v[158:161], v[18:25], v[184:191], v[158:161]
	v_mfma_f32_16x16x128_f8f6f4 v[154:157], v[26:33], v[184:191], v[154:157]
	v_mfma_f32_16x16x128_f8f6f4 v[142:145], v[18:25], v[200:207], v[142:145]
	v_mfma_f32_16x16x128_f8f6f4 v[138:141], v[26:33], v[200:207], v[138:141]
	v_mfma_f32_16x16x128_f8f6f4 v[126:129], v[18:25], v[208:215], v[126:129]
	v_mfma_f32_16x16x128_f8f6f4 v[122:125], v[26:33], v[208:215], v[122:125]
	v_mfma_f32_16x16x128_f8f6f4 v[110:113], v[18:25], v[216:223], v[110:113]
	v_mfma_f32_16x16x128_f8f6f4 v[106:109], v[26:33], v[216:223], v[106:109]
	v_mfma_f32_16x16x128_f8f6f4 v[150:153], v[2:9], v[184:191], v[150:153]
	v_mfma_f32_16x16x128_f8f6f4 v[146:149], v[10:17], v[184:191], v[146:149]
	v_mfma_f32_16x16x128_f8f6f4 v[134:137], v[2:9], v[200:207], v[134:137]
	v_mfma_f32_16x16x128_f8f6f4 v[130:133], v[10:17], v[200:207], v[130:133]
	v_mfma_f32_16x16x128_f8f6f4 v[118:121], v[2:9], v[208:215], v[118:121]
	v_mfma_f32_16x16x128_f8f6f4 v[114:117], v[10:17], v[208:215], v[114:117]
	v_mfma_f32_16x16x128_f8f6f4 v[102:105], v[2:9], v[216:223], v[102:105]
	v_mfma_f32_16x16x128_f8f6f4 v[98:101], v[10:17], v[216:223], v[98:101]
	s_setprio 0
	s_barrier
; #define PG8_STAGE(bufoff, gbase, voff) do { _Pragma("unroll") for (int _i = 0; _i < 2; ++_i) \
;         __builtin_amdgcn_global_load_lds((const unsigned*)((const char*)(gbase) + (voff)[_i]), (PG8_LAS unsigned*)(lds + (bufoff) + ldsw + _i * 8192), 16, 0, 0); } while (0)
; #define PG8_LDA(dst, b, h) do { _Pragma("unroll") for (int m = 0; m < 4; ++m) Frag<F8>::load(dst[m], lds + PG8_SA(b, h) + aoff + m * 2048); } while (0)
; #define PG8_LDB(dst, b, h) do { _Pragma("unroll") for (int n = 0; n < 2; ++n) Frag<F8>::load(dst[n], lds + PG8_SB(b, h) + boff + n * 2048); } while (0)
; #define PG8_MMA(ai, bj, At, Bt) do { __builtin_amdgcn_s_setprio(3); _Pragma("unroll") for (int m = 0; m < 4; ++m) _Pragma("unroll") for (int n = 0; n < 2; ++n) Frag<F8>::mma(acc[ai][bj][m][n], Bt[n], At[m]); \
;         __builtin_amdgcn_s_setprio(0); } while (0)
; #define PG8_WAIT_V(n) asm volatile("s_waitcnt vmcnt(" #n ")" ::: "memory")
; #define PG8_WAIT_L(n) asm volatile("s_waitcnt lgkmcnt(" #n ")" ::: "memory")
; #define PG8_BAR __builtin_amdgcn_s_barrier()
; #define PG8_SCHED __builtin_amdgcn_sched_barrier(0)
; template <class Epi, class Sched, bool ALIGN_EPI = false, bool SP2 = false, bool F8 = false>
; __device__ __forceinline__ void gemm_phase(PG8_LAS unsigned char* lds, const Gemm g, const Sched& S, const Epi& E) {
;     ...
;         for (int t = 0; t < nt; t += 2) {
;     ...
;             PG8_LDB(B0, 1, 0); PG8_LDB(B1, 1, 1); PG8_SCHED; PG8_LDA(At, 1, 0); PG8_STAGE(PG8_SA(0, 1), a2 + hstep, voffA);
;             PG8_WAIT_V(8); PG8_WAIT_L(0); PG8_BAR; PG8_MMA(0, 0, At, B0); PG8_MMA(0, 1, At, B1); PG8_BAR; PG8_SCHED;
;             PG8_LDA(At, 1, 1); PG8_STAGE(PG8_SB(1, 0), b3, voffB); PG8_STAGE(PG8_SB(1, 1), b3 + hstep, voffB); PG8_STAGE(PG8_SA(1, 0), a3, voffA);
;             PG8_WAIT_V(8); PG8_WAIT_L(0); PG8_BAR; PG8_MMA(1, 0, At, B0); PG8_MMA(1, 1, At, B1); PG8_BAR; PG8_SCHED;
	s_mov_b32 m0, s58
	v_lshl_add_u64 v[184:185], v[182:183], 0, v[166:167]
	ds_read_b128 v[200:203], v194 offset:16384
	ds_read_b128 v[204:207], v194 offset:17408
	ds_read_b128 v[208:211], v194 offset:18432
	ds_read_b128 v[212:215], v194 offset:19456
	ds_read_b128 v[216:219], v194 offset:20480
	ds_read_b128 v[220:223], v194 offset:21504
	ds_read_b128 v[224:227], v194 offset:22528
	ds_read_b128 v[228:231], v194 offset:23552
	global_load_lds_dwordx4 v[184:185], off
	v_lshl_add_u64 v[186:187], v[182:183], 0, v[170:171]
	s_mov_b32 m0, s59
	v_lshl_add_u64 v[188:189], v[182:183], 0, s[10:11]
	global_load_lds_dwordx4 v[186:187], off
	v_lshl_add_u64 v[190:191], v[188:189], 0, v[166:167]
	s_mov_b32 m0, s60
	v_lshl_add_u64 v[188:189], v[188:189], 0, v[170:171]
	global_load_lds_dwordx4 v[190:191], off
	s_mov_b32 m0, s61
	v_lshl_add_u64 v[190:191], s[38:39], 0, v[168:169]
	global_load_lds_dwordx4 v[188:189], off
	v_lshl_add_u64 v[188:189], s[38:39], 0, v[164:165]
	s_mov_b32 m0, s45
	s_nop 0
	global_load_lds_dwordx4 v[188:189], off
	s_mov_b32 m0, s46
	s_nop 0
	global_load_lds_dwordx4 v[190:191], off
	s_waitcnt vmcnt(8)
	s_waitcnt lgkmcnt(0)
	s_barrier
	s_setprio 3
	s_waitcnt lgkmcnt(0)
	v_mfma_f32_16x16x128_f8f6f4 v[94:97], v[18:25], v[200:207], v[94:97]
	v_mfma_f32_16x16x128_f8f6f4 v[90:93], v[26:33], v[200:207], v[90:93]
	v_mfma_f32_16x16x128_f8f6f4 v[78:81], v[18:25], v[208:215], v[78:81]
	v_mfma_f32_16x16x128_f8f6f4 v[74:77], v[26:33], v[208:215], v[74:77]
	v_mfma_f32_16x16x128_f8f6f4 v[62:65], v[18:25], v[216:223], v[62:65]
	v_mfma_f32_16x16x128_f8f6f4 v[58:61], v[26:33], v[216:223], v[58:61]
	v_mfma_f32_16x16x128_f8f6f4 v[46:49], v[18:25], v[224:231], v[46:49]
	v_mfma_f32_16x16x128_f8f6f4 v[42:45], v[26:33], v[224:231], v[42:45]
	v_mfma_f32_16x16x128_f8f6f4 v[86:89], v[2:9], v[200:207], v[86:89]
	v_mfma_f32_16x16x128_f8f6f4 v[82:85], v[10:17], v[200:207], v[82:85]
	v_mfma_f32_16x16x128_f8f6f4 v[70:73], v[2:9], v[208:215], v[70:73]
	v_mfma_f32_16x16x128_f8f6f4 v[66:69], v[10:17], v[208:215], v[66:69]
	v_mfma_f32_16x16x128_f8f6f4 v[54:57], v[2:9], v[216:223], v[54:57]
	v_mfma_f32_16x16x128_f8f6f4 v[50:53], v[10:17], v[216:223], v[50:53]
	v_mfma_f32_16x16x128_f8f6f4 v[38:41], v[2:9], v[224:231], v[38:41]
	v_mfma_f32_16x16x128_f8f6f4 v[34:37], v[10:17], v[224:231], v[34:37]
	s_setprio 0
	s_barrier
	ds_read_b128 v[2:5], v196
	ds_read_b128 v[6:9], v196 offset:1024
	ds_read_b128 v[10:13], v196 offset:2048
	ds_read_b128 v[14:17], v196 offset:3072
	ds_read_b128 v[18:21], v197
	ds_read_b128 v[22:25], v197 offset:1024
	ds_read_b128 v[26:29], v197 offset:2048
	ds_read_b128 v[30:33], v197 offset:3072
	s_add_u32 s4, s38, 0x70000
	s_addc_u32 s5, s39, 0
	s_mov_b32 m0, s47
	v_lshl_add_u64 v[232:233], s[4:5], 0, v[164:165]
	ds_read_b128 v[200:203], v194 offset:32768
	ds_read_b128 v[204:207], v194 offset:33792
	ds_read_b128 v[208:211], v194 offset:34816
	ds_read_b128 v[212:215], v194 offset:35840
	ds_read_b128 v[216:219], v194 offset:36864
	ds_read_b128 v[220:223], v194 offset:37888
	ds_read_b128 v[224:227], v194 offset:38912
	ds_read_b128 v[228:231], v194 offset:39936
	global_load_lds_dwordx4 v[232:233], off
	v_lshl_add_u64 v[232:233], s[4:5], 0, v[168:169]
	s_mov_b32 m0, s48
	s_nop 0
	global_load_lds_dwordx4 v[232:233], off
	s_waitcnt vmcnt(8)
	s_waitcnt lgkmcnt(0)
	s_barrier
	s_setprio 3
	s_waitcnt lgkmcnt(0)
	v_mfma_f32_16x16x128_f8f6f4 v[158:161], v[2:9], v[200:207], v[158:161]
	v_mfma_f32_16x16x128_f8f6f4 v[154:157], v[10:17], v[200:207], v[154:157]
	v_mfma_f32_16x16x128_f8f6f4 v[142:145], v[2:9], v[208:215], v[142:145]
	v_mfma_f32_16x16x128_f8f6f4 v[138:141], v[10:17], v[208:215], v[138:141]
	v_mfma_f32_16x16x128_f8f6f4 v[126:129], v[2:9], v[216:223], v[126:129]
	v_mfma_f32_16x16x128_f8f6f4 v[122:125], v[10:17], v[216:223], v[122:125]
	v_mfma_f32_16x16x128_f8f6f4 v[110:113], v[2:9], v[224:231], v[110:113]
	v_mfma_f32_16x16x128_f8f6f4 v[106:109], v[10:17], v[224:231], v[106:109]
	v_mfma_f32_16x16x128_f8f6f4 v[150:153], v[18:25], v[200:207], v[150:153]
	v_mfma_f32_16x16x128_f8f6f4 v[146:149], v[26:33], v[200:207], v[146:149]
	v_mfma_f32_16x16x128_f8f6f4 v[134:137], v[18:25], v[208:215], v[134:137]
	v_mfma_f32_16x16x128_f8f6f4 v[130:133], v[26:33], v[208:215], v[130:133]
	v_mfma_f32_16x16x128_f8f6f4 v[118:121], v[18:25], v[216:223], v[118:121]
	v_mfma_f32_16x16x128_f8f6f4 v[114:117], v[26:33], v[216:223], v[114:117]
	v_mfma_f32_16x16x128_f8f6f4 v[102:105], v[18:25], v[224:231], v[102:105]
	v_mfma_f32_16x16x128_f8f6f4 v[98:101], v[26:33], v[224:231], v[98:101]
	s_setprio 0
	s_barrier
	s_mov_b32 m0, s67
	v_lshl_add_u64 v[184:185], v[184:185], 0, s[18:19]
	ds_read_b128 v[200:203], v194 offset:49152
	ds_read_b128 v[204:207], v194 offset:50176
	ds_read_b128 v[208:211], v194 offset:51200
	ds_read_b128 v[212:215], v194 offset:52224
	ds_read_b128 v[216:219], v194 offset:53248
	ds_read_b128 v[220:223], v194 offset:54272
	ds_read_b128 v[224:227], v194 offset:55296
	ds_read_b128 v[228:231], v194 offset:56320
	global_load_lds_dwordx4 v[184:185], off
	v_lshl_add_u64 v[184:185], v[186:187], 0, s[18:19]
	s_mov_b32 m0, s70
	v_lshl_add_u64 v[182:183], v[182:183], 0, s[20:21]
	global_load_lds_dwordx4 v[184:185], off
	v_lshl_add_u64 v[184:185], v[182:183], 0, v[166:167]
	s_mov_b32 m0, s71
	v_lshl_add_u64 v[182:183], v[182:183], 0, v[170:171]
	global_load_lds_dwordx4 v[184:185], off
	s_mov_b32 m0, s72
	s_nop 0
	global_load_lds_dwordx4 v[182:183], off
	v_lshl_add_u64 v[182:183], v[188:189], 0, s[18:19]
	s_mov_b32 m0, s49
	s_nop 0
	global_load_lds_dwordx4 v[182:183], off
	v_lshl_add_u64 v[182:183], v[190:191], 0, s[18:19]
	s_mov_b32 m0, s50
	s_nop 0
	global_load_lds_dwordx4 v[182:183], off
	s_waitcnt vmcnt(8)
	s_waitcnt lgkmcnt(0)
	s_barrier
	s_setprio 3
	s_waitcnt lgkmcnt(0)
	v_mfma_f32_16x16x128_f8f6f4 v[94:97], v[2:9], v[200:207], v[94:97]
	v_mfma_f32_16x16x128_f8f6f4 v[90:93], v[10:17], v[200:207], v[90:93]
	v_mfma_f32_16x16x128_f8f6f4 v[78:81], v[2:9], v[208:215], v[78:81]
	v_mfma_f32_16x16x128_f8f6f4 v[74:77], v[10:17], v[208:215], v[74:77]
	v_mfma_f32_16x16x128_f8f6f4 v[62:65], v[2:9], v[216:223], v[62:65]
	v_mfma_f32_16x16x128_f8f6f4 v[58:61], v[10:17], v[216:223], v[58:61]
	v_mfma_f32_16x16x128_f8f6f4 v[46:49], v[2:9], v[224:231], v[46:49]
	v_mfma_f32_16x16x128_f8f6f4 v[42:45], v[10:17], v[224:231], v[42:45]
	v_mfma_f32_16x16x128_f8f6f4 v[86:89], v[18:25], v[200:207], v[86:89]
	v_mfma_f32_16x16x128_f8f6f4 v[82:85], v[26:33], v[200:207], v[82:85]
	v_mfma_f32_16x16x128_f8f6f4 v[70:73], v[18:25], v[208:215], v[70:73]
	v_mfma_f32_16x16x128_f8f6f4 v[66:69], v[26:33], v[208:215], v[66:69]
	v_mfma_f32_16x16x128_f8f6f4 v[54:57], v[18:25], v[216:223], v[54:57]
	v_mfma_f32_16x16x128_f8f6f4 v[50:53], v[26:33], v[216:223], v[50:53]
	v_mfma_f32_16x16x128_f8f6f4 v[38:41], v[18:25], v[224:231], v[38:41]
	v_mfma_f32_16x16x128_f8f6f4 v[34:37], v[26:33], v[224:231], v[34:37]
	s_setprio 0
	s_barrier
	s_add_i32 s76, s76, 2
	v_lshl_add_u64 v[180:181], v[180:181], 0, s[24:25]
	s_cmp_gt_u32 s76, 25
	s_mov_b64 s[36:37], s[30:31]
	s_cbranch_scc0 .LBB0_1392

; #define PG8_BAR __builtin_amdgcn_s_barrier()
; template <class Epi, class Sched, bool ALIGN_EPI = false, bool SP2 = false, bool F8 = false>
; __device__ __forceinline__ void gemm_phase(PG8_LAS unsigned char* lds, const Gemm g, const Sched& S, const Epi& E) {
;     ...
;         PG8_WAIT_V(2); PG8_BAR;
;         PG8_STAGE(PG8_SB(1, 0), cB + kstep, voffB); PG8_STAGE(PG8_SA(1, 0), cA + kstep, voffA); PG8_STAGE(PG8_SB(1, 1), cB + hstep + kstep, voffB);
;         PG8_WAIT_V(6); PG8_BAR;
;     } else {
;         PG8_STAGE(PG8_SB(0, 0), cB, voffB); PG8_STAGE(PG8_SA(0, 0), cA, voffA); PG8_STAGE(PG8_SB(0, 1), cB + hstep, voffB); PG8_STAGE(PG8_SA(0, 1), cA + hstep, voffA);
;         if (wr == 1) PG8_BAR;
;         PG8_WAIT_V(4); PG8_BAR;
;         PG8_STAGE(PG8_SB(1, 0), cB + kstep, voffB); PG8_STAGE(PG8_SA(1, 0), cA + kstep, voffA); PG8_STAGE(PG8_SB(1, 1), cB + hstep + kstep, voffB);
;         PG8_WAIT_V(6); PG8_BAR;
;     }
;     for (;;) {
;         const bool has_next = S.next(ui + 1, nxt);
;         const char* nA = has_next ? (const char*)g.A + (size_t)nxt.pm * tstep + nxt.ko : cA; const char* nB = has_next ? (const char*)g.Bt + (size_t)nxt.pn * tstep + nxt.ko : cB;
;         for (int t = 0; t < nt; t += 2) {
;             const bool last = (t == nt - 2);
;             const char* a1 = cA + (size_t)(t + 1) * kstep;
;             const char* a2 = last ? nA : cA + (size_t)(t + 2) * kstep; const char* b2 = last ? nB : cB + (size_t)(t + 2) * kstep;
;             const char* a3 = a2 + kstep; const char* b3 = b2 + kstep;
;             if (last && has_next) S.a_ready(nxt);
;             if constexpr (SP2) {
;             PG8_LDB(B0, 0, 0); PG8_LDB(B1, 0, 1); PG8_SCHED; PG8_LDA(At, 0, 0); PG8_STAGE(PG8_SA(1, 1), a1 + hstep, voffA);
;             PG8_WAIT_V(8); PG8_WAIT_L(0); PG8_BAR; PG8_MMA(0, 0, At, B0); PG8_MMA(0, 1, At, B1); PG8_BAR; PG8_SCHED;
;             PG8_LDA(At, 0, 1); PG8_STAGE(PG8_SB(0, 0), b2, voffB); PG8_STAGE(PG8_SB(0, 1), b2 + hstep, voffB); PG8_STAGE(PG8_SA(0, 0), a2, voffA);
;             PG8_WAIT_V(8); PG8_WAIT_L(0); PG8_BAR; PG8_MMA(1, 0, At, B0); PG8_MMA(1, 1, At, B1); PG8_BAR; PG8_SCHED;
;             PG8_LDB(B0, 1, 0); PG8_LDB(B1, 1, 1); PG8_SCHED; PG8_LDA(At, 1, 0); PG8_STAGE(PG8_SA(0, 1), a2 + hstep, voffA);
;             PG8_WAIT_V(8); PG8_WAIT_L(0); PG8_BAR; PG8_MMA(0, 0, At, B0); PG8_MMA(0, 1, At, B1); PG8_BAR; PG8_SCHED;
.LBB0_1418:
	s_lshl_b32 s1, s15, 5
	s_add_i32 s15, 0, 0x18000
	s_and_b32 s27, s1, 0x60
	s_add_i32 s30, s15, s14
	s_mov_b64 s[8:9], 0x80
	s_lshl_b32 s0, s22, 13
	s_lshl_b32 s1, s27, 7
	v_lshl_add_u64 v[130:131], v[154:155], 0, s[8:9]
	s_mov_b32 m0, s30
	s_add_i32 s36, s30, 0x2000
	s_add_i32 s31, s4, 0x8000
	s_add_i32 s37, s4, 0xa000
	s_waitcnt vmcnt(2)
	s_barrier
	global_load_lds_dwordx4 v[130:131], off
	v_lshl_add_u64 v[132:133], v[156:157], 0, s[8:9]
	s_mov_b32 m0, s36
	v_lshl_add_u64 v[128:129], v[148:149], 0, s[8:9]
	v_lshl_add_u64 v[134:135], v[146:147], 0, s[8:9]
	s_add_u32 s8, s6, 0x70080
	global_load_lds_dwordx4 v[132:133], off
	s_mov_b32 m0, s31
	s_addc_u32 s9, s7, 0
	s_add_i32 s16, 0, 0x1c000
	global_load_lds_dwordx4 v[128:129], off
	s_mov_b32 m0, s37
	s_add_i32 s38, s16, s14
	global_load_lds_dwordx4 v[134:135], off
	v_lshl_add_u64 v[136:137], s[8:9], 0, v[158:159]
	s_mov_b32 m0, s38
	s_add_i32 s39, s38, 0x2000
	global_load_lds_dwordx4 v[136:137], off
	v_lshl_add_u64 v[138:139], s[8:9], 0, v[144:145]
	s_mov_b32 m0, s39
	v_and_b32_e32 v160, 15, v0
	global_load_lds_dwordx4 v[138:139], off
	v_bfe_u32 v161, v0, 4, 2
	v_lshlrev_b32_e32 v1, 6, v160
	v_lshlrev_b32_e32 v0, 2, v0
	v_lshl_or_b32 v1, v161, 4, v1
	v_and_b32_e32 v0, 32, v0
	v_bitop3_b32 v2, v1, s0, v0 bitop3:0xde
	v_bitop3_b32 v0, v1, s1, v0 bitop3:0xde
	s_add_i32 s42, 0, 0x10000
	s_add_i32 s44, 0, 0x14000
	v_add_u32_e32 v168, s42, v0
	s_add_u32 s20, s10, 0x70080
	s_waitcnt vmcnt(6)
	s_barrier
	v_add_u32_e32 v167, s44, v0
	s_addc_u32 s21, s11, 0
	s_add_i32 s42, s42, s14
	ds_read_b128 v[96:99], v168
	ds_read_b128 v[100:103], v168 offset:1024
	ds_read_b128 v[104:107], v168 offset:2048
	ds_read_b128 v[108:111], v168 offset:3072
	ds_read_b128 v[170:173], v167
	ds_read_b128 v[174:177], v167 offset:1024
	ds_read_b128 v[178:181], v167 offset:2048
	ds_read_b128 v[182:185], v167 offset:3072
	s_add_i32 s46, s4, 0xc000
	s_add_i32 s45, s4, 0xe000
	s_add_i32 s41, s42, 0x2000
	s_add_u32 s18, s6, 0x70100
	s_addc_u32 s19, s7, 0
	s_add_i32 s44, s44, s14
	s_add_i32 s43, s44, 0x2000
	v_add_u32_e32 v165, s16, v0
	s_add_u32 s16, s10, 0x70100
	s_addc_u32 s17, s11, 0
	s_add_u32 s14, s6, 0x70180
	v_add_u32_e32 v166, s15, v0
	s_addc_u32 s15, s7, 0
	s_add_u32 s6, s10, 0x70180
	s_mov_b32 s3, 0x8000
	s_mov_b32 s26, 0xc000
	s_addc_u32 s7, s11, 0
	s_mov_b32 s8, 0
	v_add_u32_e32 v163, 0, v2
	s_cmpk_gt_u32 s47, 0xff
	s_mov_b32 m0, s46
	v_lshl_add_u64 v[0:1], s[20:21], 0, v[158:159]
	ds_read_b128 v[36:39], v163
	ds_read_b128 v[40:43], v163 offset:1024
	ds_read_b128 v[44:47], v163 offset:2048
	ds_read_b128 v[48:51], v163 offset:3072
	ds_read_b128 v[68:71], v163 offset:4096
	ds_read_b128 v[72:75], v163 offset:5120
	ds_read_b128 v[76:79], v163 offset:6144
	ds_read_b128 v[80:83], v163 offset:7168
	global_load_lds_dwordx4 v[0:1], off
	v_lshl_add_u64 v[0:1], s[20:21], 0, v[144:145]
	s_mov_b32 m0, s45
	s_nop 0
	global_load_lds_dwordx4 v[0:1], off
	s_waitcnt vmcnt(8)
	s_waitcnt lgkmcnt(0)
	s_barrier
	s_setprio 3
	s_mov_b32 s9, s8
	s_mov_b32 s10, s8
	s_mov_b32 s11, s8
	v_mov_b64_e32 v[0:1], s[8:9]
	v_mov_b64_e32 v[30:31], s[10:11]
	v_mov_b64_e32 v[34:35], s[10:11]
	v_mov_b64_e32 v[22:23], s[10:11]
	v_mov_b64_e32 v[26:27], s[10:11]
	v_mov_b64_e32 v[14:15], s[10:11]
	v_mov_b64_e32 v[18:19], s[10:11]
	v_mov_b64_e32 v[4:5], s[8:9]
	v_mov_b64_e32 v[8:9], s[8:9]
	v_mov_b64_e32 v[2:3], s[10:11]
	v_mov_b64_e32 v[28:29], s[8:9]
	v_mov_b64_e32 v[32:33], s[8:9]
	v_mov_b64_e32 v[20:21], s[8:9]
	v_mov_b64_e32 v[24:25], s[8:9]
	v_mov_b64_e32 v[12:13], s[8:9]
	v_mov_b64_e32 v[16:17], s[8:9]
	v_mov_b64_e32 v[6:7], s[10:11]
	v_mov_b64_e32 v[10:11], s[10:11]
	v_mov_b32_e32 v164, 0x7f7f7f7f
	s_waitcnt lgkmcnt(0)
	v_mfma_f32_16x16x128_f8f6f4 v[28:31], v[96:103], v[36:43], v[28:31]
	v_mfma_f32_16x16x128_f8f6f4 v[32:35], v[104:111], v[36:43], v[32:35]
	v_mfma_f32_16x16x128_f8f6f4 v[20:23], v[96:103], v[44:51], v[20:23]
	v_mfma_f32_16x16x128_f8f6f4 v[24:27], v[104:111], v[44:51], v[24:27]
	v_mfma_f32_16x16x128_f8f6f4 v[12:15], v[96:103], v[68:75], v[12:15]
	v_mfma_f32_16x16x128_f8f6f4 v[16:19], v[104:111], v[68:75], v[16:19]
	v_mfma_f32_16x16x128_f8f6f4 v[4:7], v[96:103], v[76:83], v[4:7]
	v_mfma_f32_16x16x128_f8f6f4 v[8:11], v[104:111], v[76:83], v[8:11]
	v_mov_b64_e32 v[62:63], s[10:11]
	v_mov_b64_e32 v[66:67], s[10:11]
	v_mov_b64_e32 v[54:55], s[10:11]
	v_mov_b64_e32 v[58:59], s[10:11]
	v_mov_b64_e32 v[60:61], s[8:9]
	v_mov_b64_e32 v[64:65], s[8:9]
	v_mov_b64_e32 v[52:53], s[8:9]
	v_mov_b64_e32 v[56:57], s[8:9]
	v_mfma_f32_16x16x128_f8f6f4 v[60:63], v[170:177], v[36:43], v[60:63]
	v_mfma_f32_16x16x128_f8f6f4 v[64:67], v[178:185], v[36:43], v[64:67]
	v_mfma_f32_16x16x128_f8f6f4 v[52:55], v[170:177], v[44:51], v[52:55]
	v_mfma_f32_16x16x128_f8f6f4 v[56:59], v[178:185], v[44:51], v[56:59]
	v_mov_b64_e32 v[46:47], s[10:11]
	v_mov_b64_e32 v[50:51], s[10:11]
	v_mov_b64_e32 v[38:39], s[10:11]
	v_mov_b64_e32 v[42:43], s[10:11]
	v_mov_b64_e32 v[44:45], s[8:9]
	v_mov_b64_e32 v[48:49], s[8:9]
	v_mov_b64_e32 v[36:37], s[8:9]
	v_mov_b64_e32 v[40:41], s[8:9]
	v_mfma_f32_16x16x128_f8f6f4 v[44:47], v[170:177], v[68:75], v[44:47]
	v_mfma_f32_16x16x128_f8f6f4 v[48:51], v[178:185], v[68:75], v[48:51]
	v_mfma_f32_16x16x128_f8f6f4 v[36:39], v[170:177], v[76:83], v[36:39]
	v_mfma_f32_16x16x128_f8f6f4 v[40:43], v[178:185], v[76:83], v[40:43]
	s_setprio 0
	s_barrier
; #define PG8_STAGE(bufoff, gbase, voff) do { _Pragma("unroll") for (int _i = 0; _i < 2; ++_i) \
;         __builtin_amdgcn_global_load_lds((const unsigned*)((const char*)(gbase) + (voff)[_i]), (PG8_LAS unsigned*)(lds + (bufoff) + ldsw + _i * 8192), 16, 0, 0); } while (0)
; #define PG8_LDA(dst, b, h) do { _Pragma("unroll") for (int m = 0; m < 4; ++m) Frag<F8>::load(dst[m], lds + PG8_SA(b, h) + aoff + m * 2048); } while (0)
; #define PG8_LDB(dst, b, h) do { _Pragma("unroll") for (int n = 0; n < 2; ++n) Frag<F8>::load(dst[n], lds + PG8_SB(b, h) + boff + n * 2048); } while (0)
; #define PG8_MMA(ai, bj, At, Bt) do { __builtin_amdgcn_s_setprio(3); _Pragma("unroll") for (int m = 0; m < 4; ++m) _Pragma("unroll") for (int n = 0; n < 2; ++n) Frag<F8>::mma(acc[ai][bj][m][n], Bt[n], At[m]); \
;         __builtin_amdgcn_s_setprio(0); } while (0)
; #define PG8_WAIT_V(n) asm volatile("s_waitcnt vmcnt(" #n ")" ::: "memory")
; #define PG8_WAIT_L(n) asm volatile("s_waitcnt lgkmcnt(" #n ")" ::: "memory")
; #define PG8_BAR __builtin_amdgcn_s_barrier()
; #define PG8_SCHED __builtin_amdgcn_sched_barrier(0)
; template <class Epi, class Sched, bool ALIGN_EPI = false, bool SP2 = false, bool F8 = false>
; __device__ __forceinline__ void gemm_phase(PG8_LAS unsigned char* lds, const Gemm g, const Sched& S, const Epi& E) {
;     ...
;             PG8_LDB(B1, 0, 1); PG8_STAGE(PG8_SB(0, 0), b2, voffB);
;             PG8_BAR; PG8_WAIT_L(0); PG8_MMA(0, 1, At, B1); PG8_BAR;
;             PG8_LDA(At, 0, 1); PG8_STAGE(PG8_SA(0, 0), a2, voffA);
;             PG8_BAR; PG8_WAIT_L(0); PG8_MMA(1, 0, At, B0); PG8_BAR; PG8_SCHED;
;             PG8_STAGE(PG8_SB(0, 1), b2 + hstep, voffB);
;             PG8_WAIT_V(6); PG8_BAR; PG8_MMA(1, 1, At, B1); PG8_BAR;
;             PG8_LDB(B0, 1, 0); PG8_SCHED; PG8_LDA(At, 1, 0); PG8_STAGE(PG8_SA(0, 1), a2 + hstep, voffA);
	s_mov_b64 s[8:9], 0x100
	s_mov_b32 m0, s42
	v_lshl_add_u64 v[68:69], v[154:155], 0, s[8:9]
	ds_read_b128 v[186:189], v163 offset:16384
	ds_read_b128 v[190:193], v163 offset:17408
	ds_read_b128 v[194:197], v163 offset:18432
	ds_read_b128 v[198:201], v163 offset:19456
	ds_read_b128 v[202:205], v163 offset:20480
	ds_read_b128 v[206:209], v163 offset:21504
	ds_read_b128 v[210:213], v163 offset:22528
	ds_read_b128 v[214:217], v163 offset:23552
	global_load_lds_dwordx4 v[68:69], off
	v_lshl_add_u64 v[68:69], v[156:157], 0, s[8:9]
	s_mov_b32 m0, s41
	s_nop 0
	global_load_lds_dwordx4 v[68:69], off
	v_lshl_add_u64 v[68:69], s[18:19], 0, v[158:159]
	s_mov_b32 m0, s44
	s_nop 0
	global_load_lds_dwordx4 v[68:69], off
	v_lshl_add_u64 v[68:69], s[18:19], 0, v[144:145]
	s_mov_b32 m0, s43
	s_nop 0
	global_load_lds_dwordx4 v[68:69], off
	v_lshl_add_u64 v[68:69], v[148:149], 0, s[8:9]
	s_mov_b32 m0, s4
	s_nop 0
	global_load_lds_dwordx4 v[68:69], off
	v_lshl_add_u64 v[68:69], v[146:147], 0, s[8:9]
	s_mov_b32 m0, s5
	s_nop 0
	global_load_lds_dwordx4 v[68:69], off
	s_waitcnt vmcnt(8)
	s_waitcnt lgkmcnt(0)
	s_barrier
	s_setprio 3
	v_mov_b64_e32 v[70:71], v[2:3]
	v_mov_b64_e32 v[86:87], v[2:3]
	v_mov_b64_e32 v[74:75], v[2:3]
	v_mov_b64_e32 v[90:91], v[2:3]
	v_mov_b64_e32 v[78:79], v[2:3]
	v_mov_b64_e32 v[94:95], v[2:3]
	v_mov_b64_e32 v[82:83], v[2:3]
	v_mov_b64_e32 v[68:69], v[0:1]
	v_mov_b64_e32 v[84:85], v[0:1]
	v_mov_b64_e32 v[72:73], v[0:1]
	v_mov_b64_e32 v[88:89], v[0:1]
	v_mov_b64_e32 v[76:77], v[0:1]
	v_mov_b64_e32 v[92:93], v[0:1]
	v_mov_b64_e32 v[80:81], v[0:1]
	s_waitcnt lgkmcnt(0)
	v_mfma_f32_16x16x128_f8f6f4 v[68:71], v[96:103], v[186:193], v[68:71]
	v_mfma_f32_16x16x128_f8f6f4 v[84:87], v[104:111], v[186:193], v[84:87]
	v_mfma_f32_16x16x128_f8f6f4 v[72:75], v[96:103], v[194:201], v[72:75]
	v_mfma_f32_16x16x128_f8f6f4 v[88:91], v[104:111], v[194:201], v[88:91]
	v_mfma_f32_16x16x128_f8f6f4 v[76:79], v[96:103], v[202:209], v[76:79]
	v_mfma_f32_16x16x128_f8f6f4 v[92:95], v[104:111], v[202:209], v[92:95]
	v_mfma_f32_16x16x128_f8f6f4 v[80:83], v[96:103], v[210:217], v[80:83]
	v_mov_b64_e32 v[98:99], v[2:3]
	v_mov_b64_e32 v[96:97], v[0:1]
	v_mfma_f32_16x16x128_f8f6f4 v[96:99], v[104:111], v[210:217], v[96:99]
	v_mov_b64_e32 v[118:119], v[2:3]
	v_mov_b64_e32 v[126:127], v[2:3]
	v_mov_b64_e32 v[110:111], v[2:3]
	v_mov_b64_e32 v[122:123], v[2:3]
	v_mov_b64_e32 v[106:107], v[2:3]
	v_mov_b64_e32 v[114:115], v[2:3]
	v_mov_b64_e32 v[102:103], v[2:3]
	v_mov_b64_e32 v[116:117], v[0:1]
	v_mov_b64_e32 v[124:125], v[0:1]
	v_mov_b64_e32 v[108:109], v[0:1]
	v_mov_b64_e32 v[120:121], v[0:1]
	v_mov_b64_e32 v[104:105], v[0:1]
	v_mov_b64_e32 v[112:113], v[0:1]
	v_mov_b64_e32 v[100:101], v[0:1]
	v_mfma_f32_16x16x128_f8f6f4 v[116:119], v[170:177], v[186:193], v[116:119]
	v_mfma_f32_16x16x128_f8f6f4 v[124:127], v[178:185], v[186:193], v[124:127]
	v_mfma_f32_16x16x128_f8f6f4 v[108:111], v[170:177], v[194:201], v[108:111]
	v_mfma_f32_16x16x128_f8f6f4 v[120:123], v[178:185], v[194:201], v[120:123]
	v_mfma_f32_16x16x128_f8f6f4 v[104:107], v[170:177], v[202:209], v[104:107]
	v_mfma_f32_16x16x128_f8f6f4 v[112:115], v[178:185], v[202:209], v[112:115]
	v_mfma_f32_16x16x128_f8f6f4 v[100:103], v[170:177], v[210:217], v[100:103]
	v_mfma_f32_16x16x128_f8f6f4 v[0:3], v[178:185], v[210:217], v[0:3]
	s_setprio 0
	s_barrier
	ds_read_b128 v[170:173], v166
	ds_read_b128 v[174:177], v166 offset:1024
	ds_read_b128 v[178:181], v166 offset:2048
	ds_read_b128 v[182:185], v166 offset:3072
	ds_read_b128 v[186:189], v165
	ds_read_b128 v[190:193], v165 offset:1024
	ds_read_b128 v[194:197], v165 offset:2048
	ds_read_b128 v[198:201], v165 offset:3072
	s_mov_b32 m0, s33
	v_lshl_add_u64 v[234:235], s[16:17], 0, v[158:159]
	ds_read_b128 v[202:205], v163 offset:32768
	ds_read_b128 v[206:209], v163 offset:33792
	ds_read_b128 v[210:213], v163 offset:34816
	ds_read_b128 v[214:217], v163 offset:35840
	ds_read_b128 v[218:221], v163 offset:36864
	ds_read_b128 v[222:225], v163 offset:37888
	ds_read_b128 v[226:229], v163 offset:38912
	ds_read_b128 v[230:233], v163 offset:39936
	global_load_lds_dwordx4 v[234:235], off
	v_lshl_add_u64 v[234:235], s[16:17], 0, v[144:145]
	s_mov_b32 m0, s40
	s_nop 0
	global_load_lds_dwordx4 v[234:235], off
	s_waitcnt vmcnt(8)
	s_waitcnt lgkmcnt(0)
	s_barrier
	s_setprio 3
	s_waitcnt lgkmcnt(0)
	v_mfma_f32_16x16x128_f8f6f4 v[28:31], v[170:177], v[202:209], v[28:31]
	v_mfma_f32_16x16x128_f8f6f4 v[32:35], v[178:185], v[202:209], v[32:35]
	v_mfma_f32_16x16x128_f8f6f4 v[20:23], v[170:177], v[210:217], v[20:23]
	v_mfma_f32_16x16x128_f8f6f4 v[24:27], v[178:185], v[210:217], v[24:27]
	v_mfma_f32_16x16x128_f8f6f4 v[12:15], v[170:177], v[218:225], v[12:15]
	v_mfma_f32_16x16x128_f8f6f4 v[16:19], v[178:185], v[218:225], v[16:19]
	v_mfma_f32_16x16x128_f8f6f4 v[4:7], v[170:177], v[226:233], v[4:7]
	v_mfma_f32_16x16x128_f8f6f4 v[8:11], v[178:185], v[226:233], v[8:11]
	v_mfma_f32_16x16x128_f8f6f4 v[60:63], v[186:193], v[202:209], v[60:63]
	v_mfma_f32_16x16x128_f8f6f4 v[64:67], v[194:201], v[202:209], v[64:67]
	v_mfma_f32_16x16x128_f8f6f4 v[52:55], v[186:193], v[210:217], v[52:55]
	v_mfma_f32_16x16x128_f8f6f4 v[56:59], v[194:201], v[210:217], v[56:59]
	v_mfma_f32_16x16x128_f8f6f4 v[44:47], v[186:193], v[218:225], v[44:47]
	v_mfma_f32_16x16x128_f8f6f4 v[48:51], v[194:201], v[218:225], v[48:51]
	v_mfma_f32_16x16x128_f8f6f4 v[36:39], v[186:193], v[226:233], v[36:39]
	v_mfma_f32_16x16x128_f8f6f4 v[40:43], v[194:201], v[226:233], v[40:43]
	s_setprio 0
	s_barrier
; #define PG8_STAGE(bufoff, gbase, voff) do { _Pragma("unroll") for (int _i = 0; _i < 2; ++_i) \
;         __builtin_amdgcn_global_load_lds((const unsigned*)((const char*)(gbase) + (voff)[_i]), (PG8_LAS unsigned*)(lds + (bufoff) + ldsw + _i * 8192), 16, 0, 0); } while (0)
; #define PG8_LDA(dst, b, h) do { _Pragma("unroll") for (int m = 0; m < 4; ++m) Frag<F8>::load(dst[m], lds + PG8_SA(b, h) + aoff + m * 2048); } while (0)
; #define PG8_LDB(dst, b, h) do { _Pragma("unroll") for (int n = 0; n < 2; ++n) Frag<F8>::load(dst[n], lds + PG8_SB(b, h) + boff + n * 2048); } while (0)
; #define PG8_MMA(ai, bj, At, Bt) do { __builtin_amdgcn_s_setprio(3); _Pragma("unroll") for (int m = 0; m < 4; ++m) _Pragma("unroll") for (int n = 0; n < 2; ++n) Frag<F8>::mma(acc[ai][bj][m][n], Bt[n], At[m]); \
;         __builtin_amdgcn_s_setprio(0); } while (0)
; #define PG8_WAIT_V(n) asm volatile("s_waitcnt vmcnt(" #n ")" ::: "memory")
; #define PG8_WAIT_L(n) asm volatile("s_waitcnt lgkmcnt(" #n ")" ::: "memory")
; #define PG8_BAR __builtin_amdgcn_s_barrier()
; #define PG8_SCHED __builtin_amdgcn_sched_barrier(0)
; template <class Epi, class Sched, bool ALIGN_EPI = false, bool SP2 = false, bool F8 = false>
; __device__ __forceinline__ void gemm_phase(PG8_LAS unsigned char* lds, const Gemm g, const Sched& S, const Epi& E) {
;     ...
;             PG8_WAIT_V(6); PG8_BAR; PG8_MMA(1, 1, At, B1); PG8_BAR;
;             PG8_LDB(B0, 1, 0); PG8_SCHED; PG8_LDA(At, 1, 0); PG8_STAGE(PG8_SA(0, 1), a2 + hstep, voffA);
;             PG8_WAIT_L(8); PG8_BAR; PG8_WAIT_L(0); PG8_MMA(0, 0, At, B0); PG8_BAR; PG8_SCHED;
;             PG8_LDB(B1, 1, 1); PG8_STAGE(PG8_SB(1, 0), b3, voffB);
;             PG8_BAR; PG8_WAIT_L(0); PG8_MMA(0, 1, At, B1); PG8_BAR;
;             PG8_LDA(At, 1, 1); PG8_STAGE(PG8_SA(1, 0), a3, voffA);
;             PG8_BAR; PG8_WAIT_L(0); PG8_MMA(1, 0, At, B0); PG8_BAR; PG8_SCHED;
;             PG8_STAGE(PG8_SB(1, 1), b3 + hstep, voffB);
	s_mov_b64 s[8:9], 0x180
	s_mov_b32 m0, s30
	v_lshl_add_u64 v[234:235], v[154:155], 0, s[8:9]
	ds_read_b128 v[202:205], v163 offset:49152
	ds_read_b128 v[206:209], v163 offset:50176
	ds_read_b128 v[210:213], v163 offset:51200
	ds_read_b128 v[214:217], v163 offset:52224
	ds_read_b128 v[218:221], v163 offset:53248
	ds_read_b128 v[222:225], v163 offset:54272
	ds_read_b128 v[226:229], v163 offset:55296
	ds_read_b128 v[230:233], v163 offset:56320
	global_load_lds_dwordx4 v[234:235], off
	v_lshl_add_u64 v[234:235], v[156:157], 0, s[8:9]
	s_mov_b32 m0, s36
	s_nop 0
	global_load_lds_dwordx4 v[234:235], off
	v_lshl_add_u64 v[234:235], s[14:15], 0, v[158:159]
	s_mov_b32 m0, s38
	s_nop 0
	global_load_lds_dwordx4 v[234:235], off
	v_lshl_add_u64 v[234:235], s[14:15], 0, v[144:145]
	s_mov_b32 m0, s39
	s_nop 0
	global_load_lds_dwordx4 v[234:235], off
	v_lshl_add_u64 v[234:235], v[148:149], 0, s[8:9]
	s_mov_b32 m0, s31
	s_nop 0
	global_load_lds_dwordx4 v[234:235], off
	v_lshl_add_u64 v[234:235], v[146:147], 0, s[8:9]
	s_mov_b32 m0, s37
	s_nop 0
	global_load_lds_dwordx4 v[234:235], off
	s_waitcnt vmcnt(8)
	s_waitcnt lgkmcnt(0)
	s_barrier
	s_setprio 3
	s_waitcnt lgkmcnt(0)
	v_mfma_f32_16x16x128_f8f6f4 v[68:71], v[170:177], v[202:209], v[68:71]
	v_mfma_f32_16x16x128_f8f6f4 v[84:87], v[178:185], v[202:209], v[84:87]
	v_mfma_f32_16x16x128_f8f6f4 v[72:75], v[170:177], v[210:217], v[72:75]
	v_mfma_f32_16x16x128_f8f6f4 v[88:91], v[178:185], v[210:217], v[88:91]
	v_mfma_f32_16x16x128_f8f6f4 v[76:79], v[170:177], v[218:225], v[76:79]
	v_mfma_f32_16x16x128_f8f6f4 v[92:95], v[178:185], v[218:225], v[92:95]
	v_mfma_f32_16x16x128_f8f6f4 v[80:83], v[170:177], v[226:233], v[80:83]
	v_mfma_f32_16x16x128_f8f6f4 v[96:99], v[178:185], v[226:233], v[96:99]
	v_mfma_f32_16x16x128_f8f6f4 v[116:119], v[186:193], v[202:209], v[116:119]
	v_mfma_f32_16x16x128_f8f6f4 v[124:127], v[194:201], v[202:209], v[124:127]
	v_mfma_f32_16x16x128_f8f6f4 v[108:111], v[186:193], v[210:217], v[108:111]
	v_mfma_f32_16x16x128_f8f6f4 v[120:123], v[194:201], v[210:217], v[120:123]
	v_mfma_f32_16x16x128_f8f6f4 v[104:107], v[186:193], v[218:225], v[104:107]
	v_mfma_f32_16x16x128_f8f6f4 v[112:115], v[194:201], v[218:225], v[112:115]
	v_mfma_f32_16x16x128_f8f6f4 v[100:103], v[186:193], v[226:233], v[100:103]
	v_mfma_f32_16x16x128_f8f6f4 v[0:3], v[194:201], v[226:233], v[0:3]
	s_setprio 0
	s_barrier
	ds_read_b128 v[170:173], v168
	ds_read_b128 v[174:177], v168 offset:1024
	ds_read_b128 v[178:181], v168 offset:2048
	ds_read_b128 v[182:185], v168 offset:3072
	ds_read_b128 v[186:189], v167
	ds_read_b128 v[190:193], v167 offset:1024
	ds_read_b128 v[194:197], v167 offset:2048
	ds_read_b128 v[198:201], v167 offset:3072
	s_mov_b32 m0, s46
	v_lshl_add_u64 v[158:159], s[6:7], 0, v[158:159]
	ds_read_b128 v[202:205], v163
	ds_read_b128 v[206:209], v163 offset:1024
	ds_read_b128 v[210:213], v163 offset:2048
	ds_read_b128 v[214:217], v163 offset:3072
	ds_read_b128 v[218:221], v163 offset:4096
	ds_read_b128 v[222:225], v163 offset:5120
	ds_read_b128 v[226:229], v163 offset:6144
	ds_read_b128 v[230:233], v163 offset:7168
	global_load_lds_dwordx4 v[158:159], off
	v_lshl_add_u64 v[144:145], s[6:7], 0, v[144:145]
	s_mov_b32 m0, s45
	s_nop 0
	global_load_lds_dwordx4 v[144:145], off
	s_waitcnt vmcnt(8)
	s_waitcnt lgkmcnt(0)
	s_barrier
	s_setprio 3
	s_waitcnt lgkmcnt(0)
	v_mfma_f32_16x16x128_f8f6f4 v[28:31], v[170:177], v[202:209], v[28:31]
	v_mfma_f32_16x16x128_f8f6f4 v[32:35], v[178:185], v[202:209], v[32:35]
	v_mfma_f32_16x16x128_f8f6f4 v[20:23], v[170:177], v[210:217], v[20:23]
	v_mfma_f32_16x16x128_f8f6f4 v[24:27], v[178:185], v[210:217], v[24:27]
	v_mfma_f32_16x16x128_f8f6f4 v[12:15], v[170:177], v[218:225], v[12:15]
	v_mfma_f32_16x16x128_f8f6f4 v[16:19], v[178:185], v[218:225], v[16:19]
	v_mfma_f32_16x16x128_f8f6f4 v[4:7], v[170:177], v[226:233], v[4:7]
	v_mfma_f32_16x16x128_f8f6f4 v[8:11], v[178:185], v[226:233], v[8:11]
	v_mfma_f32_16x16x128_f8f6f4 v[60:63], v[186:193], v[202:209], v[60:63]
	v_mfma_f32_16x16x128_f8f6f4 v[64:67], v[194:201], v[202:209], v[64:67]
	v_mfma_f32_16x16x128_f8f6f4 v[52:55], v[186:193], v[210:217], v[52:55]
	v_mfma_f32_16x16x128_f8f6f4 v[56:59], v[194:201], v[210:217], v[56:59]
	v_mfma_f32_16x16x128_f8f6f4 v[44:47], v[186:193], v[218:225], v[44:47]
	v_mfma_f32_16x16x128_f8f6f4 v[48:51], v[194:201], v[218:225], v[48:51]
	v_mfma_f32_16x16x128_f8f6f4 v[36:39], v[186:193], v[226:233], v[36:39]
	v_mfma_f32_16x16x128_f8f6f4 v[40:43], v[194:201], v[226:233], v[40:43]
	s_setprio 0
	s_barrier
	s_mov_b32 m0, s42
	ds_read_b128 v[202:205], v163 offset:16384
	ds_read_b128 v[206:209], v163 offset:17408
	ds_read_b128 v[210:213], v163 offset:18432
	ds_read_b128 v[214:217], v163 offset:19456
	ds_read_b128 v[218:221], v163 offset:20480
	ds_read_b128 v[222:225], v163 offset:21504
	ds_read_b128 v[226:229], v163 offset:22528
	ds_read_b128 v[230:233], v163 offset:23552
	global_load_lds_dwordx4 v[154:155], off
	s_mov_b32 m0, s41
	s_nop 0
	global_load_lds_dwordx4 v[156:157], off
	s_mov_b32 m0, s44
	s_nop 0
	global_load_lds_dwordx4 v[152:153], off
	s_mov_b32 m0, s43
	s_nop 0
	global_load_lds_dwordx4 v[150:151], off
	s_mov_b32 m0, s4
	s_nop 0
	global_load_lds_dwordx4 v[148:149], off
	s_mov_b32 m0, s5
	s_nop 0
	global_load_lds_dwordx4 v[146:147], off
	s_waitcnt vmcnt(8)
	s_waitcnt lgkmcnt(0)
	s_barrier
; #define PG8_STAGE(bufoff, gbase, voff) do { _Pragma("unroll") for (int _i = 0; _i < 2; ++_i) \
;         __builtin_amdgcn_global_load_lds((const unsigned*)((const char*)(gbase) + (voff)[_i]), (PG8_LAS unsigned*)(lds + (bufoff) + ldsw + _i * 8192), 16, 0, 0); } while (0)
; #define PG8_LDA(dst, b, h) do { _Pragma("unroll") for (int m = 0; m < 4; ++m) Frag<F8>::load(dst[m], lds + PG8_SA(b, h) + aoff + m * 2048); } while (0)
; #define PG8_MMA(ai, bj, At, Bt) do { __builtin_amdgcn_s_setprio(3); _Pragma("unroll") for (int m = 0; m < 4; ++m) _Pragma("unroll") for (int n = 0; n < 2; ++n) Frag<F8>::mma(acc[ai][bj][m][n], Bt[n], At[m]); \
;         __builtin_amdgcn_s_setprio(0); } while (0)
; #define PG8_WAIT_V(n) asm volatile("s_waitcnt vmcnt(" #n ")" ::: "memory")
; #define PG8_WAIT_L(n) asm volatile("s_waitcnt lgkmcnt(" #n ")" ::: "memory")
; #define PG8_BAR __builtin_amdgcn_s_barrier()
; #define PG8_SCHED __builtin_amdgcn_sched_barrier(0)
; template <class Epi, class Sched, bool ALIGN_EPI = false, bool SP2 = false, bool F8 = false>
; __device__ __forceinline__ void gemm_phase(PG8_LAS unsigned char* lds, const Gemm g, const Sched& S, const Epi& E) {
;     ...
;             PG8_LDA(At, 1, 1); PG8_STAGE(PG8_SA(1, 0), a3, voffA);
;             PG8_BAR; PG8_WAIT_L(0); PG8_MMA(1, 0, At, B0); PG8_BAR; PG8_SCHED;
;             PG8_STAGE(PG8_SB(1, 1), b3 + hstep, voffB);
;             PG8_WAIT_V(6); PG8_BAR; PG8_MMA(1, 1, At, B1); PG8_BAR;
;             }
;         }
;         if constexpr (ALIGN_EPI) { if (wr == 0) PG8_BAR; }
	s_setprio 3
	s_waitcnt lgkmcnt(0)
	v_mfma_f32_16x16x128_f8f6f4 v[68:71], v[170:177], v[202:209], v[68:71]
	v_mfma_f32_16x16x128_f8f6f4 v[84:87], v[178:185], v[202:209], v[84:87]
	v_mfma_f32_16x16x128_f8f6f4 v[72:75], v[170:177], v[210:217], v[72:75]
	v_mfma_f32_16x16x128_f8f6f4 v[88:91], v[178:185], v[210:217], v[88:91]
	v_mfma_f32_16x16x128_f8f6f4 v[76:79], v[170:177], v[218:225], v[76:79]
	v_mfma_f32_16x16x128_f8f6f4 v[92:95], v[178:185], v[218:225], v[92:95]
	v_mfma_f32_16x16x128_f8f6f4 v[80:83], v[170:177], v[226:233], v[80:83]
	v_mfma_f32_16x16x128_f8f6f4 v[96:99], v[178:185], v[226:233], v[96:99]
	v_mfma_f32_16x16x128_f8f6f4 v[116:119], v[186:193], v[202:209], v[116:119]
	v_mfma_f32_16x16x128_f8f6f4 v[124:127], v[194:201], v[202:209], v[124:127]
	v_mfma_f32_16x16x128_f8f6f4 v[108:111], v[186:193], v[210:217], v[108:111]
	v_mfma_f32_16x16x128_f8f6f4 v[120:123], v[194:201], v[210:217], v[120:123]
	v_mfma_f32_16x16x128_f8f6f4 v[104:107], v[186:193], v[218:225], v[104:107]
	v_mfma_f32_16x16x128_f8f6f4 v[112:115], v[194:201], v[218:225], v[112:115]
	v_mfma_f32_16x16x128_f8f6f4 v[100:103], v[186:193], v[226:233], v[100:103]
	v_mfma_f32_16x16x128_f8f6f4 v[0:3], v[194:201], v[226:233], v[0:3]
	s_setprio 0
	s_barrier
	ds_read_b128 v[144:147], v166
	ds_read_b128 v[148:151], v166 offset:1024
	ds_read_b128 v[152:155], v166 offset:2048
	ds_read_b128 v[156:159], v166 offset:3072
	ds_read_b128 v[166:169], v165
	ds_read_b128 v[170:173], v165 offset:1024
	ds_read_b128 v[174:177], v165 offset:2048
	ds_read_b128 v[178:181], v165 offset:3072
	s_mov_b32 m0, s33
	ds_read_b128 v[182:185], v163 offset:32768
	ds_read_b128 v[186:189], v163 offset:33792
	ds_read_b128 v[190:193], v163 offset:34816
	ds_read_b128 v[194:197], v163 offset:35840
	ds_read_b128 v[198:201], v163 offset:36864
	ds_read_b128 v[202:205], v163 offset:37888
	ds_read_b128 v[206:209], v163 offset:38912
	ds_read_b128 v[210:213], v163 offset:39936
	global_load_lds_dwordx4 v[140:141], off
	s_mov_b32 m0, s40
	s_nop 0
	global_load_lds_dwordx4 v[142:143], off
	s_waitcnt vmcnt(8)
	s_waitcnt lgkmcnt(0)
	s_barrier
	s_setprio 3
	s_waitcnt lgkmcnt(0)
	v_mfma_f32_16x16x128_f8f6f4 v[28:31], v[144:151], v[182:189], v[28:31]
	v_mfma_f32_16x16x128_f8f6f4 v[32:35], v[152:159], v[182:189], v[32:35]
	v_mfma_f32_16x16x128_f8f6f4 v[20:23], v[144:151], v[190:197], v[20:23]
	v_mfma_f32_16x16x128_f8f6f4 v[24:27], v[152:159], v[190:197], v[24:27]
	v_mfma_f32_16x16x128_f8f6f4 v[12:15], v[144:151], v[198:205], v[12:15]
	v_mfma_f32_16x16x128_f8f6f4 v[16:19], v[152:159], v[198:205], v[16:19]
	v_mfma_f32_16x16x128_f8f6f4 v[4:7], v[144:151], v[206:213], v[4:7]
	v_mfma_f32_16x16x128_f8f6f4 v[8:11], v[152:159], v[206:213], v[8:11]
	v_mfma_f32_16x16x128_f8f6f4 v[60:63], v[166:173], v[182:189], v[60:63]
	v_mfma_f32_16x16x128_f8f6f4 v[64:67], v[174:181], v[182:189], v[64:67]
	v_mfma_f32_16x16x128_f8f6f4 v[52:55], v[166:173], v[190:197], v[52:55]
	v_mfma_f32_16x16x128_f8f6f4 v[56:59], v[174:181], v[190:197], v[56:59]
	v_mfma_f32_16x16x128_f8f6f4 v[44:47], v[166:173], v[198:205], v[44:47]
	v_mfma_f32_16x16x128_f8f6f4 v[48:51], v[174:181], v[198:205], v[48:51]
	v_mfma_f32_16x16x128_f8f6f4 v[36:39], v[166:173], v[206:213], v[36:39]
	v_mfma_f32_16x16x128_f8f6f4 v[40:43], v[174:181], v[206:213], v[40:43]
	s_setprio 0
	s_barrier
	s_mov_b32 m0, s30
	ds_read_b128 v[182:185], v163 offset:49152
	ds_read_b128 v[186:189], v163 offset:50176
	ds_read_b128 v[190:193], v163 offset:51200
	ds_read_b128 v[194:197], v163 offset:52224
	ds_read_b128 v[198:201], v163 offset:53248
	ds_read_b128 v[202:205], v163 offset:54272
	ds_read_b128 v[206:209], v163 offset:55296
	ds_read_b128 v[210:213], v163 offset:56320
	global_load_lds_dwordx4 v[130:131], off
	s_mov_b32 m0, s36
	s_nop 0
	global_load_lds_dwordx4 v[132:133], off
	s_mov_b32 m0, s38
	s_nop 0
	global_load_lds_dwordx4 v[136:137], off
	s_mov_b32 m0, s39
	s_nop 0
	global_load_lds_dwordx4 v[138:139], off
	s_mov_b32 m0, s31
	s_nop 0
	global_load_lds_dwordx4 v[128:129], off
	s_mov_b32 m0, s37
	s_nop 0
	global_load_lds_dwordx4 v[134:135], off
	s_waitcnt vmcnt(8)
	s_waitcnt lgkmcnt(0)
	s_barrier
	s_setprio 3
	s_waitcnt lgkmcnt(0)
	v_mfma_f32_16x16x128_f8f6f4 v[68:71], v[144:151], v[182:189], v[68:71]
	v_mfma_f32_16x16x128_f8f6f4 v[84:87], v[152:159], v[182:189], v[84:87]
	v_mfma_f32_16x16x128_f8f6f4 v[72:75], v[144:151], v[190:197], v[72:75]
	v_mfma_f32_16x16x128_f8f6f4 v[88:91], v[152:159], v[190:197], v[88:91]
	v_mfma_f32_16x16x128_f8f6f4 v[76:79], v[144:151], v[198:205], v[76:79]
	v_mfma_f32_16x16x128_f8f6f4 v[92:95], v[152:159], v[198:205], v[92:95]
	v_mfma_f32_16x16x128_f8f6f4 v[80:83], v[144:151], v[206:213], v[80:83]
	v_mfma_f32_16x16x128_f8f6f4 v[96:99], v[152:159], v[206:213], v[96:99]
	v_mfma_f32_16x16x128_f8f6f4 v[116:119], v[166:173], v[182:189], v[116:119]
	v_mfma_f32_16x16x128_f8f6f4 v[124:127], v[174:181], v[182:189], v[124:127]
	v_mfma_f32_16x16x128_f8f6f4 v[108:111], v[166:173], v[190:197], v[108:111]
	v_mfma_f32_16x16x128_f8f6f4 v[120:123], v[174:181], v[190:197], v[120:123]
	v_mfma_f32_16x16x128_f8f6f4 v[104:107], v[166:173], v[198:205], v[104:107]
	v_mfma_f32_16x16x128_f8f6f4 v[112:115], v[174:181], v[198:205], v[112:115]
	v_mfma_f32_16x16x128_f8f6f4 v[100:103], v[166:173], v[206:213], v[100:103]
	v_mfma_f32_16x16x128_f8f6f4 v[0:3], v[174:181], v[206:213], v[0:3]
	s_setprio 0
	s_barrier
	s_cbranch_scc1 .LBB0_1420
	s_barrier
